# GLA chunk loop: counted vmcnt waits keep the two-chunk-ahead tile prefetch in flight; tile prefetch unconditional
# baseline (speedup 1.0000x reference)
; #define LAS __attribute__((address_space(3)))
; #define GLA_LOAD_DR(n) do { if (tid < 32) dr = *(const f32x4*)(BC + ((size_t)b * SEQ + 64 * (n) + 63) * 512 + h * 128 + tid * 4); } while (0)
; __device__ __forceinline__ void gla_unit(LAS unsigned char* lds, const unsigned char* ws, const float* g_onorm, const int b, const int h, const int wv) {
;     ...
;     u32x4 qr[2][2], kr[2][2], vr[2][4], ogr[4]; f32x4 dr = (f32x4){0.f, 0.f, 0.f, 0.f};
;     const unsigned o16 = (unsigned)tid * 16u, oog = (unsigned)tid * 64u;
;     ...
;     const LAS unsigned char* qb8 = lds + L_Q + j * QS + hh * 8;  const LAS unsigned char* qb16 = lds + L_Q + j * QS + hh * 16;
;     const LAS unsigned char* kb16 = lds + L_K + j * QS + hh * 16;
;     const int li = lane & 15, gq = li >> 2, gp = li & 3, gg = (lane >> 4) & 1;
;     const LAS unsigned char* keN = lds + L_KE + (gq + 8 * hh) * ES + (16 * gg + 4 * gp) * 2;
;     const LAS unsigned char* vN = lds + L_V + (gq + 8 * hh) * VS + (32 * w + 16 * gg + 4 * gp) * 2;
;     const LAS unsigned char* vP = lds + L_V + (gq + 4 * hh) * VS + (32 * w + 16 * gg + 4 * gp) * 2;
;     const LAS float* decb = dec + 4 * hh; LAS float* ob = obuf + 4 * hh * OS + 32 * w + j;
;     LAS unsigned char* frb = lds + L_FR + lane * 16;
;     ...
;     GLA_LOAD(0, 0); GLA_LOAD_DR(0); GLA_LOAD(1, 1);
.LBB0_633:
	s_or_b64 exec, exec, s[4:5]
	v_and_b32_e32 v12, 16, v2
	v_and_or_b32 v12, v4, 12, v12
	v_bfe_u32 v1, v2, 5, 1
	s_ashr_i32 s17, s10, 6
	v_and_b32_e32 v3, 31, v2
	s_movk_i32 s18, 0x110
	v_lshlrev_b32_e32 v14, 1, v12
	s_and_b32 s4, s10, 0xffffffc0
	v_lshlrev_b32_e32 v10, 4, v1
	v_mad_u32_u24 v203, v3, s18, 0
	v_or_b32_e32 v15, s4, v14
	s_lshl_b32 s4, s17, 7
	s_add_i32 s5, 0, 0x1fc00
	v_and_b32_e32 v0, 63, v2
	v_lshlrev_b32_e32 v202, 3, v1
	v_lshlrev_b32_e32 v16, 2, v1
	v_mul_u32_u24_e32 v1, 0x1040, v1
	s_add_i32 s4, s4, 0
	v_add_u32_e32 v204, v203, v10
	v_add_u32_e32 v205, s5, v10
	s_add_i32 s5, 0, 0x1e400
	v_lshlrev_b32_e32 v10, 2, v3
	v_lshl_add_u32 v206, v0, 4, s5
	v_add3_u32 v207, s4, v1, v10
	s_lshl_b64 s[4:5], s[94:95], 11
	s_or_b32 s4, s4, 64
	s_add_i32 s19, 0, 0x15400
	s_add_i32 s21, 0, 0x10400
	s_lshl_b64 s[6:7], s[4:5], 8
	s_add_u32 s8, s15, s6
	v_bfe_u32 v11, v2, 2, 2
	s_addc_u32 s9, s16, s7
	v_or_b32_e32 v13, v202, v11
	v_or_b32_e32 v11, v16, v11
	s_movk_i32 s20, 0x240
	v_mov_b32_e32 v12, s19
	s_add_u32 s6, s13, s6
	v_mad_u32_u24 v17, v11, s20, v12
	s_movk_i32 s22, 0x140
	v_mov_b32_e32 v11, s21
	s_addc_u32 s7, s14, s7
	v_mad_u32_u24 v18, v13, s22, v11
	v_mad_u32_u24 v19, v13, s20, v12
	v_lshl_add_u64 v[10:11], s[8:9], 0, v[180:181]
	v_lshl_add_u64 v[12:13], s[6:7], 0, v[180:181]
	s_movk_i32 s6, 0x2000
	s_lshl_b64 s[4:5], s[4:5], 9
	global_load_dwordx4 v[132:135], v[10:11], off
	global_load_dwordx4 v[136:139], v[12:13], off
	v_add_co_u32_e32 v10, vcc, s6, v10
	s_add_u32 s4, s11, s4
	s_nop 0
	v_addc_co_u32_e32 v11, vcc, 0, v11, vcc
	v_add_co_u32_e32 v12, vcc, s6, v12
	s_addc_u32 s5, s12, s5
	s_nop 0
	v_addc_co_u32_e32 v13, vcc, 0, v13, vcc
	global_load_dwordx4 v[140:143], v[10:11], off
	global_load_dwordx4 v[144:147], v[12:13], off
	v_lshl_add_u64 v[10:11], s[4:5], 0, v[180:181]
	v_add_co_u32_e32 v12, vcc, s6, v10
	s_movk_i32 s4, 0x4000
	s_nop 0
	v_addc_co_u32_e32 v13, vcc, 0, v11, vcc
	global_load_dwordx4 v[148:151], v[10:11], off
	global_load_dwordx4 v[152:155], v[12:13], off
	v_add_co_u32_e32 v12, vcc, s4, v10
	s_movk_i32 s4, 0x6000
	s_nop 0
	v_addc_co_u32_e32 v13, vcc, 0, v11, vcc
	v_add_co_u32_e32 v10, vcc, s4, v10
	s_cmp_lt_i32 s17, 3
	s_nop 0
	v_addc_co_u32_e32 v11, vcc, 0, v11, vcc
	global_load_dwordx4 v[156:159], v[12:13], off
	global_load_dwordx4 v[160:163], v[10:11], off
	v_and_b32_e32 v10, 15, v2
	v_lshlrev_b32_e32 v20, 5, v10
	v_lshl_add_u32 v21, v10, 4, s21
	v_ashrrev_i32_e32 v10, 3, v2
	s_movk_i32 s4, 0x410
	s_cselect_b64 s[54:55], -1, 0
	v_and_b32_e32 v22, 7, v2
	v_mul_lo_u32 v11, v10, s4
	s_add_i32 s4, 0, 0x1fe00
	v_lshlrev_b32_e32 v24, 7, v22
	s_cmp_eq_u32 s17, 2
	v_add_u32_e32 v208, s4, v24
	s_cselect_b64 s[4:5], -1, 0
	s_and_b64 s[6:7], s[4:5], exec
	v_lshlrev_b32_e32 v0, 6, v2
	s_cselect_b32 s61, 0x2200, 0
	s_cmp_gt_u32 s10, 63
	v_ashrrev_i32_e32 v25, 4, v2
	v_add_u32_e32 v27, 0x200, v2
	v_lshrrev_b32_e32 v30, 5, v2
	v_add_u32_e32 v31, 0x400, v2
	v_add_u32_e32 v2, 0x600, v2
	s_cselect_b64 s[6:7], -1, 0
	v_lshrrev_b32_e32 v2, 5, v2
	s_and_b64 s[8:9], s[6:7], exec
	v_mul_lo_u32 v32, v2, s20
	v_or_b32_e32 v2, 2, v16
	v_cmp_gt_u32_e64 s[8:9], v2, v3
	v_or_b32_e32 v2, 3, v16
	v_cmp_gt_u32_e64 s[10:11], v2, v3
	v_or_b32_e32 v2, 8, v16
	v_cmp_gt_u32_e64 s[12:13], v2, v3
	v_or_b32_e32 v2, 9, v16
	v_and_b32_e32 v1, 0xf0, v180
	v_cmp_gt_u32_e64 s[14:15], v2, v3
	v_or_b32_e32 v2, 10, v16
	v_add_u32_e32 v12, 0, v1
	v_and_b32_e32 v1, 0x1f0, v180
	s_cselect_b32 s64, 0x2200, 0
	s_lshl_b32 s65, s17, 11
	v_ashrrev_i32_e32 v28, 4, v27
; #define LAS __attribute__((address_space(3)))
; #define GLA_LOAD_DR(n) do { if (tid < 32) dr = *(const f32x4*)(BC + ((size_t)b * SEQ + 64 * (n) + 63) * 512 + h * 128 + tid * 4); } while (0)
; __device__ __forceinline__ void gla_unit(LAS unsigned char* lds, const unsigned char* ws, const float* g_onorm, const int b, const int h, const int wv) {
;     ...
;     f32x16 S[4];
; #pragma unroll
;     for (int et = 0; et < 4; ++et)
; #pragma unroll
;         for (int r = 0; r < 16; ++r) S[et][r] = 0.f;
;     __syncthreads();
;     if (tid < 256) gon[tid] = g_onorm[tid];
;     u32x4 qr[2][2], kr[2][2], vr[2][4], ogr[4]; f32x4 dr = (f32x4){0.f, 0.f, 0.f, 0.f};
;     const unsigned o16 = (unsigned)tid * 16u, oog = (unsigned)tid * 64u;
;     ...
;     const LAS unsigned char* qb8 = lds + L_Q + j * QS + hh * 8;  const LAS unsigned char* qb16 = lds + L_Q + j * QS + hh * 16;
;     const LAS unsigned char* kb16 = lds + L_K + j * QS + hh * 16;
;     const int li = lane & 15, gq = li >> 2, gp = li & 3, gg = (lane >> 4) & 1;
;     const LAS unsigned char* keN = lds + L_KE + (gq + 8 * hh) * ES + (16 * gg + 4 * gp) * 2;
;     const LAS unsigned char* vN = lds + L_V + (gq + 8 * hh) * VS + (32 * w + 16 * gg + 4 * gp) * 2;
;     const LAS unsigned char* vP = lds + L_V + (gq + 4 * hh) * VS + (32 * w + 16 * gg + 4 * gp) * 2;
;     const LAS float* decb = dec + 4 * hh; LAS float* ob = obuf + 4 * hh * OS + 32 * w + j;
;     LAS unsigned char* frb = lds + L_FR + lane * 16;
;     ...
;     GLA_LOAD(0, 0); GLA_LOAD_DR(0); GLA_LOAD(1, 1);
	v_cmp_gt_u32_e64 s[16:17], v2, v3
	v_or_b32_e32 v2, 11, v16
	v_add_u32_e32 v13, s19, v1
	v_mul_lo_u32 v26, v25, s18
	v_mul_lo_u32 v29, v28, s18
	v_lshrrev_b32_e32 v27, 5, v27
	v_lshrrev_b32_e32 v31, 5, v31
	v_cmp_gt_u32_e64 s[18:19], v2, v3
	v_or_b32_e32 v2, 16, v16
	v_mul_lo_u32 v30, v30, s20
	v_mul_lo_u32 v27, v27, s20
	v_mul_lo_u32 v31, v31, s20
	v_cmp_gt_u32_e64 s[20:21], v2, v3
	v_or_b32_e32 v2, 17, v16
	v_mul_lo_u32 v25, v25, s22
	v_mul_lo_u32 v28, v28, s22
	v_cmp_gt_u32_e64 s[22:23], v2, v3
	v_or_b32_e32 v2, 18, v16
	v_cmp_gt_u32_e64 s[24:25], v2, v3
	v_or_b32_e32 v2, 19, v16
	v_cmp_gt_u32_e64 s[26:27], v2, v3
	v_or_b32_e32 v2, 24, v16
	v_cmp_gt_u32_e64 s[28:29], v2, v3
	v_or_b32_e32 v2, 25, v16
	v_cmp_gt_u32_e64 s[30:31], v2, v3
	v_or_b32_e32 v2, 26, v16
	s_xor_b64 s[4:5], s[6:7], s[4:5]
	v_cmp_gt_u32_e64 s[34:35], v2, v3
	v_or_b32_e32 v2, 27, v16
	v_add_u32_e32 v23, 0, v11
	v_ashrrev_i32_e32 v11, 31, v10
	s_xor_b64 s[62:63], s[4:5], -1
	v_cmp_gt_u32_e64 s[4:5], v16, v3
	v_cmp_lt_u32_e64 s[6:7], v16, v3
	v_cmp_gt_u32_e64 s[36:37], v2, v3
	v_lshl_add_u64 v[2:3], v[8:9], 2, v[6:7]
	v_mov_b32_e32 v1, 0
	v_lshl_add_u64 v[182:183], v[4:5], 2, v[2:3]
	s_lshl_b64 s[2:3], s[2:3], 23
	v_lshlrev_b64 v[2:3], 12, v[10:11]
	v_lshl_add_u64 v[188:189], s[2:3], 0, v[2:3]
	s_lshl_b32 s2, s33, 9
	v_lshlrev_b32_e32 v2, 6, v22
	v_lshl_add_u64 v[190:191], s[38:39], 0, v[0:1]
	v_add_u32_e32 v0, 0, v20
	s_mov_b32 s60, 1
	v_lshl_add_u64 v[184:185], s[38:39], 0, v[180:181]
	v_lshl_add_u64 v[186:187], s[40:41], 0, v[180:181]
	v_or3_b32 v188, v188, s2, v2
	v_mov_b32_e32 v181, 0x358637bd
	s_mov_b64 s[68:69], 0x10000
	s_mov_b64 s[70:71], 0x80000
	v_add_u32_e32 v209, v12, v26
	v_add_u32_e32 v210, v12, v29
	v_add_u32_e32 v211, v13, v30
	v_add_u32_e32 v212, v13, v27
	v_add_u32_e32 v213, v13, v31
	v_add_u32_e32 v214, v13, v32
	v_add_u32_e32 v215, 0x1fc00, v0
	v_add_u32_e32 v216, v21, v25
	v_add_u32_e32 v217, v21, v28
	v_add_u32_e32 v218, v17, v15
	v_add_u32_e32 v219, v19, v15
	v_add_u32_e32 v220, v18, v14
	v_add_u32_e32 v221, v23, v24
	v_mov_b32_e32 v0, v1
	v_mov_b32_e32 v2, v1
	v_mov_b32_e32 v3, v1
	v_mov_b32_e32 v4, v1
	v_mov_b32_e32 v5, v1
	v_mov_b32_e32 v6, v1
	v_mov_b32_e32 v7, v1
	v_mov_b32_e32 v8, v1
	v_mov_b32_e32 v9, v1
	v_mov_b32_e32 v10, v1
	v_mov_b32_e32 v11, v1
	v_mov_b32_e32 v12, v1
	v_mov_b32_e32 v13, v1
	v_mov_b32_e32 v14, v1
	v_mov_b32_e32 v15, v1
	v_mov_b32_e32 v48, v1
	v_mov_b32_e32 v49, v1
	v_mov_b32_e32 v50, v1
	v_mov_b32_e32 v51, v1
	v_mov_b32_e32 v52, v1
	v_mov_b32_e32 v53, v1
	v_mov_b32_e32 v54, v1
	v_mov_b32_e32 v55, v1
	v_mov_b32_e32 v56, v1
	v_mov_b32_e32 v57, v1
	v_mov_b32_e32 v58, v1
	v_mov_b32_e32 v59, v1
	v_mov_b32_e32 v60, v1
	v_mov_b32_e32 v61, v1
	v_mov_b32_e32 v62, v1
	v_mov_b32_e32 v63, v1
	v_mov_b32_e32 v16, v1
	v_mov_b32_e32 v17, v1
	v_mov_b32_e32 v18, v1
	v_mov_b32_e32 v19, v1
	v_mov_b32_e32 v20, v1
	v_mov_b32_e32 v21, v1
	v_mov_b32_e32 v22, v1
	v_mov_b32_e32 v23, v1
	v_mov_b32_e32 v24, v1
	v_mov_b32_e32 v25, v1
	v_mov_b32_e32 v26, v1
	v_mov_b32_e32 v27, v1
	v_mov_b32_e32 v28, v1
	v_mov_b32_e32 v29, v1
	v_mov_b32_e32 v30, v1
	v_mov_b32_e32 v31, v1
	v_mov_b32_e32 v32, v1
	v_mov_b32_e32 v33, v1
	v_mov_b32_e32 v34, v1
	v_mov_b32_e32 v35, v1
	v_mov_b32_e32 v36, v1
	v_mov_b32_e32 v37, v1
	v_mov_b32_e32 v38, v1
	v_mov_b32_e32 v39, v1
	v_mov_b32_e32 v40, v1
	v_mov_b32_e32 v41, v1
	v_mov_b32_e32 v42, v1
	v_mov_b32_e32 v43, v1
	v_mov_b32_e32 v44, v1
	v_mov_b32_e32 v45, v1
	v_mov_b32_e32 v46, v1
	v_mov_b32_e32 v47, v1
	s_mov_b32 s33, 0x4e188000
	s_waitcnt vmcnt(0)
	s_branch .LBB0_636

; #define LAS __attribute__((address_space(3)))
; __device__ __forceinline__ void gla_unit(LAS unsigned char* lds, const unsigned char* ws, const float* g_onorm, const int b, const int h, const int wv) {
;     ...
;         f32x16 O[2];
; #pragma unroll
;         for (int tt = 0; tt < 2; ++tt)
; #pragma unroll
;             for (int r = 0; r < 16; ++r) O[tt][r] = 0.f;
; #pragma unroll
;         for (int et = 0; et < 4; ++et)
; #pragma unroll
;             for (int s2 = 0; s2 < 2; ++s2) {
;                 const bf16x8 sb = pack8(S[et], s2);
; #pragma unroll
;                 for (int tt = 0; tt < 2; ++tt) {
;                     const bf16x8 aq = ld2x64(qb8 + 32 * tt * QS + (32 * et + 16 * s2) * 2);
;                     O[tt] = __builtin_amdgcn_mfma_f32_32x32x16_bf16(aq, sb, O[tt], 0, 0, 0);
;                 }
;             }
;         __syncthreads();
; #pragma unroll
;         for (int pr = 0; pr < 3; ++pr) {
;             const int st = (pr == 2) ? 1 : 0, tt = (pr == 0) ? 0 : 1;
; #pragma unroll
;             for (int s2 = 0; s2 < 2; ++s2) {
;                 const bf16x8 ax = *(const LAS bf16x8*)(frb + (pr * 2 + s2) * 1024);
;                 const LAS unsigned char* vp = vP + (32 * st + 16 * s2) * VS;
;                 const bf16x8 bv = tr8(vp, vp + 8 * VS);
;                 O[tt] = __builtin_amdgcn_mfma_f32_32x32x16_bf16(ax, bv, O[tt], 0, 0, 0);
;             }
;         }
;         __builtin_amdgcn_sched_barrier(0);
; #pragma unroll
;         for (int tt = 0; tt < 2; ++tt)
; #pragma unroll
;             for (int r = 0; r < 16; ++r) ob[(32 * tt + (r & 3) + 8 * (r >> 2)) * OS] = O[tt][r];
;         __builtin_amdgcn_sched_barrier(0);
; #pragma unroll
;         for (int et = 0; et < 4; ++et)
; #pragma unroll
;             for (int rg = 0; rg < 4; ++rg) { const f32x4 dl = *(const LAS f32x4*)&decb[32 * et + 8 * rg];
; #pragma unroll
;                 for (int x = 0; x < 4; ++x) S[et][4 * rg + x] *= dl[x]; }
.LBB0_635:
	ds_read2_b64 v[64:67], v222 offset1:2
	v_cvt_pk_bf16_f32 v68, v32, v33
	v_cvt_pk_bf16_f32 v69, v34, v35
	v_cvt_pk_bf16_f32 v70, v36, v37
	v_cvt_pk_bf16_f32 v71, v38, v39
	ds_read2_b64 v[192:195], v222 offset0:4 offset1:6
	v_cvt_pk_bf16_f32 v196, v40, v41
	v_cvt_pk_bf16_f32 v197, v42, v43
	v_cvt_pk_bf16_f32 v198, v44, v45
	s_waitcnt lgkmcnt(1)
	v_mfma_f32_32x32x16_bf16 v[80:95], v[64:67], v[68:71], 0
	ds_read2_b64 v[64:67], v223 offset0:64 offset1:66
	v_cvt_pk_bf16_f32 v199, v46, v47
	s_waitcnt lgkmcnt(1)
	s_nop 0
	v_mfma_f32_32x32x16_bf16 v[80:95], v[192:195], v[196:199], v[80:95]
	ds_read2_b64 v[192:195], v223 offset0:68 offset1:70
	s_waitcnt lgkmcnt(1)
	v_mfma_f32_32x32x16_bf16 v[64:79], v[64:67], v[68:71], 0
	s_waitcnt lgkmcnt(0)
	v_mfma_f32_32x32x16_bf16 v[64:79], v[192:195], v[196:199], v[64:79]
	ds_read2_b64 v[192:195], v222 offset0:8 offset1:10
	v_cvt_pk_bf16_f32 v196, v16, v17
	v_cvt_pk_bf16_f32 v197, v18, v19
	v_cvt_pk_bf16_f32 v198, v20, v21
	v_cvt_pk_bf16_f32 v199, v22, v23
	s_waitcnt lgkmcnt(0)
	s_nop 0
	v_mfma_f32_32x32x16_bf16 v[80:95], v[192:195], v[196:199], v[80:95]
	ds_read2_b64 v[192:195], v223 offset0:72 offset1:74
	s_waitcnt lgkmcnt(0)
	v_mfma_f32_32x32x16_bf16 v[64:79], v[192:195], v[196:199], v[64:79]
	ds_read2_b64 v[192:195], v222 offset0:12 offset1:14
	v_cvt_pk_bf16_f32 v196, v24, v25
	v_cvt_pk_bf16_f32 v197, v26, v27
	v_cvt_pk_bf16_f32 v198, v28, v29
	v_cvt_pk_bf16_f32 v199, v30, v31
	s_waitcnt lgkmcnt(0)
	s_nop 0
	v_mfma_f32_32x32x16_bf16 v[80:95], v[192:195], v[196:199], v[80:95]
	ds_read2_b64 v[192:195], v223 offset0:76 offset1:78
	s_waitcnt lgkmcnt(0)
	v_mfma_f32_32x32x16_bf16 v[64:79], v[192:195], v[196:199], v[64:79]
	ds_read2_b64 v[192:195], v222 offset0:16 offset1:18
	v_cvt_pk_bf16_f32 v196, v48, v49
	v_cvt_pk_bf16_f32 v197, v50, v51
	v_cvt_pk_bf16_f32 v198, v52, v53
	v_cvt_pk_bf16_f32 v199, v54, v55
	s_waitcnt lgkmcnt(0)
	s_nop 0
	v_mfma_f32_32x32x16_bf16 v[80:95], v[192:195], v[196:199], v[80:95]
	ds_read2_b64 v[192:195], v223 offset0:80 offset1:82
	s_waitcnt lgkmcnt(0)
	v_mfma_f32_32x32x16_bf16 v[64:79], v[192:195], v[196:199], v[64:79]
	ds_read2_b64 v[192:195], v222 offset0:20 offset1:22
	v_cvt_pk_bf16_f32 v196, v56, v57
	v_cvt_pk_bf16_f32 v197, v58, v59
	v_cvt_pk_bf16_f32 v198, v60, v61
	v_cvt_pk_bf16_f32 v199, v62, v63
	s_waitcnt lgkmcnt(0)
	s_nop 0
	v_mfma_f32_32x32x16_bf16 v[80:95], v[192:195], v[196:199], v[80:95]
	ds_read2_b64 v[192:195], v223 offset0:84 offset1:86
	s_waitcnt lgkmcnt(0)
	v_mfma_f32_32x32x16_bf16 v[64:79], v[192:195], v[196:199], v[64:79]
	ds_read2_b64 v[192:195], v222 offset0:24 offset1:26
	v_cvt_pk_bf16_f32 v196, v0, v1
	v_cvt_pk_bf16_f32 v197, v2, v3
	v_cvt_pk_bf16_f32 v198, v4, v5
	v_cvt_pk_bf16_f32 v199, v6, v7
	s_waitcnt lgkmcnt(0)
	s_nop 0
	v_mfma_f32_32x32x16_bf16 v[80:95], v[192:195], v[196:199], v[80:95]
	ds_read2_b64 v[192:195], v223 offset0:88 offset1:90
	s_waitcnt lgkmcnt(0)
	v_mfma_f32_32x32x16_bf16 v[64:79], v[192:195], v[196:199], v[64:79]
	ds_read2_b64 v[192:195], v222 offset0:28 offset1:30
	v_cvt_pk_bf16_f32 v196, v8, v9
	v_cvt_pk_bf16_f32 v197, v10, v11
	v_cvt_pk_bf16_f32 v198, v12, v13
	v_cvt_pk_bf16_f32 v199, v14, v15
	s_waitcnt lgkmcnt(0)
	s_nop 0
	v_mfma_f32_32x32x16_bf16 v[80:95], v[192:195], v[196:199], v[80:95]
	ds_read2_b64 v[192:195], v223 offset0:92 offset1:94
	s_waitcnt lgkmcnt(0)
	s_barrier
	v_mfma_f32_32x32x16_bf16 v[64:79], v[192:195], v[196:199], v[64:79]
	ds_read_b128 v[192:195], v206
	ds_read_b64_tr_b16 v[196:197], v218
	ds_read_b64_tr_b16 v[198:199], v218 offset:4608
	ds_read_b128 v[222:225], v206 offset:1024
	ds_read_b64_tr_b16 v[226:227], v218 offset:9216
	ds_read_b64_tr_b16 v[228:229], v218 offset:13824
	s_waitcnt lgkmcnt(3)
	v_mfma_f32_32x32x16_bf16 v[80:95], v[192:195], v[196:199], v[80:95]
	s_waitcnt lgkmcnt(0)
	v_mfma_f32_32x32x16_bf16 v[80:95], v[222:225], v[226:229], v[80:95]
	ds_read_b128 v[192:195], v206 offset:2048
	ds_read_b128 v[222:225], v206 offset:3072
	s_waitcnt lgkmcnt(1)
	v_mfma_f32_32x32x16_bf16 v[64:79], v[192:195], v[196:199], v[64:79]
	s_waitcnt lgkmcnt(0)
	v_mfma_f32_32x32x16_bf16 v[64:79], v[222:225], v[226:229], v[64:79]
	ds_read_b128 v[192:195], v206 offset:4096
	ds_read_b64_tr_b16 v[196:197], v218 offset:18432
	ds_read_b64_tr_b16 v[198:199], v218 offset:23040
	ds_read_b128 v[222:225], v206 offset:5120
	ds_read_b64_tr_b16 v[226:227], v218 offset:27648
	ds_read_b64_tr_b16 v[228:229], v218 offset:32256
	s_waitcnt lgkmcnt(3)
	v_mfma_f32_32x32x16_bf16 v[64:79], v[192:195], v[196:199], v[64:79]
	s_waitcnt lgkmcnt(0)
	v_mfma_f32_32x32x16_bf16 v[64:79], v[222:225], v[226:229], v[64:79]
	ds_write_b32 v207, v80
	ds_write_b32 v207, v81 offset:1040
	ds_write_b32 v207, v82 offset:2080
	ds_write_b32 v207, v83 offset:3120
	ds_write_b32 v207, v84 offset:8320
	ds_write_b32 v207, v85 offset:9360
	ds_write_b32 v207, v86 offset:10400
	ds_write_b32 v207, v87 offset:11440
	ds_write_b32 v207, v88 offset:16640
	ds_write_b32 v207, v89 offset:17680
	ds_write_b32 v207, v90 offset:18720
	ds_write_b32 v207, v91 offset:19760
	ds_write_b32 v207, v92 offset:24960
	ds_write_b32 v207, v93 offset:26000
	ds_write_b32 v207, v94 offset:27040
	ds_write_b32 v207, v95 offset:28080
	ds_write_b32 v207, v64 offset:33280
	ds_write_b32 v207, v65 offset:34320
	ds_write_b32 v207, v66 offset:35360
	ds_write_b32 v207, v67 offset:36400
	ds_write_b32 v207, v68 offset:41600
	ds_write_b32 v207, v69 offset:42640
	ds_write_b32 v207, v70 offset:43680
	ds_write_b32 v207, v71 offset:44720
	ds_write_b32 v207, v72 offset:49920
	ds_write_b32 v207, v73 offset:50960
	ds_write_b32 v207, v74 offset:52000
	ds_write_b32 v207, v75 offset:53040
	ds_write_b32 v207, v76 offset:58240
	ds_write_b32 v207, v77 offset:59280
	ds_write_b32 v207, v78 offset:60320
	ds_write_b32 v207, v79 offset:61360
	ds_read_b128 v[64:67], v205 offset:96
	ds_read_b128 v[68:71], v205 offset:64
	ds_read_b128 v[72:75], v205 offset:32
	ds_read_b128 v[76:79], v205
	s_waitcnt vmcnt(11)
; #define LAS __attribute__((address_space(3)))
; __device__ __forceinline__ void gla_unit(LAS unsigned char* lds, const unsigned char* ws, const float* g_onorm, const int b, const int h, const int wv) {
;     ...
; #pragma unroll
;         for (int et = 0; et < 4; ++et)
; #pragma unroll
;             for (int rg = 0; rg < 4; ++rg) { const f32x4 dl = *(const LAS f32x4*)&decb[32 * et + 8 * rg];
; #pragma unroll
;                 for (int x = 0; x < 4; ++x) S[et][4 * rg + x] *= dl[x]; }
; #pragma unroll
;         for (int ks = 0; ks < 4; ++ks) {
;             const LAS unsigned char* vp = vN + 16 * ks * VS;
;             const bf16x8 bv = tr8(vp, vp + 4 * VS);
; #pragma unroll
;             for (int et = 0; et < 4; ++et) {
;                 const LAS unsigned char* kp = keN + 32 * et * 2 + 16 * ks * ES;
;                 const bf16x8 ak = tr8(kp, kp + 4 * ES);
;                 S[et] = __builtin_amdgcn_mfma_f32_32x32x16_bf16(ak, bv, S[et], 0, 0, 0);
;             }
;         }
	v_lshlrev_b32_e32 v232, 16, v176
	s_waitcnt lgkmcnt(3)
	v_pk_mul_f32 v[46:47], v[46:47], v[66:67]
	s_waitcnt lgkmcnt(2)
	v_pk_mul_f32 v[42:43], v[42:43], v[70:71]
	v_pk_mul_f32 v[44:45], v[44:45], v[64:65]
	s_waitcnt lgkmcnt(0)
	v_pk_mul_f32 v[34:35], v[34:35], v[78:79]
	v_pk_mul_f32 v[40:41], v[40:41], v[68:69]
	ds_read_b128 v[68:71], v205 offset:192
	ds_read_b128 v[78:81], v205 offset:224
	ds_read_b128 v[64:67], v205 offset:128
	ds_read_b128 v[82:85], v205 offset:160
	v_pk_mul_f32 v[38:39], v[38:39], v[74:75]
	v_pk_mul_f32 v[36:37], v[36:37], v[72:73]
	v_pk_mul_f32 v[32:33], v[32:33], v[76:77]
	s_waitcnt lgkmcnt(2)
	v_pk_mul_f32 v[30:31], v[30:31], v[80:81]
	v_pk_mul_f32 v[26:27], v[26:27], v[70:71]
	s_waitcnt lgkmcnt(0)
	v_pk_mul_f32 v[22:23], v[22:23], v[84:85]
	v_pk_mul_f32 v[18:19], v[18:19], v[66:67]
	v_pk_mul_f32 v[28:29], v[28:29], v[78:79]
	v_pk_mul_f32 v[24:25], v[24:25], v[68:69]
	v_pk_mul_f32 v[20:21], v[20:21], v[82:83]
	ds_read_b128 v[66:69], v205 offset:256
	ds_read_b128 v[70:73], v205 offset:288
	ds_read_b128 v[74:77], v205 offset:320
	ds_read_b128 v[78:81], v205 offset:352
	ds_read_b64_tr_b16 v[82:83], v219
	ds_read_b64_tr_b16 v[84:85], v219 offset:2304
	ds_read_b64_tr_b16 v[88:89], v220 offset:1280
	ds_read_b64_tr_b16 v[86:87], v220
	ds_read_b64_tr_b16 v[90:91], v220 offset:64
	ds_read_b64_tr_b16 v[192:193], v220 offset:128
	ds_read_b64_tr_b16 v[196:197], v220 offset:192
	ds_read_b64_tr_b16 v[92:93], v220 offset:1344
	ds_read_b64_tr_b16 v[194:195], v220 offset:1408
	ds_read_b64_tr_b16 v[198:199], v220 offset:1472
	ds_read_b64_tr_b16 v[222:223], v219 offset:9216
	ds_read_b64_tr_b16 v[224:225], v219 offset:11520
	s_waitcnt lgkmcnt(8)
	v_mfma_f32_32x32x16_bf16 v[32:47], v[86:89], v[82:85], v[32:47]
	v_mul_f32_e64 v58, v58, v76
	v_mul_f32_e64 v59, v59, v77
	v_mul_f32_e64 v54, v54, v72
	v_mul_f32_e64 v55, v55, v73
	v_mul_f32_e64 v50, v50, v68
	v_mul_f32_e64 v51, v51, v69
	v_pk_mul_f32 v[60:61], v[60:61], v[78:79]
	v_pk_mul_f32 v[56:57], v[56:57], v[74:75]
	ds_read_b128 v[72:75], v205 offset:448
	ds_read_b128 v[76:79], v205 offset:480
	v_pk_mul_f32 v[52:53], v[52:53], v[70:71]
	ds_read_b128 v[68:71], v205 offset:384
	ds_read_b128 v[86:89], v205 offset:416
	v_pk_mul_f32 v[16:17], v[16:17], v[64:65]
	v_pk_mul_f32 v[62:63], v[62:63], v[80:81]
	v_pk_mul_f32 v[48:49], v[48:49], v[66:67]
	s_waitcnt lgkmcnt(2)
	v_pk_mul_f32 v[14:15], v[14:15], v[78:79]
	v_pk_mul_f32 v[10:11], v[10:11], v[74:75]
	s_waitcnt lgkmcnt(0)
	v_pk_mul_f32 v[6:7], v[6:7], v[88:89]
	v_pk_mul_f32 v[2:3], v[2:3], v[70:71]
	v_pk_mul_f32 v[12:13], v[12:13], v[76:77]
	v_pk_mul_f32 v[8:9], v[8:9], v[72:73]
	v_pk_mul_f32 v[4:5], v[4:5], v[86:87]
	v_pk_mul_f32 v[0:1], v[0:1], v[68:69]
	v_mfma_f32_32x32x16_bf16 v[16:31], v[90:93], v[82:85], v[16:31]
	ds_read_b64_tr_b16 v[66:67], v220 offset:6400
	ds_read_b64_tr_b16 v[64:65], v220 offset:5120
	ds_read_b64_tr_b16 v[68:69], v220 offset:5184
	ds_read_b64_tr_b16 v[72:73], v220 offset:5248
	ds_read_b64_tr_b16 v[76:77], v220 offset:5312
	ds_read_b64_tr_b16 v[70:71], v220 offset:6464
	ds_read_b64_tr_b16 v[74:75], v220 offset:6528
	ds_read_b64_tr_b16 v[78:79], v220 offset:6592
	v_and_b32_e32 v233, 0xffff0000, v176
	s_mov_b32 s2, 0x4e1c8000
	s_add_i32 s60, s60, 2
	v_lshl_add_u64 v[184:185], v[184:185], 0, s[68:69]
	v_lshl_add_u64 v[188:189], v[188:189], 0, s[70:71]
	s_cmp_lt_u32 s66, 30
	v_mfma_f32_32x32x16_bf16 v[48:63], v[192:195], v[82:85], v[48:63]
	v_lshl_add_u64 v[190:191], v[190:191], 0, s[68:69]
	v_mfma_f32_32x32x16_bf16 v[0:15], v[196:199], v[82:85], v[0:15]
	s_waitcnt lgkmcnt(6)
	v_mfma_f32_32x32x16_bf16 v[32:47], v[64:67], v[222:225], v[32:47]
	s_waitcnt lgkmcnt(2)
	v_mfma_f32_32x32x16_bf16 v[16:31], v[68:71], v[222:225], v[16:31]
	s_waitcnt lgkmcnt(1)
	v_mfma_f32_32x32x16_bf16 v[48:63], v[72:75], v[222:225], v[48:63]
	s_waitcnt lgkmcnt(0)
	v_mfma_f32_32x32x16_bf16 v[0:15], v[76:79], v[222:225], v[0:15]
	ds_read_b64_tr_b16 v[64:65], v219 offset:18432
	ds_read_b64_tr_b16 v[66:67], v219 offset:20736
	ds_read_b64_tr_b16 v[70:71], v220 offset:11520
	ds_read_b64_tr_b16 v[68:69], v220 offset:10240
	ds_read_b64_tr_b16 v[72:73], v220 offset:10304
	ds_read_b64_tr_b16 v[76:77], v220 offset:10368
	ds_read_b64_tr_b16 v[80:81], v220 offset:10432
	ds_read_b64_tr_b16 v[74:75], v220 offset:11584
	ds_read_b64_tr_b16 v[78:79], v220 offset:11648
	ds_read_b64_tr_b16 v[82:83], v220 offset:11712
	ds_read_b64_tr_b16 v[84:85], v219 offset:27648
	ds_read_b64_tr_b16 v[86:87], v219 offset:29952
	s_waitcnt lgkmcnt(8)
	v_mfma_f32_32x32x16_bf16 v[32:47], v[68:71], v[64:67], v[32:47]
	ds_read_b64_tr_b16 v[68:69], v220 offset:16640
	s_waitcnt lgkmcnt(5)
	v_mfma_f32_32x32x16_bf16 v[16:31], v[72:75], v[64:67], v[16:31]
	s_waitcnt lgkmcnt(4)
	v_mfma_f32_32x32x16_bf16 v[48:63], v[76:79], v[64:67], v[48:63]
	s_waitcnt lgkmcnt(3)
	v_mfma_f32_32x32x16_bf16 v[0:15], v[80:83], v[64:67], v[0:15]
	ds_read_b64_tr_b16 v[66:67], v220 offset:15360
	ds_read_b64_tr_b16 v[70:71], v220 offset:15424
	ds_read_b64_tr_b16 v[74:75], v220 offset:15488
	ds_read_b64_tr_b16 v[78:79], v220 offset:15552
	ds_read_b64_tr_b16 v[72:73], v220 offset:16704
	ds_read_b64_tr_b16 v[76:77], v220 offset:16768
	ds_read_b64_tr_b16 v[80:81], v220 offset:16832
	s_waitcnt lgkmcnt(0)
	s_barrier
; #define LAS __attribute__((address_space(3)))
; __device__ __forceinline__ unsigned cvt_pk_bf16(float lo, float hi) { const bf16x2_t r = __builtin_convertvector((f32x2_t){lo, hi}, bf16x2_t); return __builtin_bit_cast(unsigned, r); }
; __device__ __forceinline__ float bf_lo(unsigned w) { return __uint_as_float(w << 16); }
; __device__ __forceinline__ float bf_hi(unsigned w) { return __uint_as_float(w & 0xffff0000u); }
; __device__ __forceinline__ void gla_unit(LAS unsigned char* lds, const unsigned char* ws, const float* g_onorm, const int b, const int h, const int wv) {
;     ...
;         {
;             const int t = tid >> 3, g8 = tid & 7;
;             float ov[32]; float ss = 0.f;
; #pragma unroll
;             for (int x = 0; x < 8; ++x) { const f32x4 v = *(const LAS f32x4*)&obuf[t * OS + 32 * g8 + 4 * x]; ov[4 * x] = v[0]; ov[4 * x + 1] = v[1]; ov[4 * x + 2] = v[2]; ov[4 * x + 3] = v[3];
;                 ss += v[0] * v[0] + v[1] * v[1] + v[2] * v[2] + v[3] * v[3]; }
;             ss += __builtin_bit_cast(float, __builtin_amdgcn_ds_swizzle(__builtin_bit_cast(int, ss), (1 << 10) | 0x1F)); ss += __builtin_bit_cast(float, __builtin_amdgcn_ds_swizzle(__builtin_bit_cast(int, ss), (2 << 10) | 0x1F));
;             ss += __builtin_bit_cast(float, __builtin_amdgcn_ds_swizzle(__builtin_bit_cast(int, ss), (4 << 10) | 0x1F));
;             const float rstd = __builtin_amdgcn_rsqf(ss * (1.0f / 256.0f) + EPSV);
;             bf16_t* mp = mix + (t0 + t) * DM + 1024 + h * 256 + 32 * g8;
; #pragma unroll
;             for (int x = 0; x < 4; ++x) {
;                 const u32x4 og = ogr[x];
;                 const f32x4 g0 = *(const LAS f32x4*)&gon[32 * g8 + 8 * x], g1 = *(const LAS f32x4*)&gon[32 * g8 + 8 * x + 4];
;                 const float gg2[8] = {g0[0], g0[1], g0[2], g0[3], g1[0], g1[1], g1[2], g1[3]};
;                 float res[8];
; #pragma unroll
;                 for (int y = 0; y < 4; ++y) { const float a0 = bf_lo(og[y]), a1 = bf_hi(og[y]);
;                     res[2 * y] = ov[8 * x + 2 * y] * rstd * gg2[2 * y] * a0;
;                     res[2 * y + 1] = ov[8 * x + 2 * y + 1] * rstd * gg2[2 * y + 1] * a1; }
;                 u32x4 wv4; wv4[0] = cvt_pk_bf16(res[0], res[1]); wv4[1] = cvt_pk_bf16(res[2], res[3]); wv4[2] = cvt_pk_bf16(res[4], res[5]); wv4[3] = cvt_pk_bf16(res[6], res[7]);
;                 *(u32x4*)(mp + 8 * x) = wv4;
;             }
	v_mfma_f32_32x32x16_bf16 v[32:47], v[66:69], v[84:87], v[32:47]
	ds_read_b128 v[64:67], v221
	ds_read_b128 v[88:91], v221 offset:16
	ds_read_b128 v[92:95], v221 offset:32
	ds_read_b128 v[192:195], v221 offset:48
	s_waitcnt lgkmcnt(3)
	v_mul_f32_e32 v68, v65, v65
	s_waitcnt lgkmcnt(2)
	v_mul_f32_e32 v69, v89, v89
	v_fmac_f32_e32 v68, v64, v64
	v_fmac_f32_e32 v69, v88, v88
	v_fmac_f32_e32 v68, v66, v66
	v_fmac_f32_e32 v69, v90, v90
	v_mfma_f32_32x32x16_bf16 v[16:31], v[70:73], v[84:87], v[16:31]
	v_fmac_f32_e32 v68, v67, v67
	v_fmac_f32_e32 v69, v91, v91
	s_waitcnt lgkmcnt(1)
	v_mov_b32_e32 v70, v93
	s_waitcnt lgkmcnt(0)
	v_mov_b32_e32 v71, v193
	v_add_f32_e32 v222, v68, v69
	v_mov_b32_e32 v68, v92
	v_mov_b32_e32 v69, v192
	v_pk_mul_f32 v[70:71], v[70:71], v[70:71]
	v_mov_b32_e32 v82, v95
	v_pk_fma_f32 v[68:69], v[68:69], v[68:69], v[70:71]
	v_mov_b32_e32 v70, v94
	v_mov_b32_e32 v71, v194
	v_pk_fma_f32 v[72:73], v[70:71], v[70:71], v[68:69]
	ds_read_b128 v[68:71], v221 offset:64
	ds_read_b128 v[196:199], v221 offset:80
	v_mov_b32_e32 v83, v195
	v_pk_fma_f32 v[72:73], v[82:83], v[82:83], v[72:73]
	v_mfma_f32_32x32x16_bf16 v[48:63], v[74:77], v[84:87], v[48:63]
	v_add_f32_e32 v72, v222, v72
	s_waitcnt lgkmcnt(1)
	v_mov_b32_e32 v82, v69
	s_waitcnt lgkmcnt(0)
	v_mov_b32_e32 v83, v197
	ds_read_b128 v[222:225], v221 offset:96
	ds_read_b128 v[226:229], v221 offset:112
	v_add_f32_e32 v230, v72, v73
	v_mov_b32_e32 v72, v68
	v_mov_b32_e32 v73, v196
	v_pk_mul_f32 v[82:83], v[82:83], v[82:83]
	v_mfma_f32_32x32x16_bf16 v[0:15], v[78:81], v[84:87], v[0:15]
	v_fma_f32 v72, v72, v72, v82
	v_fma_f32 v73, v73, v73, v83
	v_mov_b32_e32 v82, v70
	v_mov_b32_e32 v83, v198
	v_fma_f32 v72, v82, v82, v72
	v_fma_f32 v73, v83, v83, v73
	v_mov_b32_e32 v82, v71
	v_mov_b32_e32 v83, v199
	v_pk_fma_f32 v[72:73], v[82:83], v[82:83], v[72:73]
	s_waitcnt lgkmcnt(1)
	v_mov_b32_e32 v82, v223
	v_add_f32_e32 v72, v230, v72
	s_waitcnt lgkmcnt(0)
	v_mov_b32_e32 v83, v227
	v_add_f32_e32 v230, v72, v73
	v_mov_b32_e32 v72, v222
	v_mov_b32_e32 v73, v226
	v_pk_mul_f32 v[82:83], v[82:83], v[82:83]
	s_nop 0
	v_pk_fma_f32 v[72:73], v[72:73], v[72:73], v[82:83]
	v_mov_b32_e32 v82, v224
	v_mov_b32_e32 v83, v228
	v_pk_fma_f32 v[72:73], v[82:83], v[82:83], v[72:73]
	v_mov_b32_e32 v82, v225
	v_mov_b32_e32 v83, v229
	v_pk_fma_f32 v[72:73], v[82:83], v[82:83], v[72:73]
	s_nop 0
	v_add_f32_e32 v72, v230, v72
	v_add_f32_e32 v72, v72, v73
	ds_swizzle_b32 v73, v72 offset:swizzle(SWAP,1)
	s_waitcnt lgkmcnt(0)
	v_add_f32_e32 v72, v72, v73
	ds_swizzle_b32 v73, v72 offset:swizzle(SWAP,2)
	s_waitcnt lgkmcnt(0)
	v_add_f32_e32 v72, v72, v73
	ds_swizzle_b32 v73, v72 offset:swizzle(SWAP,4)
	s_waitcnt lgkmcnt(0)
	v_add_f32_e32 v72, v72, v73
	v_fmamk_f32 v72, v72, 0x3b800000, v181
	v_rsq_f32_e32 v230, v72
	ds_read_b128 v[72:75], v208
	ds_read_b128 v[76:79], v208 offset:16
	ds_read_b128 v[80:83], v208 offset:32
	ds_read_b128 v[84:87], v208 offset:48
	v_pk_mul_f32 v[64:65], v[64:65], v[230:231] op_sel_hi:[1,0]
	v_pk_mul_f32 v[66:67], v[66:67], v[230:231] op_sel_hi:[1,0]
	s_waitcnt lgkmcnt(3)
	v_pk_mul_f32 v[64:65], v[72:73], v[64:65]
	v_lshlrev_b32_e32 v72, 16, v177
	v_and_b32_e32 v73, 0xffff0000, v177
	v_pk_mul_f32 v[66:67], v[74:75], v[66:67]
	v_pk_mul_f32 v[74:75], v[88:89], v[230:231] op_sel_hi:[1,0]
	v_pk_mul_f32 v[66:67], v[66:67], v[72:73]
	v_lshlrev_b32_e32 v72, 16, v178
	v_and_b32_e32 v73, 0xffff0000, v178
	s_waitcnt lgkmcnt(2)
	v_pk_mul_f32 v[74:75], v[76:77], v[74:75]
	v_pk_mul_f32 v[76:77], v[90:91], v[230:231] op_sel_hi:[1,0]
	v_pk_mul_f32 v[72:73], v[74:75], v[72:73]
	v_lshlrev_b32_e32 v74, 16, v179
	v_and_b32_e32 v75, 0xffff0000, v179
	v_pk_mul_f32 v[76:77], v[78:79], v[76:77]
	v_pk_mul_f32 v[64:65], v[64:65], v[232:233]
	v_pk_mul_f32 v[74:75], v[76:77], v[74:75]
	v_add_co_u32_e32 v76, vcc, s2, v200
	v_cvt_pk_bf16_f32 v64, v64, v65
	v_cvt_pk_bf16_f32 v65, v66, v67
	v_cvt_pk_bf16_f32 v66, v72, v73
	v_cvt_pk_bf16_f32 v67, v74, v75
	v_addc_co_u32_e32 v77, vcc, 0, v201, vcc
	global_store_dwordx4 v[76:77], v[64:67], off offset:2048
	v_pk_mul_f32 v[72:73], v[94:95], v[230:231] op_sel_hi:[1,0]
	v_pk_mul_f32 v[74:75], v[192:193], v[230:231] op_sel_hi:[1,0]
	v_pk_mul_f32 v[66:67], v[92:93], v[230:231] op_sel_hi:[1,0]
	s_waitcnt vmcnt(9)
; #define LAS __attribute__((address_space(3)))
; __device__ __forceinline__ unsigned cvt_pk_bf16(float lo, float hi) { const bf16x2_t r = __builtin_convertvector((f32x2_t){lo, hi}, bf16x2_t); return __builtin_bit_cast(unsigned, r); }
; __device__ __forceinline__ float bf_lo(unsigned w) { return __uint_as_float(w << 16); }
; __device__ __forceinline__ float bf_hi(unsigned w) { return __uint_as_float(w & 0xffff0000u); }
; __device__ __forceinline__ void gla_unit(LAS unsigned char* lds, const unsigned char* ws, const float* g_onorm, const int b, const int h, const int wv) {
;     ...
;         __syncthreads();
; #pragma unroll
;         for (int i = 0; i < 2; ++i) { const int c = tid + 512 * i, row = c >> 4, cc = (c & 15) * 16;
;             *(LAS u32x4*)(lds + L_Q + row * QS + cc) = qr[par][i]; *(LAS u32x4*)(lds + L_K + row * QS + cc) = kr[par][i]; }
; #pragma unroll
;         for (int i = 0; i < 4; ++i) { const int c = tid + 512 * i; *(LAS u32x4*)(lds + L_V + (c >> 5) * VS + (c & 31) * 16) = vr[par][i]; }
;         if (tid < 32) {
;             const float L2E_ = 1.4426950408889634f;
;             *(LAS f32x4*)&dec[tid * 4] = (f32x4){__builtin_amdgcn_exp2f(dr[0] * L2E_), __builtin_amdgcn_exp2f(dr[1] * L2E_), __builtin_amdgcn_exp2f(dr[2] * L2E_), __builtin_amdgcn_exp2f(dr[3] * L2E_)};
;         }
;     ...
; #pragma unroll
;             for (int x = 0; x < 4; ++x) {
;                 const u32x4 og = ogr[x];
;                 const f32x4 g0 = *(const LAS f32x4*)&gon[32 * g8 + 8 * x], g1 = *(const LAS f32x4*)&gon[32 * g8 + 8 * x + 4];
;                 const float gg2[8] = {g0[0], g0[1], g0[2], g0[3], g1[0], g1[1], g1[2], g1[3]};
;                 float res[8];
; #pragma unroll
;                 for (int y = 0; y < 4; ++y) { const float a0 = bf_lo(og[y]), a1 = bf_hi(og[y]);
;                     res[2 * y] = ov[8 * x + 2 * y] * rstd * gg2[2 * y] * a0;
;                     res[2 * y + 1] = ov[8 * x + 2 * y + 1] * rstd * gg2[2 * y + 1] * a1; }
;                 u32x4 wv4; wv4[0] = cvt_pk_bf16(res[0], res[1]); wv4[1] = cvt_pk_bf16(res[2], res[3]); wv4[2] = cvt_pk_bf16(res[4], res[5]); wv4[3] = cvt_pk_bf16(res[6], res[7]);
;                 *(u32x4*)(mp + 8 * x) = wv4;
;             }
	v_lshlrev_b32_e32 v64, 16, v172
	v_and_b32_e32 v65, 0xffff0000, v172
	s_waitcnt lgkmcnt(1)
	v_pk_mul_f32 v[66:67], v[80:81], v[66:67]
	v_pk_mul_f32 v[72:73], v[82:83], v[72:73]
	v_pk_mul_f32 v[64:65], v[66:67], v[64:65]
	v_lshlrev_b32_e32 v66, 16, v173
	v_and_b32_e32 v67, 0xffff0000, v173
	v_pk_mul_f32 v[66:67], v[72:73], v[66:67]
	v_lshlrev_b32_e32 v72, 16, v174
	v_and_b32_e32 v73, 0xffff0000, v174
	s_waitcnt lgkmcnt(0)
	v_pk_mul_f32 v[74:75], v[84:85], v[74:75]
	v_pk_mul_f32 v[78:79], v[194:195], v[230:231] op_sel_hi:[1,0]
	v_pk_mul_f32 v[72:73], v[74:75], v[72:73]
	v_lshlrev_b32_e32 v74, 16, v175
	v_and_b32_e32 v75, 0xffff0000, v175
	v_pk_mul_f32 v[78:79], v[86:87], v[78:79]
	v_cvt_pk_bf16_f32 v64, v64, v65
	v_pk_mul_f32 v[74:75], v[78:79], v[74:75]
	v_cvt_pk_bf16_f32 v65, v66, v67
	v_cvt_pk_bf16_f32 v66, v72, v73
	v_cvt_pk_bf16_f32 v67, v74, v75
	global_store_dwordx4 v[76:77], v[64:67], off offset:2064
	ds_read_b128 v[64:67], v208 offset:64
	ds_read_b128 v[72:75], v208 offset:80
	v_pk_mul_f32 v[68:69], v[68:69], v[230:231] op_sel_hi:[1,0]
	v_pk_mul_f32 v[70:71], v[70:71], v[230:231] op_sel_hi:[1,0]
	v_lshlrev_b32_e32 v78, 16, v168
	s_waitcnt lgkmcnt(1)
	v_pk_mul_f32 v[64:65], v[64:65], v[68:69]
	v_lshlrev_b32_e32 v68, 16, v169
	v_and_b32_e32 v69, 0xffff0000, v169
	v_pk_mul_f32 v[66:67], v[66:67], v[70:71]
	v_pk_mul_f32 v[70:71], v[196:197], v[230:231] op_sel_hi:[1,0]
	v_pk_mul_f32 v[66:67], v[66:67], v[68:69]
	v_lshlrev_b32_e32 v68, 16, v170
	v_and_b32_e32 v69, 0xffff0000, v170
	s_waitcnt lgkmcnt(0)
	v_pk_mul_f32 v[70:71], v[72:73], v[70:71]
	v_pk_mul_f32 v[72:73], v[198:199], v[230:231] op_sel_hi:[1,0]
	v_and_b32_e32 v79, 0xffff0000, v168
	v_pk_mul_f32 v[68:69], v[70:71], v[68:69]
	v_lshlrev_b32_e32 v70, 16, v171
	v_and_b32_e32 v71, 0xffff0000, v171
	v_pk_mul_f32 v[72:73], v[74:75], v[72:73]
	v_pk_mul_f32 v[64:65], v[64:65], v[78:79]
	v_pk_mul_f32 v[70:71], v[72:73], v[70:71]
	v_cvt_pk_bf16_f32 v64, v64, v65
	v_cvt_pk_bf16_f32 v65, v66, v67
	v_cvt_pk_bf16_f32 v66, v68, v69
	v_cvt_pk_bf16_f32 v67, v70, v71
	global_store_dwordx4 v[76:77], v[64:67], off offset:2080
	ds_read_b128 v[64:67], v208 offset:96
	ds_read_b128 v[68:71], v208 offset:112
	v_pk_mul_f32 v[74:75], v[222:223], v[230:231] op_sel_hi:[1,0]
	v_lshlrev_b32_e32 v72, 16, v164
	v_and_b32_e32 v73, 0xffff0000, v164
	s_waitcnt lgkmcnt(1)
	v_pk_mul_f32 v[64:65], v[74:75], v[64:65]
	v_pk_mul_f32 v[74:75], v[224:225], v[230:231] op_sel_hi:[1,0]
	v_pk_mul_f32 v[64:65], v[64:65], v[72:73]
	v_lshlrev_b32_e32 v72, 16, v165
	v_and_b32_e32 v73, 0xffff0000, v165
	v_pk_mul_f32 v[66:67], v[74:75], v[66:67]
	v_pk_mul_f32 v[74:75], v[226:227], v[230:231] op_sel_hi:[1,0]
	v_pk_mul_f32 v[66:67], v[66:67], v[72:73]
	v_lshlrev_b32_e32 v72, 16, v166
	v_and_b32_e32 v73, 0xffff0000, v166
	s_waitcnt lgkmcnt(0)
	v_pk_mul_f32 v[68:69], v[74:75], v[68:69]
	v_pk_mul_f32 v[74:75], v[228:229], v[230:231] op_sel_hi:[1,0]
	v_pk_mul_f32 v[68:69], v[68:69], v[72:73]
	v_lshlrev_b32_e32 v72, 16, v167
	v_and_b32_e32 v73, 0xffff0000, v167
	v_pk_mul_f32 v[70:71], v[74:75], v[70:71]
	s_mov_b64 s[2:3], 0x40000
	v_pk_mul_f32 v[70:71], v[70:71], v[72:73]
	v_lshl_add_u64 v[182:183], v[182:183], 0, s[2:3]
	s_mov_b64 s[2:3], 0x8000
	v_cvt_pk_bf16_f32 v64, v64, v65
	v_cvt_pk_bf16_f32 v65, v66, v67
	v_cvt_pk_bf16_f32 v66, v68, v69
	v_cvt_pk_bf16_f32 v67, v70, v71
	v_lshl_add_u64 v[186:187], v[186:187], 0, s[2:3]
	global_store_dwordx4 v[76:77], v[64:67], off offset:2096
	s_cbranch_scc0 .LBB0_655
.LBB0_636:
	s_nop 0
	v_add_u32_e32 v64, 0, v180
	v_add_u32_e32 v226, 0x1fc00, v64
	s_waitcnt lgkmcnt(0)
	s_barrier
	s_waitcnt vmcnt(20)
	ds_write_b128 v209, v[108:111]
	ds_write_b128 v209, v[96:99] offset:17408
	ds_write_b128 v210, v[100:103]
	ds_write_b128 v210, v[104:107] offset:17408
	ds_write_b128 v211, v[112:115]
	ds_write_b128 v212, v[116:119]
	ds_write_b128 v213, v[120:123]
	s_nop 0
	ds_write_b128 v214, v[128:131]
	s_and_saveexec_b64 s[2:3], s[0:1]
	s_cbranch_execz .LBB0_638
	s_waitcnt vmcnt(12)
	v_mul_f32_e32 v64, 0x3fb8aa3b, v124
	v_mul_f32_e32 v65, 0x3fb8aa3b, v125
	v_mul_f32_e32 v66, 0x3fb8aa3b, v126
	v_mul_f32_e32 v67, 0x3fb8aa3b, v127
	v_exp_f32_e32 v64, v64
	v_exp_f32_e32 v65, v65
	v_exp_f32_e32 v66, v66
	v_exp_f32_e32 v67, v67
	ds_write_b128 v226, v[64:67]

; #define GLA_LOAD_DR(n) do { if (tid < 32) dr = *(const f32x4*)(BC + ((size_t)b * SEQ + 64 * (n) + 63) * 512 + h * 128 + tid * 4); } while (0)
; __device__ __forceinline__ void gla_unit(LAS unsigned char* lds, const unsigned char* ws, const float* g_onorm, const int b, const int h, const int wv) {
;     ...
;         if (n + 1 < SEQ / 64) GLA_LOAD_DR(n + 1);
;         if (n + 2 < SEQ / 64) GLA_LOAD(par, n + 2);
.LBB0_640:
	s_or_b64 exec, exec, s[2:3]
	s_add_i32 s66, s60, -1
	s_cmp_lt_u32 s66, 30
	s_mov_b64 s[2:3], -1
	s_cmp_gt_u32 s66, 29
	v_lshl_add_u64 v[194:195], s[76:77], 0, v[186:187]
	v_lshl_add_u64 v[192:193], s[76:77], 0, v[184:185]
	s_nop 0
	v_add_co_u32_e32 v64, vcc, 0x46190000, v194
	s_nop 1
	v_addc_co_u32_e32 v65, vcc, 0, v195, vcc
	v_add_co_u32_e32 v66, vcc, 0x47190000, v194
	s_nop 1
	v_addc_co_u32_e32 v67, vcc, 0, v195, vcc
	global_load_dwordx4 v[108:111], v[64:65], off
	global_load_dwordx4 v[96:99], v[66:67], off
	v_add_co_u32_e32 v64, vcc, 0x46192000, v194
	s_nop 1
	v_addc_co_u32_e32 v65, vcc, 0, v195, vcc
	v_add_co_u32_e32 v66, vcc, 0x47192000, v194
	s_nop 1
	v_addc_co_u32_e32 v67, vcc, 0, v195, vcc
	global_load_dwordx4 v[100:103], v[64:65], off
	global_load_dwordx4 v[104:107], v[66:67], off
	v_add_co_u32_e32 v64, vcc, 0x48198000, v192
	s_nop 1
	v_addc_co_u32_e32 v65, vcc, 0, v193, vcc
	v_add_co_u32_e32 v66, vcc, 0x4819a000, v192
	s_nop 1
	v_addc_co_u32_e32 v67, vcc, 0, v193, vcc
	global_load_dwordx4 v[112:115], v[64:65], off
	global_load_dwordx4 v[116:119], v[66:67], off
	v_add_co_u32_e32 v64, vcc, 0x4819c000, v192
	s_nop 1
	v_addc_co_u32_e32 v65, vcc, 0, v193, vcc
	v_add_co_u32_e32 v66, vcc, 0x4819e000, v192
	s_nop 1
	v_addc_co_u32_e32 v67, vcc, 0, v193, vcc
	global_load_dwordx4 v[120:123], v[64:65], off
	global_load_dwordx4 v[128:131], v[66:67], off

; #define LAS __attribute__((address_space(3)))
; __device__ __forceinline__ void gla_unit(LAS unsigned char* lds, const unsigned char* ws, const float* g_onorm, const int b, const int h, const int wv) {
;     ...
;         f32x16 O[2];
; #pragma unroll
;         for (int tt = 0; tt < 2; ++tt)
; #pragma unroll
;             for (int r = 0; r < 16; ++r) O[tt][r] = 0.f;
; #pragma unroll
;         for (int et = 0; et < 4; ++et)
; #pragma unroll
;             for (int s2 = 0; s2 < 2; ++s2) {
;                 const bf16x8 sb = pack8(S[et], s2);
; #pragma unroll
;                 for (int tt = 0; tt < 2; ++tt) {
;                     const bf16x8 aq = ld2x64(qb8 + 32 * tt * QS + (32 * et + 16 * s2) * 2);
;                     O[tt] = __builtin_amdgcn_mfma_f32_32x32x16_bf16(aq, sb, O[tt], 0, 0, 0);
;                 }
;             }
;         __syncthreads();
; #pragma unroll
;         for (int pr = 0; pr < 3; ++pr) {
;             const int st = (pr == 2) ? 1 : 0, tt = (pr == 0) ? 0 : 1;
; #pragma unroll
;             for (int s2 = 0; s2 < 2; ++s2) {
;                 const bf16x8 ax = *(const LAS bf16x8*)(frb + (pr * 2 + s2) * 1024);
;                 const LAS unsigned char* vp = vP + (32 * st + 16 * s2) * VS;
;                 const bf16x8 bv = tr8(vp, vp + 8 * VS);
;                 O[tt] = __builtin_amdgcn_mfma_f32_32x32x16_bf16(ax, bv, O[tt], 0, 0, 0);
;             }
;         }
;         __builtin_amdgcn_sched_barrier(0);
; #pragma unroll
;         for (int tt = 0; tt < 2; ++tt)
; #pragma unroll
;             for (int r = 0; r < 16; ++r) ob[(32 * tt + (r & 3) + 8 * (r >> 2)) * OS] = O[tt][r];
;         __builtin_amdgcn_sched_barrier(0);
; #pragma unroll
;         for (int et = 0; et < 4; ++et)
; #pragma unroll
;             for (int rg = 0; rg < 4; ++rg) { const f32x4 dl = *(const LAS f32x4*)&decb[32 * et + 8 * rg];
.LBB0_646:
	v_add_u32_e32 v222, v203, v202
	ds_read2_b64 v[64:67], v222 offset1:2
	v_cvt_pk_bf16_f32 v68, v32, v33
	v_cvt_pk_bf16_f32 v69, v34, v35
	v_cvt_pk_bf16_f32 v70, v36, v37
	v_cvt_pk_bf16_f32 v71, v38, v39
	v_add_u32_e32 v223, 0x2000, v222
	ds_read2_b64 v[228:231], v222 offset0:4 offset1:6
	v_cvt_pk_bf16_f32 v232, v40, v41
	v_cvt_pk_bf16_f32 v233, v42, v43
	s_waitcnt lgkmcnt(1)
	v_mfma_f32_32x32x16_bf16 v[80:95], v[64:67], v[68:71], 0
	ds_read2_b64 v[64:67], v223 offset0:64 offset1:66
	v_cvt_pk_bf16_f32 v234, v44, v45
	v_cvt_pk_bf16_f32 v235, v46, v47
	s_waitcnt lgkmcnt(1)
	s_nop 0
	v_mfma_f32_32x32x16_bf16 v[80:95], v[228:231], v[232:235], v[80:95]
	ds_read2_b64 v[228:231], v223 offset0:68 offset1:70
	s_waitcnt lgkmcnt(1)
	v_mfma_f32_32x32x16_bf16 v[64:79], v[64:67], v[68:71], 0
	s_waitcnt lgkmcnt(0)
	v_mfma_f32_32x32x16_bf16 v[64:79], v[228:231], v[232:235], v[64:79]
	ds_read2_b64 v[228:231], v222 offset0:8 offset1:10
	v_cvt_pk_bf16_f32 v232, v16, v17
	v_cvt_pk_bf16_f32 v233, v18, v19
	v_cvt_pk_bf16_f32 v234, v20, v21
	v_cvt_pk_bf16_f32 v235, v22, v23
	s_waitcnt lgkmcnt(0)
	s_nop 0
	v_mfma_f32_32x32x16_bf16 v[80:95], v[228:231], v[232:235], v[80:95]
	ds_read2_b64 v[228:231], v223 offset0:72 offset1:74
	s_waitcnt lgkmcnt(0)
	v_mfma_f32_32x32x16_bf16 v[64:79], v[228:231], v[232:235], v[64:79]
	ds_read2_b64 v[228:231], v222 offset0:12 offset1:14
	v_cvt_pk_bf16_f32 v232, v24, v25
	v_cvt_pk_bf16_f32 v233, v26, v27
	v_cvt_pk_bf16_f32 v234, v28, v29
	v_cvt_pk_bf16_f32 v235, v30, v31
	s_waitcnt lgkmcnt(0)
	s_nop 0
	v_mfma_f32_32x32x16_bf16 v[80:95], v[228:231], v[232:235], v[80:95]
	ds_read2_b64 v[228:231], v223 offset0:76 offset1:78
	s_waitcnt lgkmcnt(0)
	v_mfma_f32_32x32x16_bf16 v[64:79], v[228:231], v[232:235], v[64:79]
	ds_read2_b64 v[228:231], v222 offset0:16 offset1:18
	v_cvt_pk_bf16_f32 v232, v48, v49
	v_cvt_pk_bf16_f32 v233, v50, v51
	v_cvt_pk_bf16_f32 v234, v52, v53
	v_cvt_pk_bf16_f32 v235, v54, v55
	s_waitcnt lgkmcnt(0)
	s_nop 0
	v_mfma_f32_32x32x16_bf16 v[80:95], v[228:231], v[232:235], v[80:95]
	ds_read2_b64 v[228:231], v223 offset0:80 offset1:82
	s_waitcnt lgkmcnt(0)
	v_mfma_f32_32x32x16_bf16 v[64:79], v[228:231], v[232:235], v[64:79]
	ds_read2_b64 v[228:231], v222 offset0:20 offset1:22
	v_cvt_pk_bf16_f32 v232, v56, v57
	v_cvt_pk_bf16_f32 v233, v58, v59
	v_cvt_pk_bf16_f32 v234, v60, v61
	v_cvt_pk_bf16_f32 v235, v62, v63
	s_waitcnt lgkmcnt(0)
	s_nop 0
	v_mfma_f32_32x32x16_bf16 v[80:95], v[228:231], v[232:235], v[80:95]
	ds_read2_b64 v[228:231], v223 offset0:84 offset1:86
	s_waitcnt lgkmcnt(0)
	v_mfma_f32_32x32x16_bf16 v[64:79], v[228:231], v[232:235], v[64:79]
	ds_read2_b64 v[228:231], v222 offset0:24 offset1:26
	v_cvt_pk_bf16_f32 v232, v0, v1
	v_cvt_pk_bf16_f32 v233, v2, v3
	v_cvt_pk_bf16_f32 v234, v4, v5
	v_cvt_pk_bf16_f32 v235, v6, v7
	s_waitcnt lgkmcnt(0)
	s_nop 0
	v_mfma_f32_32x32x16_bf16 v[80:95], v[228:231], v[232:235], v[80:95]
	ds_read2_b64 v[228:231], v223 offset0:88 offset1:90
	s_waitcnt lgkmcnt(0)
	v_mfma_f32_32x32x16_bf16 v[64:79], v[228:231], v[232:235], v[64:79]
	ds_read2_b64 v[228:231], v222 offset0:28 offset1:30
	v_cvt_pk_bf16_f32 v232, v8, v9
	v_cvt_pk_bf16_f32 v233, v10, v11
	v_cvt_pk_bf16_f32 v234, v12, v13
	v_cvt_pk_bf16_f32 v235, v14, v15
	s_waitcnt lgkmcnt(0)
	s_nop 0
	v_mfma_f32_32x32x16_bf16 v[80:95], v[228:231], v[232:235], v[80:95]
	ds_read2_b64 v[228:231], v223 offset0:92 offset1:94
	s_waitcnt lgkmcnt(0)
	s_barrier
	v_mfma_f32_32x32x16_bf16 v[64:79], v[228:231], v[232:235], v[64:79]
	ds_read_b128 v[228:231], v206
	ds_read_b64_tr_b16 v[232:233], v218
	ds_read_b64_tr_b16 v[234:235], v218 offset:4608
	ds_read_b128 v[236:239], v206 offset:1024
	ds_read_b64_tr_b16 v[240:241], v218 offset:9216
	ds_read_b64_tr_b16 v[242:243], v218 offset:13824
	s_waitcnt lgkmcnt(3)
	v_mfma_f32_32x32x16_bf16 v[80:95], v[228:231], v[232:235], v[80:95]
	s_waitcnt lgkmcnt(0)
	v_mfma_f32_32x32x16_bf16 v[80:95], v[236:239], v[240:243], v[80:95]
	ds_read_b128 v[228:231], v206 offset:2048
	ds_read_b128 v[236:239], v206 offset:3072
	s_waitcnt lgkmcnt(1)
	v_mfma_f32_32x32x16_bf16 v[64:79], v[228:231], v[232:235], v[64:79]
	s_waitcnt lgkmcnt(0)
	v_mfma_f32_32x32x16_bf16 v[64:79], v[236:239], v[240:243], v[64:79]
	ds_read_b128 v[228:231], v206 offset:4096
	ds_read_b64_tr_b16 v[232:233], v218 offset:18432
	ds_read_b64_tr_b16 v[234:235], v218 offset:23040
	ds_read_b128 v[236:239], v206 offset:5120
	ds_read_b64_tr_b16 v[240:241], v218 offset:27648
	ds_read_b64_tr_b16 v[242:243], v218 offset:32256
	s_waitcnt lgkmcnt(3)
	v_mfma_f32_32x32x16_bf16 v[64:79], v[228:231], v[232:235], v[64:79]
	s_waitcnt lgkmcnt(0)
	v_mfma_f32_32x32x16_bf16 v[64:79], v[236:239], v[240:243], v[64:79]
	ds_write_b32 v207, v80
	ds_write_b32 v207, v81 offset:1040
	ds_write_b32 v207, v82 offset:2080
	ds_write_b32 v207, v83 offset:3120
	ds_write_b32 v207, v84 offset:8320
	ds_write_b32 v207, v85 offset:9360
	ds_write_b32 v207, v86 offset:10400
	ds_write_b32 v207, v87 offset:11440
	ds_write_b32 v207, v88 offset:16640
	ds_write_b32 v207, v89 offset:17680
	ds_write_b32 v207, v90 offset:18720
	ds_write_b32 v207, v91 offset:19760
	ds_write_b32 v207, v92 offset:24960
	ds_write_b32 v207, v93 offset:26000
	ds_write_b32 v207, v94 offset:27040
	ds_write_b32 v207, v95 offset:28080
	ds_write_b32 v207, v64 offset:33280
	ds_write_b32 v207, v65 offset:34320
	ds_write_b32 v207, v66 offset:35360
	ds_write_b32 v207, v67 offset:36400
	ds_write_b32 v207, v68 offset:41600
	ds_write_b32 v207, v69 offset:42640
	ds_write_b32 v207, v70 offset:43680
	ds_write_b32 v207, v71 offset:44720
	ds_write_b32 v207, v72 offset:49920
	ds_write_b32 v207, v73 offset:50960
	ds_write_b32 v207, v74 offset:52000
	ds_write_b32 v207, v75 offset:53040
	ds_write_b32 v207, v76 offset:58240
	ds_write_b32 v207, v77 offset:59280
	ds_write_b32 v207, v78 offset:60320
	ds_write_b32 v207, v79 offset:61360
	ds_read_b128 v[64:67], v205
	ds_read_b128 v[68:71], v205 offset:32
	ds_read_b128 v[72:75], v205 offset:64
	ds_read_b128 v[76:79], v205 offset:96
	s_waitcnt vmcnt(11)
; #define LAS __attribute__((address_space(3)))
; __device__ __forceinline__ void gla_unit(LAS unsigned char* lds, const unsigned char* ws, const float* g_onorm, const int b, const int h, const int wv) {
;     ...
; #pragma unroll
;         for (int et = 0; et < 4; ++et)
; #pragma unroll
;             for (int rg = 0; rg < 4; ++rg) { const f32x4 dl = *(const LAS f32x4*)&decb[32 * et + 8 * rg];
; #pragma unroll
;                 for (int x = 0; x < 4; ++x) S[et][4 * rg + x] *= dl[x]; }
; #pragma unroll
;         for (int ks = 0; ks < 4; ++ks) {
;             const LAS unsigned char* vp = vN + 16 * ks * VS;
;             const bf16x8 bv = tr8(vp, vp + 4 * VS);
; #pragma unroll
;             for (int et = 0; et < 4; ++et) {
;                 const LAS unsigned char* kp = keN + 32 * et * 2 + 16 * ks * ES;
;                 const bf16x8 ak = tr8(kp, kp + 4 * ES);
;                 S[et] = __builtin_amdgcn_mfma_f32_32x32x16_bf16(ak, bv, S[et], 0, 0, 0);
;             }
;         }
	v_lshlrev_b32_e32 v246, 16, v176
	s_waitcnt lgkmcnt(3)
	v_pk_mul_f32 v[34:35], v[34:35], v[66:67]
	s_waitcnt lgkmcnt(2)
	v_pk_mul_f32 v[38:39], v[38:39], v[70:71]
	s_waitcnt lgkmcnt(1)
	v_pk_mul_f32 v[42:43], v[42:43], v[74:75]
	s_waitcnt lgkmcnt(0)
	v_pk_mul_f32 v[46:47], v[46:47], v[78:79]
	v_pk_mul_f32 v[44:45], v[44:45], v[76:77]
	v_pk_mul_f32 v[40:41], v[40:41], v[72:73]
	v_pk_mul_f32 v[36:37], v[36:37], v[68:69]
	v_pk_mul_f32 v[32:33], v[32:33], v[64:65]
	ds_read_b128 v[64:67], v205 offset:128
	ds_read_b128 v[68:71], v205 offset:160
	ds_read_b128 v[72:75], v205 offset:192
	ds_read_b128 v[76:79], v205 offset:224
	v_and_b32_e32 v247, 0xffff0000, v176
	s_waitcnt lgkmcnt(3)
	v_pk_mul_f32 v[18:19], v[18:19], v[66:67]
	s_waitcnt lgkmcnt(2)
	v_pk_mul_f32 v[22:23], v[22:23], v[70:71]
	s_waitcnt lgkmcnt(1)
	v_pk_mul_f32 v[26:27], v[26:27], v[74:75]
	s_waitcnt lgkmcnt(0)
	v_pk_mul_f32 v[30:31], v[30:31], v[78:79]
	v_pk_mul_f32 v[28:29], v[28:29], v[76:77]
	v_pk_mul_f32 v[24:25], v[24:25], v[72:73]
	v_pk_mul_f32 v[20:21], v[20:21], v[68:69]
	v_pk_mul_f32 v[16:17], v[16:17], v[64:65]
	ds_read_b128 v[64:67], v205 offset:256
	ds_read_b128 v[68:71], v205 offset:288
	ds_read_b128 v[72:75], v205 offset:320
	ds_read_b128 v[76:79], v205 offset:352
	v_lshlrev_b32_e32 v176, 16, v177
	s_waitcnt lgkmcnt(3)
	v_pk_mul_f32 v[50:51], v[50:51], v[66:67]
	s_waitcnt lgkmcnt(2)
	v_pk_mul_f32 v[54:55], v[54:55], v[70:71]
	s_waitcnt lgkmcnt(1)
	v_pk_mul_f32 v[58:59], v[58:59], v[74:75]
	s_waitcnt lgkmcnt(0)
	v_pk_mul_f32 v[62:63], v[62:63], v[78:79]
	v_pk_mul_f32 v[60:61], v[60:61], v[76:77]
	v_pk_mul_f32 v[56:57], v[56:57], v[72:73]
	v_pk_mul_f32 v[52:53], v[52:53], v[68:69]
	v_pk_mul_f32 v[48:49], v[48:49], v[64:65]
	ds_read_b128 v[64:67], v205 offset:384
	ds_read_b128 v[68:71], v205 offset:416
	ds_read_b128 v[72:75], v205 offset:448
	ds_read_b128 v[76:79], v205 offset:480
	v_and_b32_e32 v177, 0xffff0000, v177
	s_waitcnt lgkmcnt(3)
	v_pk_mul_f32 v[2:3], v[2:3], v[66:67]
	s_waitcnt lgkmcnt(2)
	v_pk_mul_f32 v[6:7], v[6:7], v[70:71]
	v_pk_mul_f32 v[4:5], v[4:5], v[68:69]
	v_pk_mul_f32 v[0:1], v[0:1], v[64:65]
	ds_read_b64_tr_b16 v[64:65], v219
	ds_read_b64_tr_b16 v[66:67], v219 offset:2304
	ds_read_b64_tr_b16 v[68:69], v220
	ds_read_b64_tr_b16 v[70:71], v220 offset:1280
	s_waitcnt lgkmcnt(0)
	v_mfma_f32_32x32x16_bf16 v[32:47], v[68:71], v[64:67], v[32:47]
	ds_read_b64_tr_b16 v[68:69], v220 offset:64
	ds_read_b64_tr_b16 v[70:71], v220 offset:1344
	v_mul_f32_e64 v14, v14, v78
	v_mul_f32_e64 v15, v15, v79
	v_mul_f32_e64 v10, v10, v74
	v_mul_f32_e64 v11, v11, v75
	v_pk_mul_f32 v[12:13], v[12:13], v[76:77]
	v_pk_mul_f32 v[8:9], v[8:9], v[72:73]
	s_waitcnt lgkmcnt(0)
	v_mfma_f32_32x32x16_bf16 v[16:31], v[68:71], v[64:67], v[16:31]
	ds_read_b64_tr_b16 v[68:69], v220 offset:128
	ds_read_b64_tr_b16 v[70:71], v220 offset:1408
	s_waitcnt lgkmcnt(0)
	v_mfma_f32_32x32x16_bf16 v[48:63], v[68:71], v[64:67], v[48:63]
	ds_read_b64_tr_b16 v[68:69], v220 offset:192
	ds_read_b64_tr_b16 v[70:71], v220 offset:1472
	s_waitcnt lgkmcnt(0)
	v_mfma_f32_32x32x16_bf16 v[0:15], v[68:71], v[64:67], v[0:15]
	ds_read_b64_tr_b16 v[64:65], v219 offset:9216
	ds_read_b64_tr_b16 v[66:67], v219 offset:11520
	ds_read_b64_tr_b16 v[68:69], v220 offset:5120
	ds_read_b64_tr_b16 v[70:71], v220 offset:6400
	s_waitcnt lgkmcnt(0)
	v_mfma_f32_32x32x16_bf16 v[32:47], v[68:71], v[64:67], v[32:47]
	ds_read_b64_tr_b16 v[68:69], v220 offset:5184
	ds_read_b64_tr_b16 v[70:71], v220 offset:6464
	s_waitcnt lgkmcnt(0)
	v_mfma_f32_32x32x16_bf16 v[16:31], v[68:71], v[64:67], v[16:31]
	ds_read_b64_tr_b16 v[68:69], v220 offset:5248
	ds_read_b64_tr_b16 v[70:71], v220 offset:6528
	s_waitcnt lgkmcnt(0)
	v_mfma_f32_32x32x16_bf16 v[48:63], v[68:71], v[64:67], v[48:63]
	ds_read_b64_tr_b16 v[68:69], v220 offset:5312
	ds_read_b64_tr_b16 v[70:71], v220 offset:6592
	s_waitcnt lgkmcnt(0)
	v_mfma_f32_32x32x16_bf16 v[0:15], v[68:71], v[64:67], v[0:15]
	ds_read_b64_tr_b16 v[64:65], v219 offset:18432
	ds_read_b64_tr_b16 v[66:67], v219 offset:20736
	ds_read_b64_tr_b16 v[68:69], v220 offset:10240
	ds_read_b64_tr_b16 v[70:71], v220 offset:11520
	s_waitcnt lgkmcnt(0)
	v_mfma_f32_32x32x16_bf16 v[32:47], v[68:71], v[64:67], v[32:47]
	ds_read_b64_tr_b16 v[68:69], v220 offset:10304
	ds_read_b64_tr_b16 v[70:71], v220 offset:11584
	s_waitcnt lgkmcnt(0)
	v_mfma_f32_32x32x16_bf16 v[16:31], v[68:71], v[64:67], v[16:31]
	ds_read_b64_tr_b16 v[68:69], v220 offset:10368
	ds_read_b64_tr_b16 v[70:71], v220 offset:11648
	s_waitcnt lgkmcnt(0)
	v_mfma_f32_32x32x16_bf16 v[48:63], v[68:71], v[64:67], v[48:63]
	ds_read_b64_tr_b16 v[68:69], v220 offset:10432
	ds_read_b64_tr_b16 v[70:71], v220 offset:11712
	s_waitcnt lgkmcnt(0)
	v_mfma_f32_32x32x16_bf16 v[0:15], v[68:71], v[64:67], v[0:15]
	ds_read_b64_tr_b16 v[64:65], v219 offset:27648
	ds_read_b64_tr_b16 v[66:67], v219 offset:29952
	ds_read_b64_tr_b16 v[68:69], v220 offset:15360
	ds_read_b64_tr_b16 v[70:71], v220 offset:16640
	s_waitcnt lgkmcnt(0)
	v_mfma_f32_32x32x16_bf16 v[32:47], v[68:71], v[64:67], v[32:47]
	ds_read_b64_tr_b16 v[68:69], v220 offset:15424
	ds_read_b64_tr_b16 v[70:71], v220 offset:16704
	s_waitcnt lgkmcnt(0)
	v_mfma_f32_32x32x16_bf16 v[16:31], v[68:71], v[64:67], v[16:31]
	ds_read_b64_tr_b16 v[68:69], v220 offset:15488
	ds_read_b64_tr_b16 v[70:71], v220 offset:16768
	s_waitcnt lgkmcnt(0)
	v_mfma_f32_32x32x16_bf16 v[48:63], v[68:71], v[64:67], v[48:63]
	ds_read_b64_tr_b16 v[68:69], v220 offset:15552
	ds_read_b64_tr_b16 v[70:71], v220 offset:16832
	s_waitcnt lgkmcnt(0)
	s_barrier
; #define LAS __attribute__((address_space(3)))
; __device__ __forceinline__ unsigned cvt_pk_bf16(float lo, float hi) { const bf16x2_t r = __builtin_convertvector((f32x2_t){lo, hi}, bf16x2_t); return __builtin_bit_cast(unsigned, r); }
; __device__ __forceinline__ float bf_lo(unsigned w) { return __uint_as_float(w << 16); }
; __device__ __forceinline__ float bf_hi(unsigned w) { return __uint_as_float(w & 0xffff0000u); }
; __device__ __forceinline__ void gla_unit(LAS unsigned char* lds, const unsigned char* ws, const float* g_onorm, const int b, const int h, const int wv) {
;     ...
;         {
;             const int t = tid >> 3, g8 = tid & 7;
;             float ov[32]; float ss = 0.f;
; #pragma unroll
;             for (int x = 0; x < 8; ++x) { const f32x4 v = *(const LAS f32x4*)&obuf[t * OS + 32 * g8 + 4 * x]; ov[4 * x] = v[0]; ov[4 * x + 1] = v[1]; ov[4 * x + 2] = v[2]; ov[4 * x + 3] = v[3];
;                 ss += v[0] * v[0] + v[1] * v[1] + v[2] * v[2] + v[3] * v[3]; }
;             ss += __builtin_bit_cast(float, __builtin_amdgcn_ds_swizzle(__builtin_bit_cast(int, ss), (1 << 10) | 0x1F)); ss += __builtin_bit_cast(float, __builtin_amdgcn_ds_swizzle(__builtin_bit_cast(int, ss), (2 << 10) | 0x1F));
;             ss += __builtin_bit_cast(float, __builtin_amdgcn_ds_swizzle(__builtin_bit_cast(int, ss), (4 << 10) | 0x1F));
;             const float rstd = __builtin_amdgcn_rsqf(ss * (1.0f / 256.0f) + EPSV);
;             bf16_t* mp = mix + (t0 + t) * DM + 1024 + h * 256 + 32 * g8;
; #pragma unroll
;             for (int x = 0; x < 4; ++x) {
;                 const u32x4 og = ogr[x];
;                 const f32x4 g0 = *(const LAS f32x4*)&gon[32 * g8 + 8 * x], g1 = *(const LAS f32x4*)&gon[32 * g8 + 8 * x + 4];
;                 const float gg2[8] = {g0[0], g0[1], g0[2], g0[3], g1[0], g1[1], g1[2], g1[3]};
;                 float res[8];
; #pragma unroll
;                 for (int y = 0; y < 4; ++y) { const float a0 = bf_lo(og[y]), a1 = bf_hi(og[y]);
;                     res[2 * y] = ov[8 * x + 2 * y] * rstd * gg2[2 * y] * a0;
;                     res[2 * y + 1] = ov[8 * x + 2 * y + 1] * rstd * gg2[2 * y + 1] * a1; }
;                 u32x4 wv4; wv4[0] = cvt_pk_bf16(res[0], res[1]); wv4[1] = cvt_pk_bf16(res[2], res[3]); wv4[2] = cvt_pk_bf16(res[4], res[5]); wv4[3] = cvt_pk_bf16(res[6], res[7]);
;                 *(u32x4*)(mp + 8 * x) = wv4;
	v_mfma_f32_32x32x16_bf16 v[0:15], v[68:71], v[64:67], v[0:15]
	ds_read_b128 v[64:67], v221
	ds_read_b128 v[68:71], v221 offset:16
	ds_read_b128 v[72:75], v221 offset:32
	ds_read_b128 v[76:79], v221 offset:48
	s_waitcnt lgkmcnt(3)
	v_mul_f32_e32 v80, v65, v65
	s_waitcnt lgkmcnt(2)
	v_mul_f32_e32 v81, v69, v69
	v_fmac_f32_e32 v80, v64, v64
	v_fmac_f32_e32 v81, v68, v68
	v_fmac_f32_e32 v80, v66, v66
	v_fmac_f32_e32 v81, v70, v70
	v_fmac_f32_e32 v80, v67, v67
	v_fmac_f32_e32 v81, v71, v71
	s_waitcnt lgkmcnt(1)
	v_mov_b32_e32 v82, v73
	s_waitcnt lgkmcnt(0)
	v_mov_b32_e32 v83, v77
	v_add_f32_e32 v84, v80, v81
	v_mov_b32_e32 v80, v72
	v_mov_b32_e32 v81, v76
	v_pk_mul_f32 v[82:83], v[82:83], v[82:83]
	s_nop 0
	v_pk_fma_f32 v[80:81], v[80:81], v[80:81], v[82:83]
	v_mov_b32_e32 v82, v74
	v_mov_b32_e32 v83, v78
	v_pk_fma_f32 v[80:81], v[82:83], v[82:83], v[80:81]
	v_mov_b32_e32 v82, v75
	v_mov_b32_e32 v83, v79
	v_pk_fma_f32 v[80:81], v[82:83], v[82:83], v[80:81]
	s_nop 0
	v_add_f32_e32 v80, v84, v80
	v_add_f32_e32 v92, v80, v81
	ds_read_b128 v[80:83], v221 offset:64
	ds_read_b128 v[84:87], v221 offset:80
	s_waitcnt lgkmcnt(1)
	v_mov_b32_e32 v90, v81
	s_waitcnt lgkmcnt(0)
	v_mov_b32_e32 v91, v85
	v_mov_b32_e32 v88, v80
	v_mov_b32_e32 v89, v84
	v_pk_mul_f32 v[90:91], v[90:91], v[90:91]
	s_nop 0
	v_pk_fma_f32 v[88:89], v[88:89], v[88:89], v[90:91]
	v_mov_b32_e32 v90, v82
	v_mov_b32_e32 v91, v86
	v_pk_fma_f32 v[88:89], v[90:91], v[90:91], v[88:89]
	v_mov_b32_e32 v90, v83
	v_mov_b32_e32 v91, v87
	v_pk_fma_f32 v[88:89], v[90:91], v[90:91], v[88:89]
	s_nop 0
	v_add_f32_e32 v88, v92, v88
	v_add_f32_e32 v227, v88, v89
	ds_read_b128 v[88:91], v221 offset:96
	ds_read_b128 v[92:95], v221 offset:112
	s_waitcnt lgkmcnt(1)
	v_mov_b32_e32 v228, v89
	s_waitcnt lgkmcnt(0)
	v_mov_b32_e32 v229, v93
	v_mov_b32_e32 v200, v88
	v_mov_b32_e32 v201, v92
	v_pk_mul_f32 v[228:229], v[228:229], v[228:229]
	s_nop 0
	v_pk_fma_f32 v[200:201], v[200:201], v[200:201], v[228:229]
	v_mov_b32_e32 v228, v90
	v_mov_b32_e32 v229, v94
	v_pk_fma_f32 v[200:201], v[228:229], v[228:229], v[200:201]
	v_mov_b32_e32 v228, v91
	v_mov_b32_e32 v229, v95
	v_pk_fma_f32 v[200:201], v[228:229], v[228:229], v[200:201]
	ds_read_b128 v[228:231], v208
	ds_read_b128 v[232:235], v208 offset:16
	ds_read_b128 v[236:239], v208 offset:32
	ds_read_b128 v[240:243], v208 offset:48
	v_add_f32_e32 v200, v227, v200
	v_add_f32_e32 v200, v200, v201
	ds_swizzle_b32 v201, v200 offset:swizzle(SWAP,1)
	s_waitcnt lgkmcnt(0)
	v_add_f32_e32 v200, v200, v201
	ds_swizzle_b32 v201, v200 offset:swizzle(SWAP,2)
	s_waitcnt lgkmcnt(0)
	v_add_f32_e32 v200, v200, v201
	ds_swizzle_b32 v201, v200 offset:swizzle(SWAP,4)
	s_waitcnt lgkmcnt(0)
	v_add_f32_e32 v200, v200, v201
	v_fmamk_f32 v200, v200, 0x3b800000, v181
	v_rsq_f32_e32 v244, v200
	v_lshl_add_u64 v[200:201], s[76:77], 0, v[188:189]
	v_pk_mul_f32 v[66:67], v[66:67], v[244:245] op_sel_hi:[1,0]
	s_nop 0
	v_pk_mul_f32 v[66:67], v[230:231], v[66:67]
	v_pk_mul_f32 v[68:69], v[68:69], v[244:245] op_sel_hi:[1,0]
	v_pk_mul_f32 v[64:65], v[64:65], v[244:245] op_sel_hi:[1,0]
	v_pk_mul_f32 v[66:67], v[66:67], v[176:177]
	v_lshlrev_b32_e32 v176, 16, v178
	v_and_b32_e32 v177, 0xffff0000, v178
	v_pk_mul_f32 v[68:69], v[232:233], v[68:69]
	v_pk_mul_f32 v[70:71], v[70:71], v[244:245] op_sel_hi:[1,0]
	v_pk_mul_f32 v[64:65], v[228:229], v[64:65]
	v_pk_mul_f32 v[68:69], v[68:69], v[176:177]
	v_lshlrev_b32_e32 v176, 16, v179
	v_and_b32_e32 v177, 0xffff0000, v179
	v_pk_mul_f32 v[70:71], v[234:235], v[70:71]
	v_pk_mul_f32 v[64:65], v[64:65], v[246:247]
	v_pk_mul_f32 v[70:71], v[70:71], v[176:177]
	v_add_co_u32_e32 v176, vcc, s33, v200
	v_cvt_pk_bf16_f32 v64, v64, v65
	v_cvt_pk_bf16_f32 v65, v66, v67
	v_cvt_pk_bf16_f32 v66, v68, v69
	v_cvt_pk_bf16_f32 v67, v70, v71
	v_addc_co_u32_e32 v177, vcc, 0, v201, vcc
	global_store_dwordx4 v[176:177], v[64:67], off offset:2048
	v_pk_mul_f32 v[68:69], v[74:75], v[244:245] op_sel_hi:[1,0]
	v_pk_mul_f32 v[70:71], v[76:77], v[244:245] op_sel_hi:[1,0]
	v_pk_mul_f32 v[66:67], v[72:73], v[244:245] op_sel_hi:[1,0]
	s_waitcnt vmcnt(9)
; #define LAS __attribute__((address_space(3)))
; __device__ __forceinline__ unsigned cvt_pk_bf16(float lo, float hi) { const bf16x2_t r = __builtin_convertvector((f32x2_t){lo, hi}, bf16x2_t); return __builtin_bit_cast(unsigned, r); }
; __device__ __forceinline__ float bf_lo(unsigned w) { return __uint_as_float(w << 16); }
; __device__ __forceinline__ float bf_hi(unsigned w) { return __uint_as_float(w & 0xffff0000u); }
; __device__ __forceinline__ void gla_unit(LAS unsigned char* lds, const unsigned char* ws, const float* g_onorm, const int b, const int h, const int wv) {
;     ...
;         __syncthreads();
; #pragma unroll
;         for (int i = 0; i < 2; ++i) { const int c = tid + 512 * i, row = c >> 4, cc = (c & 15) * 16;
;             *(LAS u32x4*)(lds + L_Q + row * QS + cc) = qr[par][i]; *(LAS u32x4*)(lds + L_K + row * QS + cc) = kr[par][i]; }
; #pragma unroll
;         for (int i = 0; i < 4; ++i) { const int c = tid + 512 * i; *(LAS u32x4*)(lds + L_V + (c >> 5) * VS + (c & 31) * 16) = vr[par][i]; }
;         if (tid < 32) {
;             const float L2E_ = 1.4426950408889634f;
;             *(LAS f32x4*)&dec[tid * 4] = (f32x4){__builtin_amdgcn_exp2f(dr[0] * L2E_), __builtin_amdgcn_exp2f(dr[1] * L2E_), __builtin_amdgcn_exp2f(dr[2] * L2E_), __builtin_amdgcn_exp2f(dr[3] * L2E_)};
;         }
;     ...
; #pragma unroll
;             for (int x = 0; x < 4; ++x) {
;                 const u32x4 og = ogr[x];
;                 const f32x4 g0 = *(const LAS f32x4*)&gon[32 * g8 + 8 * x], g1 = *(const LAS f32x4*)&gon[32 * g8 + 8 * x + 4];
;                 const float gg2[8] = {g0[0], g0[1], g0[2], g0[3], g1[0], g1[1], g1[2], g1[3]};
;                 float res[8];
; #pragma unroll
;                 for (int y = 0; y < 4; ++y) { const float a0 = bf_lo(og[y]), a1 = bf_hi(og[y]);
;                     res[2 * y] = ov[8 * x + 2 * y] * rstd * gg2[2 * y] * a0;
;                     res[2 * y + 1] = ov[8 * x + 2 * y + 1] * rstd * gg2[2 * y + 1] * a1; }
;                 u32x4 wv4; wv4[0] = cvt_pk_bf16(res[0], res[1]); wv4[1] = cvt_pk_bf16(res[2], res[3]); wv4[2] = cvt_pk_bf16(res[4], res[5]); wv4[3] = cvt_pk_bf16(res[6], res[7]);
;                 *(u32x4*)(mp + 8 * x) = wv4;
;             }
	v_lshlrev_b32_e32 v64, 16, v172
	v_and_b32_e32 v65, 0xffff0000, v172
	v_pk_mul_f32 v[66:67], v[236:237], v[66:67]
	v_pk_mul_f32 v[68:69], v[238:239], v[68:69]
	v_pk_mul_f32 v[64:65], v[66:67], v[64:65]
	v_lshlrev_b32_e32 v66, 16, v173
	v_and_b32_e32 v67, 0xffff0000, v173
	v_pk_mul_f32 v[66:67], v[68:69], v[66:67]
	v_lshlrev_b32_e32 v68, 16, v174
	v_and_b32_e32 v69, 0xffff0000, v174
	v_pk_mul_f32 v[70:71], v[240:241], v[70:71]
	v_pk_mul_f32 v[72:73], v[78:79], v[244:245] op_sel_hi:[1,0]
	v_pk_mul_f32 v[68:69], v[70:71], v[68:69]
	v_lshlrev_b32_e32 v70, 16, v175
	v_and_b32_e32 v71, 0xffff0000, v175
	v_pk_mul_f32 v[72:73], v[242:243], v[72:73]
	v_cvt_pk_bf16_f32 v64, v64, v65
	v_pk_mul_f32 v[70:71], v[72:73], v[70:71]
	v_cvt_pk_bf16_f32 v65, v66, v67
	v_cvt_pk_bf16_f32 v66, v68, v69
	v_cvt_pk_bf16_f32 v67, v70, v71
	global_store_dwordx4 v[176:177], v[64:67], off offset:2064
	ds_read_b128 v[64:67], v208 offset:64
	ds_read_b128 v[68:71], v208 offset:80
	v_pk_mul_f32 v[74:75], v[80:81], v[244:245] op_sel_hi:[1,0]
	v_lshlrev_b32_e32 v72, 16, v168
	v_and_b32_e32 v73, 0xffff0000, v168
	s_waitcnt lgkmcnt(1)
	v_pk_mul_f32 v[64:65], v[64:65], v[74:75]
	v_pk_mul_f32 v[74:75], v[82:83], v[244:245] op_sel_hi:[1,0]
	v_pk_mul_f32 v[64:65], v[64:65], v[72:73]
	v_lshlrev_b32_e32 v72, 16, v169
	v_and_b32_e32 v73, 0xffff0000, v169
	v_pk_mul_f32 v[66:67], v[66:67], v[74:75]
	v_pk_mul_f32 v[74:75], v[84:85], v[244:245] op_sel_hi:[1,0]
	v_pk_mul_f32 v[66:67], v[66:67], v[72:73]
	v_lshlrev_b32_e32 v72, 16, v170
	v_and_b32_e32 v73, 0xffff0000, v170
	s_waitcnt lgkmcnt(0)
	v_pk_mul_f32 v[68:69], v[68:69], v[74:75]
	v_pk_mul_f32 v[74:75], v[86:87], v[244:245] op_sel_hi:[1,0]
	v_pk_mul_f32 v[68:69], v[68:69], v[72:73]
	v_lshlrev_b32_e32 v72, 16, v171
	v_and_b32_e32 v73, 0xffff0000, v171
	v_pk_mul_f32 v[70:71], v[70:71], v[74:75]
	v_cvt_pk_bf16_f32 v64, v64, v65
	v_pk_mul_f32 v[70:71], v[70:71], v[72:73]
	v_cvt_pk_bf16_f32 v65, v66, v67
	v_cvt_pk_bf16_f32 v66, v68, v69
	v_cvt_pk_bf16_f32 v67, v70, v71
	global_store_dwordx4 v[176:177], v[64:67], off offset:2080
	ds_read_b128 v[64:67], v208 offset:96
	ds_read_b128 v[68:71], v208 offset:112
	v_pk_mul_f32 v[74:75], v[88:89], v[244:245] op_sel_hi:[1,0]
	v_lshlrev_b32_e32 v72, 16, v164
	v_and_b32_e32 v73, 0xffff0000, v164
	s_waitcnt lgkmcnt(1)
	v_pk_mul_f32 v[64:65], v[74:75], v[64:65]
	v_pk_mul_f32 v[74:75], v[90:91], v[244:245] op_sel_hi:[1,0]
	v_pk_mul_f32 v[64:65], v[64:65], v[72:73]
	v_lshlrev_b32_e32 v72, 16, v165
	v_and_b32_e32 v73, 0xffff0000, v165
	v_pk_mul_f32 v[66:67], v[74:75], v[66:67]
	v_pk_mul_f32 v[74:75], v[92:93], v[244:245] op_sel_hi:[1,0]
	v_pk_mul_f32 v[66:67], v[66:67], v[72:73]
	v_lshlrev_b32_e32 v72, 16, v166
	v_and_b32_e32 v73, 0xffff0000, v166
	s_waitcnt lgkmcnt(0)
	v_pk_mul_f32 v[68:69], v[74:75], v[68:69]
	v_pk_mul_f32 v[74:75], v[94:95], v[244:245] op_sel_hi:[1,0]
	v_pk_mul_f32 v[68:69], v[68:69], v[72:73]
	v_lshlrev_b32_e32 v72, 16, v167
	v_and_b32_e32 v73, 0xffff0000, v167
	v_pk_mul_f32 v[70:71], v[74:75], v[70:71]
	v_cvt_pk_bf16_f32 v64, v64, v65
	v_pk_mul_f32 v[70:71], v[70:71], v[72:73]
	v_cvt_pk_bf16_f32 v65, v66, v67
	v_cvt_pk_bf16_f32 v66, v68, v69
	v_cvt_pk_bf16_f32 v67, v70, v71
	global_store_dwordx4 v[176:177], v[64:67], off offset:2096
	s_barrier
	s_waitcnt vmcnt(20)
	ds_write_b128 v209, v[132:135]
	ds_write_b128 v209, v[136:139] offset:17408
	ds_write_b128 v210, v[140:143]
	ds_write_b128 v210, v[144:147] offset:17408
	ds_write_b128 v211, v[148:151]
	ds_write_b128 v212, v[152:155]
	ds_write_b128 v213, v[156:159]
	ds_write_b128 v214, v[160:163]
	s_and_saveexec_b64 s[42:43], s[0:1]
	s_cbranch_execz .LBB0_648
	s_waitcnt vmcnt(12)
	v_mul_f32_e32 v64, 0x3fb8aa3b, v124
	v_mul_f32_e32 v65, 0x3fb8aa3b, v125
	v_mul_f32_e32 v66, 0x3fb8aa3b, v126
	v_mul_f32_e32 v67, 0x3fb8aa3b, v127
	v_exp_f32_e32 v64, v64
	v_exp_f32_e32 v65, v65
	v_exp_f32_e32 v66, v66
	v_exp_f32_e32 v67, v67
	ds_write_b128 v226, v[64:67]

; #define LAS __attribute__((address_space(3)))
; __device__ __forceinline__ int mk_tid(const int wv) { int ln; asm volatile("v_mbcnt_lo_u32_b32 %0, -1, 0\n\tv_mbcnt_hi_u32_b32 %0, -1, %0" : "=v"(ln)); return wv * 64 + ln; }
; #define GLA_LOAD_DR(n) do { if (tid < 32) dr = *(const f32x4*)(BC + ((size_t)b * SEQ + 64 * (n) + 63) * 512 + h * 128 + tid * 4); } while (0)
; __device__ __forceinline__ void gla_unit(LAS unsigned char* lds, const unsigned char* ws, const float* g_onorm, const int b, const int h, const int wv) {
;     int tid = mk_tid(wv); asm volatile("" : "+v"(tid));
;     const int w = __builtin_amdgcn_readfirstlane(tid >> 6), lane = tid & 63, j = lane & 31, hh = lane >> 5;
;     const bf16_t* QG = (const bf16_t*)(ws + WS_QG); const bf16_t* KG = (const bf16_t*)(ws + WS_KG);
;     const bf16_t* VG = (const bf16_t*)(ws + WS_VG); const bf16_t* OG = (const bf16_t*)(ws + WS_OG);
;     const float* BC = (const float*)(ws + WS_LA); bf16_t* mix = (bf16_t*)(ws + WS_MIX);
;     LAS float* dec = (LAS float*)(lds + L_DEC); LAS float* gon = (LAS float*)(lds + L_GON); LAS float* obuf = (LAS float*)(lds + L_OB);
;     f32x16 S[4];
; #pragma unroll
;     for (int et = 0; et < 4; ++et)
; #pragma unroll
;         for (int r = 0; r < 16; ++r) S[et][r] = 0.f;
;     __syncthreads();
;     if (tid < 256) gon[tid] = g_onorm[tid];
;     u32x4 qr[2][2], kr[2][2], vr[2][4], ogr[4]; f32x4 dr = (f32x4){0.f, 0.f, 0.f, 0.f};
;     const unsigned o16 = (unsigned)tid * 16u, oog = (unsigned)tid * 64u;
;     ...
;     const LAS unsigned char* qb8 = lds + L_Q + j * QS + hh * 8;  const LAS unsigned char* qb16 = lds + L_Q + j * QS + hh * 16;
;     const LAS unsigned char* kb16 = lds + L_K + j * QS + hh * 16;
;     const int li = lane & 15, gq = li >> 2, gp = li & 3, gg = (lane >> 4) & 1;
;     const LAS unsigned char* keN = lds + L_KE + (gq + 8 * hh) * ES + (16 * gg + 4 * gp) * 2;
;     const LAS unsigned char* vN = lds + L_V + (gq + 8 * hh) * VS + (32 * w + 16 * gg + 4 * gp) * 2;
;     const LAS unsigned char* vP = lds + L_V + (gq + 4 * hh) * VS + (32 * w + 16 * gg + 4 * gp) * 2;
;     const LAS float* decb = dec + 4 * hh; LAS float* ob = obuf + 4 * hh * OS + 32 * w + j;
;     LAS unsigned char* frb = lds + L_FR + lane * 16;
;     ...
;     GLA_LOAD(0, 0); GLA_LOAD_DR(0); GLA_LOAD(1, 1);
.LBB0_1690:
	s_or_b64 exec, exec, s[4:5]
	v_and_b32_e32 v12, 16, v2
	v_and_or_b32 v12, v4, 12, v12
	v_bfe_u32 v1, v2, 5, 1
	s_ashr_i32 s17, s10, 6
	v_and_b32_e32 v3, 31, v2
	s_movk_i32 s18, 0x110
	v_lshlrev_b32_e32 v14, 1, v12
	s_and_b32 s4, s10, 0xffffffc0
	v_lshlrev_b32_e32 v10, 4, v1
	v_mad_u32_u24 v203, v3, s18, 0
	v_or_b32_e32 v15, s4, v14
	s_lshl_b32 s4, s17, 7
	s_add_i32 s5, 0, 0x1fc00
	v_and_b32_e32 v0, 63, v2
	v_lshlrev_b32_e32 v202, 3, v1
	v_lshlrev_b32_e32 v16, 2, v1
	v_mul_u32_u24_e32 v1, 0x1040, v1
	s_add_i32 s4, s4, 0
	v_add_u32_e32 v204, v203, v10
	v_add_u32_e32 v205, s5, v10
	s_add_i32 s5, 0, 0x1e400
	v_lshlrev_b32_e32 v10, 2, v3
	v_lshl_add_u32 v206, v0, 4, s5
	v_add3_u32 v207, s4, v1, v10
	s_lshl_b64 s[4:5], s[94:95], 11
	s_or_b32 s4, s4, 64
	s_add_i32 s19, 0, 0x15400
	s_add_i32 s21, 0, 0x10400
	s_lshl_b64 s[6:7], s[4:5], 8
	s_add_u32 s8, s15, s6
	v_bfe_u32 v11, v2, 2, 2
	s_addc_u32 s9, s16, s7
	v_or_b32_e32 v13, v202, v11
	v_or_b32_e32 v11, v16, v11
	s_movk_i32 s20, 0x240
	v_mov_b32_e32 v12, s19
	s_add_u32 s6, s13, s6
	v_mad_u32_u24 v17, v11, s20, v12
	s_movk_i32 s22, 0x140
	v_mov_b32_e32 v11, s21
	s_addc_u32 s7, s14, s7
	v_mad_u32_u24 v18, v13, s22, v11
	v_mad_u32_u24 v19, v13, s20, v12
	v_lshl_add_u64 v[10:11], s[8:9], 0, v[180:181]
	v_lshl_add_u64 v[12:13], s[6:7], 0, v[180:181]
	s_movk_i32 s6, 0x2000
	s_lshl_b64 s[4:5], s[4:5], 9
	global_load_dwordx4 v[132:135], v[10:11], off
	global_load_dwordx4 v[136:139], v[12:13], off
	v_add_co_u32_e32 v10, vcc, s6, v10
	s_add_u32 s4, s11, s4
	s_nop 0
	v_addc_co_u32_e32 v11, vcc, 0, v11, vcc
	v_add_co_u32_e32 v12, vcc, s6, v12
	s_addc_u32 s5, s12, s5
	s_nop 0
	v_addc_co_u32_e32 v13, vcc, 0, v13, vcc
	global_load_dwordx4 v[140:143], v[10:11], off
	global_load_dwordx4 v[144:147], v[12:13], off
	v_lshl_add_u64 v[10:11], s[4:5], 0, v[180:181]
	v_add_co_u32_e32 v12, vcc, s6, v10
	s_movk_i32 s4, 0x4000
	s_nop 0
	v_addc_co_u32_e32 v13, vcc, 0, v11, vcc
	global_load_dwordx4 v[148:151], v[10:11], off
	global_load_dwordx4 v[152:155], v[12:13], off
	v_add_co_u32_e32 v12, vcc, s4, v10
	s_movk_i32 s4, 0x6000
	s_nop 0
	v_addc_co_u32_e32 v13, vcc, 0, v11, vcc
	v_add_co_u32_e32 v10, vcc, s4, v10
	s_cmp_lt_i32 s17, 3
	s_nop 0
	v_addc_co_u32_e32 v11, vcc, 0, v11, vcc
	global_load_dwordx4 v[156:159], v[12:13], off
	global_load_dwordx4 v[160:163], v[10:11], off
	v_and_b32_e32 v10, 15, v2
	v_lshlrev_b32_e32 v20, 5, v10
	v_lshl_add_u32 v21, v10, 4, s21
	v_ashrrev_i32_e32 v10, 3, v2
	s_movk_i32 s4, 0x410
	s_cselect_b64 s[46:47], -1, 0
	v_and_b32_e32 v22, 7, v2
	v_mul_lo_u32 v11, v10, s4
	s_add_i32 s4, 0, 0x1fe00
	v_lshlrev_b32_e32 v24, 7, v22
	s_cmp_eq_u32 s17, 2
	v_add_u32_e32 v208, s4, v24
	s_cselect_b64 s[4:5], -1, 0
	s_and_b64 s[6:7], s[4:5], exec
	v_lshlrev_b32_e32 v0, 6, v2
	s_cselect_b32 s67, 0x2200, 0
	s_cmp_gt_u32 s10, 63
	v_ashrrev_i32_e32 v25, 4, v2
	v_add_u32_e32 v27, 0x200, v2
	v_lshrrev_b32_e32 v30, 5, v2
	v_add_u32_e32 v31, 0x400, v2
	v_add_u32_e32 v2, 0x600, v2
	s_cselect_b64 s[6:7], -1, 0
	v_lshrrev_b32_e32 v2, 5, v2
	s_and_b64 s[8:9], s[6:7], exec
	v_mul_lo_u32 v32, v2, s20
	v_or_b32_e32 v2, 2, v16
	v_cmp_gt_u32_e64 s[8:9], v2, v3
	v_or_b32_e32 v2, 3, v16
	v_cmp_gt_u32_e64 s[10:11], v2, v3
	v_or_b32_e32 v2, 8, v16
	v_cmp_gt_u32_e64 s[12:13], v2, v3
	v_or_b32_e32 v2, 9, v16
	v_and_b32_e32 v1, 0xf0, v180
	v_cmp_gt_u32_e64 s[14:15], v2, v3
	v_or_b32_e32 v2, 10, v16
	v_add_u32_e32 v12, 0, v1
	v_and_b32_e32 v1, 0x1f0, v180
	s_cselect_b32 s70, 0x2200, 0
	s_lshl_b32 s71, s17, 11
	v_ashrrev_i32_e32 v28, 4, v27
	v_cmp_gt_u32_e64 s[16:17], v2, v3
	v_or_b32_e32 v2, 11, v16
	v_add_u32_e32 v13, s19, v1
; #define LAS __attribute__((address_space(3)))
; #define GLA_LOAD_DR(n) do { if (tid < 32) dr = *(const f32x4*)(BC + ((size_t)b * SEQ + 64 * (n) + 63) * 512 + h * 128 + tid * 4); } while (0)
; __device__ __forceinline__ void gla_unit(LAS unsigned char* lds, const unsigned char* ws, const float* g_onorm, const int b, const int h, const int wv) {
;     ...
;     f32x16 S[4];
; #pragma unroll
;     for (int et = 0; et < 4; ++et)
; #pragma unroll
;         for (int r = 0; r < 16; ++r) S[et][r] = 0.f;
;     __syncthreads();
;     if (tid < 256) gon[tid] = g_onorm[tid];
;     u32x4 qr[2][2], kr[2][2], vr[2][4], ogr[4]; f32x4 dr = (f32x4){0.f, 0.f, 0.f, 0.f};
;     const unsigned o16 = (unsigned)tid * 16u, oog = (unsigned)tid * 64u;
;     ...
;     const LAS unsigned char* qb8 = lds + L_Q + j * QS + hh * 8;  const LAS unsigned char* qb16 = lds + L_Q + j * QS + hh * 16;
;     const LAS unsigned char* kb16 = lds + L_K + j * QS + hh * 16;
;     const int li = lane & 15, gq = li >> 2, gp = li & 3, gg = (lane >> 4) & 1;
;     const LAS unsigned char* keN = lds + L_KE + (gq + 8 * hh) * ES + (16 * gg + 4 * gp) * 2;
;     const LAS unsigned char* vN = lds + L_V + (gq + 8 * hh) * VS + (32 * w + 16 * gg + 4 * gp) * 2;
;     const LAS unsigned char* vP = lds + L_V + (gq + 4 * hh) * VS + (32 * w + 16 * gg + 4 * gp) * 2;
;     const LAS float* decb = dec + 4 * hh; LAS float* ob = obuf + 4 * hh * OS + 32 * w + j;
;     LAS unsigned char* frb = lds + L_FR + lane * 16;
;     ...
;     GLA_LOAD(0, 0); GLA_LOAD_DR(0); GLA_LOAD(1, 1);
	v_mul_lo_u32 v26, v25, s18
	v_mul_lo_u32 v29, v28, s18
	v_lshrrev_b32_e32 v27, 5, v27
	v_lshrrev_b32_e32 v31, 5, v31
	v_cmp_gt_u32_e64 s[18:19], v2, v3
	v_or_b32_e32 v2, 16, v16
	v_mul_lo_u32 v30, v30, s20
	v_mul_lo_u32 v27, v27, s20
	v_mul_lo_u32 v31, v31, s20
	v_cmp_gt_u32_e64 s[20:21], v2, v3
	v_or_b32_e32 v2, 17, v16
	v_mul_lo_u32 v25, v25, s22
	v_mul_lo_u32 v28, v28, s22
	v_cmp_gt_u32_e64 s[22:23], v2, v3
	v_or_b32_e32 v2, 18, v16
	v_cmp_gt_u32_e64 s[24:25], v2, v3
	v_or_b32_e32 v2, 19, v16
	v_cmp_gt_u32_e64 s[26:27], v2, v3
	v_or_b32_e32 v2, 24, v16
	v_cmp_gt_u32_e64 s[28:29], v2, v3
	v_or_b32_e32 v2, 25, v16
	v_cmp_gt_u32_e64 s[30:31], v2, v3
	v_or_b32_e32 v2, 26, v16
	s_xor_b64 s[4:5], s[6:7], s[4:5]
	v_cmp_gt_u32_e64 s[34:35], v2, v3
	v_or_b32_e32 v2, 27, v16
	v_add_u32_e32 v23, 0, v11
	v_ashrrev_i32_e32 v11, 31, v10
	s_xor_b64 s[48:49], s[4:5], -1
	v_cmp_gt_u32_e64 s[4:5], v16, v3
	v_cmp_lt_u32_e64 s[6:7], v16, v3
	v_cmp_gt_u32_e64 s[36:37], v2, v3
	v_lshl_add_u64 v[2:3], v[8:9], 2, v[6:7]
	v_mov_b32_e32 v1, 0
	v_lshl_add_u64 v[182:183], v[4:5], 2, v[2:3]
	s_lshl_b64 s[2:3], s[2:3], 23
	v_lshlrev_b64 v[2:3], 12, v[10:11]
	v_lshl_add_u64 v[188:189], s[2:3], 0, v[2:3]
	s_lshl_b32 s2, s33, 9
	v_lshlrev_b32_e32 v2, 6, v22
	v_lshl_add_u64 v[190:191], s[38:39], 0, v[0:1]
	v_add_u32_e32 v0, 0, v20
	s_mov_b32 s66, 1
	v_lshl_add_u64 v[184:185], s[38:39], 0, v[180:181]
	v_lshl_add_u64 v[186:187], s[40:41], 0, v[180:181]
	v_or3_b32 v188, v188, s2, v2
	s_mov_b64 s[50:51], 0x4a188000
	v_mov_b32_e32 v181, 0x358637bd
	s_mov_b32 s33, 0x4e188000
	s_mov_b64 s[54:55], 0x4a190000
	s_mov_b32 s72, 0x4e1c8000
	s_mov_b64 s[60:61], 0x40000
	s_mov_b64 s[62:63], 0x10000
	s_mov_b64 s[64:65], 0x8000
	s_mov_b64 s[68:69], 0x80000
	v_add_u32_e32 v209, v12, v26
	v_add_u32_e32 v210, v12, v29
	v_add_u32_e32 v211, v13, v30
	v_add_u32_e32 v212, v13, v27
	v_add_u32_e32 v213, v13, v31
	v_add_u32_e32 v214, v13, v32
	v_add_u32_e32 v215, 0x1fc00, v0
	v_add_u32_e32 v216, v21, v25
	v_add_u32_e32 v217, v21, v28
	v_add_u32_e32 v218, v17, v15
	v_add_u32_e32 v219, v19, v15
	v_add_u32_e32 v220, v18, v14
	v_add_u32_e32 v221, v23, v24
	v_mov_b32_e32 v0, v1
	v_mov_b32_e32 v2, v1
	v_mov_b32_e32 v3, v1
	v_mov_b32_e32 v4, v1
	v_mov_b32_e32 v5, v1
	v_mov_b32_e32 v6, v1
	v_mov_b32_e32 v7, v1
	v_mov_b32_e32 v8, v1
	v_mov_b32_e32 v9, v1
	v_mov_b32_e32 v10, v1
	v_mov_b32_e32 v11, v1
	v_mov_b32_e32 v12, v1
	v_mov_b32_e32 v13, v1
	v_mov_b32_e32 v14, v1
	v_mov_b32_e32 v15, v1
	v_mov_b32_e32 v32, v1
	v_mov_b32_e32 v33, v1
	v_mov_b32_e32 v34, v1
	v_mov_b32_e32 v35, v1
	v_mov_b32_e32 v36, v1
	v_mov_b32_e32 v37, v1
	v_mov_b32_e32 v38, v1
	v_mov_b32_e32 v39, v1
	v_mov_b32_e32 v40, v1
	v_mov_b32_e32 v41, v1
	v_mov_b32_e32 v42, v1
	v_mov_b32_e32 v43, v1
	v_mov_b32_e32 v44, v1
	v_mov_b32_e32 v45, v1
	v_mov_b32_e32 v46, v1
	v_mov_b32_e32 v47, v1
	v_mov_b32_e32 v16, v1
	v_mov_b32_e32 v17, v1
	v_mov_b32_e32 v18, v1
	v_mov_b32_e32 v19, v1
	v_mov_b32_e32 v20, v1
	v_mov_b32_e32 v21, v1
	v_mov_b32_e32 v22, v1
	v_mov_b32_e32 v23, v1
	v_mov_b32_e32 v24, v1
	v_mov_b32_e32 v25, v1
	v_mov_b32_e32 v26, v1
	v_mov_b32_e32 v27, v1
	v_mov_b32_e32 v28, v1
	v_mov_b32_e32 v29, v1
	v_mov_b32_e32 v30, v1
	v_mov_b32_e32 v31, v1
	v_mov_b32_e32 v48, v1
	v_mov_b32_e32 v49, v1
	v_mov_b32_e32 v50, v1
	v_mov_b32_e32 v51, v1
	v_mov_b32_e32 v52, v1
	v_mov_b32_e32 v53, v1
	v_mov_b32_e32 v54, v1
	v_mov_b32_e32 v55, v1
	v_mov_b32_e32 v56, v1
	v_mov_b32_e32 v57, v1
	v_mov_b32_e32 v58, v1
	v_mov_b32_e32 v59, v1
	v_mov_b32_e32 v60, v1
	v_mov_b32_e32 v61, v1
	v_mov_b32_e32 v62, v1
	v_mov_b32_e32 v63, v1
	s_waitcnt vmcnt(0)
	s_branch .LBB0_1693

; #define LAS __attribute__((address_space(3)))
; __device__ __forceinline__ void gla_unit(LAS unsigned char* lds, const unsigned char* ws, const float* g_onorm, const int b, const int h, const int wv) {
;     ...
;         f32x16 O[2];
; #pragma unroll
;         for (int tt = 0; tt < 2; ++tt)
; #pragma unroll
;             for (int r = 0; r < 16; ++r) O[tt][r] = 0.f;
; #pragma unroll
;         for (int et = 0; et < 4; ++et)
; #pragma unroll
;             for (int s2 = 0; s2 < 2; ++s2) {
;                 const bf16x8 sb = pack8(S[et], s2);
; #pragma unroll
;                 for (int tt = 0; tt < 2; ++tt) {
;                     const bf16x8 aq = ld2x64(qb8 + 32 * tt * QS + (32 * et + 16 * s2) * 2);
;                     O[tt] = __builtin_amdgcn_mfma_f32_32x32x16_bf16(aq, sb, O[tt], 0, 0, 0);
;                 }
;             }
;         __syncthreads();
; #pragma unroll
;         for (int pr = 0; pr < 3; ++pr) {
;             const int st = (pr == 2) ? 1 : 0, tt = (pr == 0) ? 0 : 1;
; #pragma unroll
;             for (int s2 = 0; s2 < 2; ++s2) {
;                 const bf16x8 ax = *(const LAS bf16x8*)(frb + (pr * 2 + s2) * 1024);
;                 const LAS unsigned char* vp = vP + (32 * st + 16 * s2) * VS;
;                 const bf16x8 bv = tr8(vp, vp + 8 * VS);
;                 O[tt] = __builtin_amdgcn_mfma_f32_32x32x16_bf16(ax, bv, O[tt], 0, 0, 0);
;             }
;         }
;         __builtin_amdgcn_sched_barrier(0);
; #pragma unroll
;         for (int tt = 0; tt < 2; ++tt)
; #pragma unroll
;             for (int r = 0; r < 16; ++r) ob[(32 * tt + (r & 3) + 8 * (r >> 2)) * OS] = O[tt][r];
;         __builtin_amdgcn_sched_barrier(0);
; #pragma unroll
;         for (int et = 0; et < 4; ++et)
; #pragma unroll
;             for (int rg = 0; rg < 4; ++rg) { const f32x4 dl = *(const LAS f32x4*)&decb[32 * et + 8 * rg];
.LBB0_1692:
	ds_read2_b64 v[64:67], v222 offset1:2
	v_cvt_pk_bf16_f32 v68, v48, v49
	v_cvt_pk_bf16_f32 v69, v50, v51
	v_cvt_pk_bf16_f32 v70, v52, v53
	v_cvt_pk_bf16_f32 v71, v54, v55
	ds_read2_b64 v[192:195], v222 offset0:4 offset1:6
	v_cvt_pk_bf16_f32 v198, v56, v57
	v_cvt_pk_bf16_f32 v199, v58, v59
	v_cvt_pk_bf16_f32 v200, v60, v61
	s_waitcnt lgkmcnt(1)
	v_mfma_f32_32x32x16_bf16 v[80:95], v[64:67], v[68:71], 0
	ds_read2_b64 v[64:67], v223 offset0:64 offset1:66
	v_cvt_pk_bf16_f32 v201, v62, v63
	s_waitcnt lgkmcnt(1)
	s_nop 0
	v_mfma_f32_32x32x16_bf16 v[80:95], v[192:195], v[198:201], v[80:95]
	ds_read2_b64 v[192:195], v223 offset0:68 offset1:70
	s_waitcnt lgkmcnt(1)
	v_mfma_f32_32x32x16_bf16 v[64:79], v[64:67], v[68:71], 0
	s_waitcnt lgkmcnt(0)
	v_mfma_f32_32x32x16_bf16 v[64:79], v[192:195], v[198:201], v[64:79]
	ds_read2_b64 v[192:195], v222 offset0:8 offset1:10
	v_cvt_pk_bf16_f32 v198, v16, v17
	v_cvt_pk_bf16_f32 v199, v18, v19
	v_cvt_pk_bf16_f32 v200, v20, v21
	v_cvt_pk_bf16_f32 v201, v22, v23
	s_waitcnt lgkmcnt(0)
	s_nop 0
	v_mfma_f32_32x32x16_bf16 v[80:95], v[192:195], v[198:201], v[80:95]
	ds_read2_b64 v[192:195], v223 offset0:72 offset1:74
	s_waitcnt lgkmcnt(0)
	v_mfma_f32_32x32x16_bf16 v[64:79], v[192:195], v[198:201], v[64:79]
	ds_read2_b64 v[192:195], v222 offset0:12 offset1:14
	v_cvt_pk_bf16_f32 v198, v24, v25
	v_cvt_pk_bf16_f32 v199, v26, v27
	v_cvt_pk_bf16_f32 v200, v28, v29
	v_cvt_pk_bf16_f32 v201, v30, v31
	s_waitcnt lgkmcnt(0)
	s_nop 0
	v_mfma_f32_32x32x16_bf16 v[80:95], v[192:195], v[198:201], v[80:95]
	ds_read2_b64 v[192:195], v223 offset0:76 offset1:78
	s_waitcnt lgkmcnt(0)
	v_mfma_f32_32x32x16_bf16 v[64:79], v[192:195], v[198:201], v[64:79]
	ds_read2_b64 v[192:195], v222 offset0:16 offset1:18
	v_cvt_pk_bf16_f32 v198, v32, v33
	v_cvt_pk_bf16_f32 v199, v34, v35
	v_cvt_pk_bf16_f32 v200, v36, v37
	v_cvt_pk_bf16_f32 v201, v38, v39
	s_waitcnt lgkmcnt(0)
	s_nop 0
	v_mfma_f32_32x32x16_bf16 v[80:95], v[192:195], v[198:201], v[80:95]
	ds_read2_b64 v[192:195], v223 offset0:80 offset1:82
	s_waitcnt lgkmcnt(0)
	v_mfma_f32_32x32x16_bf16 v[64:79], v[192:195], v[198:201], v[64:79]
	ds_read2_b64 v[192:195], v222 offset0:20 offset1:22
	v_cvt_pk_bf16_f32 v198, v40, v41
	v_cvt_pk_bf16_f32 v199, v42, v43
	v_cvt_pk_bf16_f32 v200, v44, v45
	v_cvt_pk_bf16_f32 v201, v46, v47
	s_waitcnt lgkmcnt(0)
	s_nop 0
	v_mfma_f32_32x32x16_bf16 v[80:95], v[192:195], v[198:201], v[80:95]
	ds_read2_b64 v[192:195], v223 offset0:84 offset1:86
	s_waitcnt lgkmcnt(0)
	v_mfma_f32_32x32x16_bf16 v[64:79], v[192:195], v[198:201], v[64:79]
	ds_read2_b64 v[192:195], v222 offset0:24 offset1:26
	v_cvt_pk_bf16_f32 v198, v0, v1
	v_cvt_pk_bf16_f32 v199, v2, v3
	v_cvt_pk_bf16_f32 v200, v4, v5
	v_cvt_pk_bf16_f32 v201, v6, v7
	s_waitcnt lgkmcnt(0)
	s_nop 0
	v_mfma_f32_32x32x16_bf16 v[80:95], v[192:195], v[198:201], v[80:95]
	ds_read2_b64 v[192:195], v223 offset0:88 offset1:90
	s_waitcnt lgkmcnt(0)
	v_mfma_f32_32x32x16_bf16 v[64:79], v[192:195], v[198:201], v[64:79]
	ds_read2_b64 v[192:195], v222 offset0:28 offset1:30
	v_cvt_pk_bf16_f32 v198, v8, v9
	v_cvt_pk_bf16_f32 v199, v10, v11
	v_cvt_pk_bf16_f32 v200, v12, v13
	v_cvt_pk_bf16_f32 v201, v14, v15
	s_waitcnt lgkmcnt(0)
	s_nop 0
	v_mfma_f32_32x32x16_bf16 v[80:95], v[192:195], v[198:201], v[80:95]
	ds_read2_b64 v[192:195], v223 offset0:92 offset1:94
	s_waitcnt lgkmcnt(0)
	s_barrier
	v_mfma_f32_32x32x16_bf16 v[64:79], v[192:195], v[198:201], v[64:79]
	ds_read_b128 v[192:195], v206
	ds_read_b64_tr_b16 v[198:199], v218
	ds_read_b64_tr_b16 v[200:201], v218 offset:4608
	ds_read_b128 v[222:225], v206 offset:1024
	ds_read_b64_tr_b16 v[226:227], v218 offset:9216
	ds_read_b64_tr_b16 v[228:229], v218 offset:13824
	s_waitcnt lgkmcnt(3)
	v_mfma_f32_32x32x16_bf16 v[80:95], v[192:195], v[198:201], v[80:95]
	s_waitcnt lgkmcnt(0)
	v_mfma_f32_32x32x16_bf16 v[80:95], v[222:225], v[226:229], v[80:95]
	ds_read_b128 v[192:195], v206 offset:2048
	ds_read_b128 v[222:225], v206 offset:3072
	s_waitcnt lgkmcnt(1)
	v_mfma_f32_32x32x16_bf16 v[64:79], v[192:195], v[198:201], v[64:79]
	s_waitcnt lgkmcnt(0)
	v_mfma_f32_32x32x16_bf16 v[64:79], v[222:225], v[226:229], v[64:79]
	ds_read_b128 v[192:195], v206 offset:4096
	ds_read_b64_tr_b16 v[198:199], v218 offset:18432
	ds_read_b64_tr_b16 v[200:201], v218 offset:23040
	ds_read_b128 v[222:225], v206 offset:5120
	ds_read_b64_tr_b16 v[226:227], v218 offset:27648
	ds_read_b64_tr_b16 v[228:229], v218 offset:32256
	s_waitcnt lgkmcnt(3)
	v_mfma_f32_32x32x16_bf16 v[64:79], v[192:195], v[198:201], v[64:79]
	s_waitcnt lgkmcnt(0)
	v_mfma_f32_32x32x16_bf16 v[64:79], v[222:225], v[226:229], v[64:79]
	ds_write_b32 v207, v80
	ds_write_b32 v207, v81 offset:1040
	ds_write_b32 v207, v82 offset:2080
	ds_write_b32 v207, v83 offset:3120
	ds_write_b32 v207, v84 offset:8320
	ds_write_b32 v207, v85 offset:9360
	ds_write_b32 v207, v86 offset:10400
	ds_write_b32 v207, v87 offset:11440
	ds_write_b32 v207, v88 offset:16640
	ds_write_b32 v207, v89 offset:17680
	ds_write_b32 v207, v90 offset:18720
	ds_write_b32 v207, v91 offset:19760
	ds_write_b32 v207, v92 offset:24960
	ds_write_b32 v207, v93 offset:26000
	ds_write_b32 v207, v94 offset:27040
	ds_write_b32 v207, v95 offset:28080
	ds_write_b32 v207, v64 offset:33280
	ds_write_b32 v207, v65 offset:34320
	ds_write_b32 v207, v66 offset:35360
	ds_write_b32 v207, v67 offset:36400
	ds_write_b32 v207, v68 offset:41600
	ds_write_b32 v207, v69 offset:42640
	ds_write_b32 v207, v70 offset:43680
	ds_write_b32 v207, v71 offset:44720
	ds_write_b32 v207, v72 offset:49920
	ds_write_b32 v207, v73 offset:50960
	ds_write_b32 v207, v74 offset:52000
	ds_write_b32 v207, v75 offset:53040
	ds_write_b32 v207, v76 offset:58240
	ds_write_b32 v207, v77 offset:59280
	ds_write_b32 v207, v78 offset:60320
	ds_write_b32 v207, v79 offset:61360
	ds_read_b128 v[64:67], v205 offset:96
	ds_read_b128 v[68:71], v205 offset:64
	ds_read_b128 v[72:75], v205 offset:32
	ds_read_b128 v[76:79], v205
	s_waitcnt vmcnt(11)
; #define LAS __attribute__((address_space(3)))
; __device__ __forceinline__ void gla_unit(LAS unsigned char* lds, const unsigned char* ws, const float* g_onorm, const int b, const int h, const int wv) {
;     ...
; #pragma unroll
;         for (int et = 0; et < 4; ++et)
; #pragma unroll
;             for (int rg = 0; rg < 4; ++rg) { const f32x4 dl = *(const LAS f32x4*)&decb[32 * et + 8 * rg];
; #pragma unroll
;                 for (int x = 0; x < 4; ++x) S[et][4 * rg + x] *= dl[x]; }
; #pragma unroll
;         for (int ks = 0; ks < 4; ++ks) {
;             const LAS unsigned char* vp = vN + 16 * ks * VS;
;             const bf16x8 bv = tr8(vp, vp + 4 * VS);
; #pragma unroll
;             for (int et = 0; et < 4; ++et) {
;                 const LAS unsigned char* kp = keN + 32 * et * 2 + 16 * ks * ES;
;                 const bf16x8 ak = tr8(kp, kp + 4 * ES);
;                 S[et] = __builtin_amdgcn_mfma_f32_32x32x16_bf16(ak, bv, S[et], 0, 0, 0);
;             }
;         }
	v_lshlrev_b32_e32 v232, 16, v176
	s_waitcnt lgkmcnt(3)
	v_pk_mul_f32 v[62:63], v[62:63], v[66:67]
	s_waitcnt lgkmcnt(2)
	v_pk_mul_f32 v[58:59], v[58:59], v[70:71]
	v_pk_mul_f32 v[60:61], v[60:61], v[64:65]
	s_waitcnt lgkmcnt(0)
	v_pk_mul_f32 v[50:51], v[50:51], v[78:79]
	v_pk_mul_f32 v[56:57], v[56:57], v[68:69]
	ds_read_b128 v[64:67], v205 offset:192
	ds_read_b128 v[68:71], v205 offset:224
	ds_read_b128 v[78:81], v205 offset:128
	ds_read_b128 v[82:85], v205 offset:160
	v_pk_mul_f32 v[54:55], v[54:55], v[74:75]
	v_pk_mul_f32 v[52:53], v[52:53], v[72:73]
	v_pk_mul_f32 v[48:49], v[48:49], v[76:77]
	s_waitcnt lgkmcnt(2)
	v_pk_mul_f32 v[30:31], v[30:31], v[70:71]
	v_pk_mul_f32 v[26:27], v[26:27], v[66:67]
	s_waitcnt lgkmcnt(0)
	v_pk_mul_f32 v[22:23], v[22:23], v[84:85]
	v_pk_mul_f32 v[18:19], v[18:19], v[80:81]
	v_pk_mul_f32 v[28:29], v[28:29], v[68:69]
	v_pk_mul_f32 v[24:25], v[24:25], v[64:65]
	v_pk_mul_f32 v[20:21], v[20:21], v[82:83]
	ds_read_b128 v[64:67], v205 offset:256
	ds_read_b128 v[68:71], v205 offset:288
	ds_read_b128 v[72:75], v205 offset:320
	ds_read_b128 v[80:83], v205 offset:352
	ds_read_b64_tr_b16 v[84:85], v219
	ds_read_b64_tr_b16 v[86:87], v219 offset:2304
	ds_read_b64_tr_b16 v[90:91], v220 offset:1280
	ds_read_b64_tr_b16 v[88:89], v220
	ds_read_b64_tr_b16 v[92:93], v220 offset:64
	ds_read_b64_tr_b16 v[192:193], v220 offset:128
	ds_read_b64_tr_b16 v[198:199], v220 offset:192
	ds_read_b64_tr_b16 v[94:95], v220 offset:1344
	ds_read_b64_tr_b16 v[194:195], v220 offset:1408
	ds_read_b64_tr_b16 v[200:201], v220 offset:1472
	ds_read_b64_tr_b16 v[222:223], v219 offset:9216
	ds_read_b64_tr_b16 v[224:225], v219 offset:11520
	s_waitcnt lgkmcnt(8)
	v_mfma_f32_32x32x16_bf16 v[48:63], v[88:91], v[84:87], v[48:63]
	v_mul_f32_e64 v16, v16, v78
	v_mul_f32_e64 v17, v17, v79
	v_mul_f32_e64 v42, v42, v74
	v_mul_f32_e64 v43, v43, v75
	v_mul_f32_e64 v38, v38, v70
	v_mul_f32_e64 v39, v39, v71
	v_pk_mul_f32 v[34:35], v[34:35], v[66:67]
	v_pk_mul_f32 v[44:45], v[44:45], v[80:81]
	v_pk_mul_f32 v[40:41], v[40:41], v[72:73]
	ds_read_b128 v[70:73], v205 offset:448
	ds_read_b128 v[74:77], v205 offset:480
	v_pk_mul_f32 v[36:37], v[36:37], v[68:69]
	ds_read_b128 v[66:69], v205 offset:384
	ds_read_b128 v[78:81], v205 offset:416
	v_pk_mul_f32 v[46:47], v[46:47], v[82:83]
	v_pk_mul_f32 v[32:33], v[32:33], v[64:65]
	s_waitcnt lgkmcnt(2)
	v_pk_mul_f32 v[14:15], v[14:15], v[76:77]
	v_pk_mul_f32 v[10:11], v[10:11], v[72:73]
	s_waitcnt lgkmcnt(0)
	v_pk_mul_f32 v[6:7], v[6:7], v[80:81]
	v_pk_mul_f32 v[2:3], v[2:3], v[68:69]
	v_pk_mul_f32 v[12:13], v[12:13], v[74:75]
	v_pk_mul_f32 v[8:9], v[8:9], v[70:71]
	v_pk_mul_f32 v[4:5], v[4:5], v[78:79]
	v_pk_mul_f32 v[0:1], v[0:1], v[66:67]
	v_mfma_f32_32x32x16_bf16 v[16:31], v[92:95], v[84:87], v[16:31]
	ds_read_b64_tr_b16 v[66:67], v220 offset:6400
	ds_read_b64_tr_b16 v[64:65], v220 offset:5120
	ds_read_b64_tr_b16 v[68:69], v220 offset:5184
	ds_read_b64_tr_b16 v[72:73], v220 offset:5248
	ds_read_b64_tr_b16 v[76:77], v220 offset:5312
	ds_read_b64_tr_b16 v[70:71], v220 offset:6464
	ds_read_b64_tr_b16 v[74:75], v220 offset:6528
	ds_read_b64_tr_b16 v[78:79], v220 offset:6592
	v_and_b32_e32 v233, 0xffff0000, v176
	s_add_i32 s66, s66, 2
	v_lshl_add_u64 v[182:183], v[182:183], 0, s[60:61]
	v_lshl_add_u64 v[184:185], v[184:185], 0, s[62:63]
	v_lshl_add_u64 v[186:187], v[186:187], 0, s[64:65]
	v_lshl_add_u64 v[188:189], v[188:189], 0, s[68:69]
	v_mfma_f32_32x32x16_bf16 v[32:47], v[192:195], v[84:87], v[32:47]
	s_cmp_lt_u32 s73, 30
	v_lshl_add_u64 v[190:191], v[190:191], 0, s[62:63]
	v_mfma_f32_32x32x16_bf16 v[0:15], v[198:201], v[84:87], v[0:15]
	s_waitcnt lgkmcnt(6)
	v_mfma_f32_32x32x16_bf16 v[48:63], v[64:67], v[222:225], v[48:63]
	s_waitcnt lgkmcnt(2)
	v_mfma_f32_32x32x16_bf16 v[16:31], v[68:71], v[222:225], v[16:31]
	s_waitcnt lgkmcnt(1)
	v_mfma_f32_32x32x16_bf16 v[32:47], v[72:75], v[222:225], v[32:47]
	s_waitcnt lgkmcnt(0)
	v_mfma_f32_32x32x16_bf16 v[0:15], v[76:79], v[222:225], v[0:15]
	ds_read_b64_tr_b16 v[64:65], v219 offset:18432
	ds_read_b64_tr_b16 v[66:67], v219 offset:20736
	ds_read_b64_tr_b16 v[70:71], v220 offset:11520
	ds_read_b64_tr_b16 v[68:69], v220 offset:10240
	ds_read_b64_tr_b16 v[72:73], v220 offset:10304
	ds_read_b64_tr_b16 v[76:77], v220 offset:10368
	ds_read_b64_tr_b16 v[80:81], v220 offset:10432
	ds_read_b64_tr_b16 v[74:75], v220 offset:11584
	ds_read_b64_tr_b16 v[78:79], v220 offset:11648
	ds_read_b64_tr_b16 v[82:83], v220 offset:11712
	ds_read_b64_tr_b16 v[84:85], v219 offset:27648
	ds_read_b64_tr_b16 v[86:87], v219 offset:29952
	s_waitcnt lgkmcnt(8)
	v_mfma_f32_32x32x16_bf16 v[48:63], v[68:71], v[64:67], v[48:63]
	ds_read_b64_tr_b16 v[68:69], v220 offset:16640
	s_waitcnt lgkmcnt(5)
	v_mfma_f32_32x32x16_bf16 v[16:31], v[72:75], v[64:67], v[16:31]
	s_waitcnt lgkmcnt(4)
	v_mfma_f32_32x32x16_bf16 v[32:47], v[76:79], v[64:67], v[32:47]
	s_waitcnt lgkmcnt(3)
	v_mfma_f32_32x32x16_bf16 v[0:15], v[80:83], v[64:67], v[0:15]
	ds_read_b64_tr_b16 v[66:67], v220 offset:15360
	ds_read_b64_tr_b16 v[70:71], v220 offset:15424
	ds_read_b64_tr_b16 v[74:75], v220 offset:15488
	ds_read_b64_tr_b16 v[78:79], v220 offset:15552
	ds_read_b64_tr_b16 v[72:73], v220 offset:16704
	ds_read_b64_tr_b16 v[76:77], v220 offset:16768
	ds_read_b64_tr_b16 v[80:81], v220 offset:16832
	s_waitcnt lgkmcnt(0)
	s_barrier
; #define LAS __attribute__((address_space(3)))
; __device__ __forceinline__ unsigned cvt_pk_bf16(float lo, float hi) { const bf16x2_t r = __builtin_convertvector((f32x2_t){lo, hi}, bf16x2_t); return __builtin_bit_cast(unsigned, r); }
; __device__ __forceinline__ float bf_lo(unsigned w) { return __uint_as_float(w << 16); }
; __device__ __forceinline__ float bf_hi(unsigned w) { return __uint_as_float(w & 0xffff0000u); }
; __device__ __forceinline__ void gla_unit(LAS unsigned char* lds, const unsigned char* ws, const float* g_onorm, const int b, const int h, const int wv) {
;     ...
;         {
;             const int t = tid >> 3, g8 = tid & 7;
;             float ov[32]; float ss = 0.f;
; #pragma unroll
;             for (int x = 0; x < 8; ++x) { const f32x4 v = *(const LAS f32x4*)&obuf[t * OS + 32 * g8 + 4 * x]; ov[4 * x] = v[0]; ov[4 * x + 1] = v[1]; ov[4 * x + 2] = v[2]; ov[4 * x + 3] = v[3];
;                 ss += v[0] * v[0] + v[1] * v[1] + v[2] * v[2] + v[3] * v[3]; }
;             ss += __builtin_bit_cast(float, __builtin_amdgcn_ds_swizzle(__builtin_bit_cast(int, ss), (1 << 10) | 0x1F)); ss += __builtin_bit_cast(float, __builtin_amdgcn_ds_swizzle(__builtin_bit_cast(int, ss), (2 << 10) | 0x1F));
;             ss += __builtin_bit_cast(float, __builtin_amdgcn_ds_swizzle(__builtin_bit_cast(int, ss), (4 << 10) | 0x1F));
;             const float rstd = __builtin_amdgcn_rsqf(ss * (1.0f / 256.0f) + EPSV);
;             bf16_t* mp = mix + (t0 + t) * DM + 1024 + h * 256 + 32 * g8;
; #pragma unroll
;             for (int x = 0; x < 4; ++x) {
;                 const u32x4 og = ogr[x];
;                 const f32x4 g0 = *(const LAS f32x4*)&gon[32 * g8 + 8 * x], g1 = *(const LAS f32x4*)&gon[32 * g8 + 8 * x + 4];
;                 const float gg2[8] = {g0[0], g0[1], g0[2], g0[3], g1[0], g1[1], g1[2], g1[3]};
;                 float res[8];
; #pragma unroll
;                 for (int y = 0; y < 4; ++y) { const float a0 = bf_lo(og[y]), a1 = bf_hi(og[y]);
;                     res[2 * y] = ov[8 * x + 2 * y] * rstd * gg2[2 * y] * a0;
;                     res[2 * y + 1] = ov[8 * x + 2 * y + 1] * rstd * gg2[2 * y + 1] * a1; }
;                 u32x4 wv4; wv4[0] = cvt_pk_bf16(res[0], res[1]); wv4[1] = cvt_pk_bf16(res[2], res[3]); wv4[2] = cvt_pk_bf16(res[4], res[5]); wv4[3] = cvt_pk_bf16(res[6], res[7]);
;                 *(u32x4*)(mp + 8 * x) = wv4;
	v_mfma_f32_32x32x16_bf16 v[48:63], v[66:69], v[84:87], v[48:63]
	ds_read_b128 v[64:67], v221
	ds_read_b128 v[88:91], v221 offset:16
	ds_read_b128 v[92:95], v221 offset:32
	ds_read_b128 v[192:195], v221 offset:48
	s_waitcnt lgkmcnt(3)
	v_mul_f32_e32 v68, v65, v65
	s_waitcnt lgkmcnt(2)
	v_mul_f32_e32 v69, v89, v89
	v_fmac_f32_e32 v68, v64, v64
	v_fmac_f32_e32 v69, v88, v88
	v_fmac_f32_e32 v68, v66, v66
	v_fmac_f32_e32 v69, v90, v90
	v_mfma_f32_32x32x16_bf16 v[16:31], v[70:73], v[84:87], v[16:31]
	v_fmac_f32_e32 v68, v67, v67
	v_fmac_f32_e32 v69, v91, v91
	s_waitcnt lgkmcnt(1)
	v_mov_b32_e32 v70, v93
	s_waitcnt lgkmcnt(0)
	v_mov_b32_e32 v71, v193
	v_add_f32_e32 v222, v68, v69
	v_mov_b32_e32 v68, v92
	v_mov_b32_e32 v69, v192
	v_pk_mul_f32 v[70:71], v[70:71], v[70:71]
	v_mov_b32_e32 v82, v95
	v_pk_fma_f32 v[68:69], v[68:69], v[68:69], v[70:71]
	v_mov_b32_e32 v70, v94
	v_mov_b32_e32 v71, v194
	v_pk_fma_f32 v[72:73], v[70:71], v[70:71], v[68:69]
	ds_read_b128 v[68:71], v221 offset:64
	ds_read_b128 v[198:201], v221 offset:80
	v_mov_b32_e32 v83, v195
	v_pk_fma_f32 v[72:73], v[82:83], v[82:83], v[72:73]
	v_mfma_f32_32x32x16_bf16 v[32:47], v[74:77], v[84:87], v[32:47]
	v_add_f32_e32 v72, v222, v72
	s_waitcnt lgkmcnt(1)
	v_mov_b32_e32 v82, v69
	s_waitcnt lgkmcnt(0)
	v_mov_b32_e32 v83, v199
	ds_read_b128 v[222:225], v221 offset:96
	ds_read_b128 v[226:229], v221 offset:112
	v_add_f32_e32 v230, v72, v73
	v_mov_b32_e32 v72, v68
	v_mov_b32_e32 v73, v198
	v_pk_mul_f32 v[82:83], v[82:83], v[82:83]
	v_mfma_f32_32x32x16_bf16 v[0:15], v[78:81], v[84:87], v[0:15]
	v_fma_f32 v72, v72, v72, v82
	v_fma_f32 v73, v73, v73, v83
	v_mov_b32_e32 v82, v70
	v_mov_b32_e32 v83, v200
	v_fma_f32 v72, v82, v82, v72
	v_fma_f32 v73, v83, v83, v73
	v_mov_b32_e32 v82, v71
	v_mov_b32_e32 v83, v201
	v_pk_fma_f32 v[72:73], v[82:83], v[82:83], v[72:73]
	s_waitcnt lgkmcnt(1)
	v_mov_b32_e32 v82, v223
	v_add_f32_e32 v72, v230, v72
	s_waitcnt lgkmcnt(0)
	v_mov_b32_e32 v83, v227
	v_add_f32_e32 v230, v72, v73
	v_mov_b32_e32 v72, v222
	v_mov_b32_e32 v73, v226
	v_pk_mul_f32 v[82:83], v[82:83], v[82:83]
	s_nop 0
	v_pk_fma_f32 v[72:73], v[72:73], v[72:73], v[82:83]
	v_mov_b32_e32 v82, v224
	v_mov_b32_e32 v83, v228
	v_pk_fma_f32 v[72:73], v[82:83], v[82:83], v[72:73]
	v_mov_b32_e32 v82, v225
	v_mov_b32_e32 v83, v229
	v_pk_fma_f32 v[72:73], v[82:83], v[82:83], v[72:73]
	s_nop 0
	v_add_f32_e32 v72, v230, v72
	v_add_f32_e32 v72, v72, v73
	ds_swizzle_b32 v73, v72 offset:swizzle(SWAP,1)
	s_waitcnt lgkmcnt(0)
	v_add_f32_e32 v72, v72, v73
	ds_swizzle_b32 v73, v72 offset:swizzle(SWAP,2)
	s_waitcnt lgkmcnt(0)
	v_add_f32_e32 v72, v72, v73
	ds_swizzle_b32 v73, v72 offset:swizzle(SWAP,4)
	s_waitcnt lgkmcnt(0)
	v_add_f32_e32 v72, v72, v73
	v_fmamk_f32 v72, v72, 0x3b800000, v181
	v_rsq_f32_e32 v230, v72
	ds_read_b128 v[72:75], v208
	ds_read_b128 v[76:79], v208 offset:16
	ds_read_b128 v[80:83], v208 offset:32
	ds_read_b128 v[84:87], v208 offset:48
	v_pk_mul_f32 v[64:65], v[64:65], v[230:231] op_sel_hi:[1,0]
	v_pk_mul_f32 v[66:67], v[66:67], v[230:231] op_sel_hi:[1,0]
	s_waitcnt lgkmcnt(3)
	v_pk_mul_f32 v[64:65], v[72:73], v[64:65]
	v_lshlrev_b32_e32 v72, 16, v177
	v_and_b32_e32 v73, 0xffff0000, v177
	v_pk_mul_f32 v[66:67], v[74:75], v[66:67]
	v_pk_mul_f32 v[74:75], v[88:89], v[230:231] op_sel_hi:[1,0]
	v_pk_mul_f32 v[66:67], v[66:67], v[72:73]
	v_lshlrev_b32_e32 v72, 16, v178
	v_and_b32_e32 v73, 0xffff0000, v178
	s_waitcnt lgkmcnt(2)
	v_pk_mul_f32 v[74:75], v[76:77], v[74:75]
	v_pk_mul_f32 v[76:77], v[90:91], v[230:231] op_sel_hi:[1,0]
	v_pk_mul_f32 v[72:73], v[74:75], v[72:73]
	v_lshlrev_b32_e32 v74, 16, v179
	v_and_b32_e32 v75, 0xffff0000, v179
	v_pk_mul_f32 v[76:77], v[78:79], v[76:77]
	v_pk_mul_f32 v[64:65], v[64:65], v[232:233]
	v_pk_mul_f32 v[74:75], v[76:77], v[74:75]
	v_add_co_u32_e32 v76, vcc, s72, v196
	v_cvt_pk_bf16_f32 v64, v64, v65
	v_cvt_pk_bf16_f32 v65, v66, v67
	v_cvt_pk_bf16_f32 v66, v72, v73
	v_cvt_pk_bf16_f32 v67, v74, v75
	v_addc_co_u32_e32 v77, vcc, 0, v197, vcc
	global_store_dwordx4 v[76:77], v[64:67], off offset:2048
	v_pk_mul_f32 v[72:73], v[94:95], v[230:231] op_sel_hi:[1,0]
	v_pk_mul_f32 v[74:75], v[192:193], v[230:231] op_sel_hi:[1,0]
	v_pk_mul_f32 v[66:67], v[92:93], v[230:231] op_sel_hi:[1,0]
	s_waitcnt vmcnt(9)
; #define LAS __attribute__((address_space(3)))
; __device__ __forceinline__ unsigned cvt_pk_bf16(float lo, float hi) { const bf16x2_t r = __builtin_convertvector((f32x2_t){lo, hi}, bf16x2_t); return __builtin_bit_cast(unsigned, r); }
; __device__ __forceinline__ float bf_lo(unsigned w) { return __uint_as_float(w << 16); }
; __device__ __forceinline__ float bf_hi(unsigned w) { return __uint_as_float(w & 0xffff0000u); }
; __device__ __forceinline__ void gla_unit(LAS unsigned char* lds, const unsigned char* ws, const float* g_onorm, const int b, const int h, const int wv) {
;     ...
;         __syncthreads();
; #pragma unroll
;         for (int i = 0; i < 2; ++i) { const int c = tid + 512 * i, row = c >> 4, cc = (c & 15) * 16;
;             *(LAS u32x4*)(lds + L_Q + row * QS + cc) = qr[par][i]; *(LAS u32x4*)(lds + L_K + row * QS + cc) = kr[par][i]; }
; #pragma unroll
;         for (int i = 0; i < 4; ++i) { const int c = tid + 512 * i; *(LAS u32x4*)(lds + L_V + (c >> 5) * VS + (c & 31) * 16) = vr[par][i]; }
;         if (tid < 32) {
;             const float L2E_ = 1.4426950408889634f;
;             *(LAS f32x4*)&dec[tid * 4] = (f32x4){__builtin_amdgcn_exp2f(dr[0] * L2E_), __builtin_amdgcn_exp2f(dr[1] * L2E_), __builtin_amdgcn_exp2f(dr[2] * L2E_), __builtin_amdgcn_exp2f(dr[3] * L2E_)};
;         }
;     ...
; #pragma unroll
;             for (int x = 0; x < 4; ++x) {
;                 const u32x4 og = ogr[x];
;                 const f32x4 g0 = *(const LAS f32x4*)&gon[32 * g8 + 8 * x], g1 = *(const LAS f32x4*)&gon[32 * g8 + 8 * x + 4];
;                 const float gg2[8] = {g0[0], g0[1], g0[2], g0[3], g1[0], g1[1], g1[2], g1[3]};
;                 float res[8];
; #pragma unroll
;                 for (int y = 0; y < 4; ++y) { const float a0 = bf_lo(og[y]), a1 = bf_hi(og[y]);
;                     res[2 * y] = ov[8 * x + 2 * y] * rstd * gg2[2 * y] * a0;
;                     res[2 * y + 1] = ov[8 * x + 2 * y + 1] * rstd * gg2[2 * y + 1] * a1; }
;                 u32x4 wv4; wv4[0] = cvt_pk_bf16(res[0], res[1]); wv4[1] = cvt_pk_bf16(res[2], res[3]); wv4[2] = cvt_pk_bf16(res[4], res[5]); wv4[3] = cvt_pk_bf16(res[6], res[7]);
;                 *(u32x4*)(mp + 8 * x) = wv4;
;             }
	v_lshlrev_b32_e32 v64, 16, v172
	v_and_b32_e32 v65, 0xffff0000, v172
	s_waitcnt lgkmcnt(1)
	v_pk_mul_f32 v[66:67], v[80:81], v[66:67]
	v_pk_mul_f32 v[72:73], v[82:83], v[72:73]
	v_pk_mul_f32 v[64:65], v[66:67], v[64:65]
	v_lshlrev_b32_e32 v66, 16, v173
	v_and_b32_e32 v67, 0xffff0000, v173
	v_pk_mul_f32 v[66:67], v[72:73], v[66:67]
	v_lshlrev_b32_e32 v72, 16, v174
	v_and_b32_e32 v73, 0xffff0000, v174
	s_waitcnt lgkmcnt(0)
	v_pk_mul_f32 v[74:75], v[84:85], v[74:75]
	v_pk_mul_f32 v[78:79], v[194:195], v[230:231] op_sel_hi:[1,0]
	v_pk_mul_f32 v[72:73], v[74:75], v[72:73]
	v_lshlrev_b32_e32 v74, 16, v175
	v_and_b32_e32 v75, 0xffff0000, v175
	v_pk_mul_f32 v[78:79], v[86:87], v[78:79]
	v_cvt_pk_bf16_f32 v64, v64, v65
	v_pk_mul_f32 v[74:75], v[78:79], v[74:75]
	v_cvt_pk_bf16_f32 v65, v66, v67
	v_cvt_pk_bf16_f32 v66, v72, v73
	v_cvt_pk_bf16_f32 v67, v74, v75
	global_store_dwordx4 v[76:77], v[64:67], off offset:2064
	ds_read_b128 v[64:67], v208 offset:64
	ds_read_b128 v[72:75], v208 offset:80
	v_pk_mul_f32 v[68:69], v[68:69], v[230:231] op_sel_hi:[1,0]
	v_pk_mul_f32 v[70:71], v[70:71], v[230:231] op_sel_hi:[1,0]
	v_lshlrev_b32_e32 v78, 16, v168
	s_waitcnt lgkmcnt(1)
	v_pk_mul_f32 v[64:65], v[64:65], v[68:69]
	v_lshlrev_b32_e32 v68, 16, v169
	v_and_b32_e32 v69, 0xffff0000, v169
	v_pk_mul_f32 v[66:67], v[66:67], v[70:71]
	v_pk_mul_f32 v[70:71], v[198:199], v[230:231] op_sel_hi:[1,0]
	v_pk_mul_f32 v[66:67], v[66:67], v[68:69]
	v_lshlrev_b32_e32 v68, 16, v170
	v_and_b32_e32 v69, 0xffff0000, v170
	s_waitcnt lgkmcnt(0)
	v_pk_mul_f32 v[70:71], v[72:73], v[70:71]
	v_pk_mul_f32 v[72:73], v[200:201], v[230:231] op_sel_hi:[1,0]
	v_and_b32_e32 v79, 0xffff0000, v168
	v_pk_mul_f32 v[68:69], v[70:71], v[68:69]
	v_lshlrev_b32_e32 v70, 16, v171
	v_and_b32_e32 v71, 0xffff0000, v171
	v_pk_mul_f32 v[72:73], v[74:75], v[72:73]
	v_pk_mul_f32 v[64:65], v[64:65], v[78:79]
	v_pk_mul_f32 v[70:71], v[72:73], v[70:71]
	v_cvt_pk_bf16_f32 v64, v64, v65
	v_cvt_pk_bf16_f32 v65, v66, v67
	v_cvt_pk_bf16_f32 v66, v68, v69
	v_cvt_pk_bf16_f32 v67, v70, v71
	global_store_dwordx4 v[76:77], v[64:67], off offset:2080
	ds_read_b128 v[64:67], v208 offset:96
	ds_read_b128 v[68:71], v208 offset:112
	v_pk_mul_f32 v[74:75], v[222:223], v[230:231] op_sel_hi:[1,0]
	v_lshlrev_b32_e32 v72, 16, v164
	v_and_b32_e32 v73, 0xffff0000, v164
	s_waitcnt lgkmcnt(1)
	v_pk_mul_f32 v[64:65], v[74:75], v[64:65]
	v_pk_mul_f32 v[74:75], v[224:225], v[230:231] op_sel_hi:[1,0]
	v_pk_mul_f32 v[64:65], v[64:65], v[72:73]
	v_lshlrev_b32_e32 v72, 16, v165
	v_and_b32_e32 v73, 0xffff0000, v165
	v_pk_mul_f32 v[66:67], v[74:75], v[66:67]
	v_pk_mul_f32 v[74:75], v[226:227], v[230:231] op_sel_hi:[1,0]
	v_pk_mul_f32 v[66:67], v[66:67], v[72:73]
	v_lshlrev_b32_e32 v72, 16, v166
	v_and_b32_e32 v73, 0xffff0000, v166
	s_waitcnt lgkmcnt(0)
	v_pk_mul_f32 v[68:69], v[74:75], v[68:69]
	v_pk_mul_f32 v[74:75], v[228:229], v[230:231] op_sel_hi:[1,0]
	v_pk_mul_f32 v[68:69], v[68:69], v[72:73]
	v_lshlrev_b32_e32 v72, 16, v167
	v_and_b32_e32 v73, 0xffff0000, v167
	v_pk_mul_f32 v[70:71], v[74:75], v[70:71]
	v_cvt_pk_bf16_f32 v64, v64, v65
	v_pk_mul_f32 v[70:71], v[70:71], v[72:73]
	v_cvt_pk_bf16_f32 v65, v66, v67
	v_cvt_pk_bf16_f32 v66, v68, v69
	v_cvt_pk_bf16_f32 v67, v70, v71
	global_store_dwordx4 v[76:77], v[64:67], off offset:2096
	s_cbranch_scc0 .LBB0_1712
.LBB0_1693:
	s_nop 0
	v_add_u32_e32 v64, 0, v180
	v_add_u32_e32 v226, 0x1fc00, v64
	s_waitcnt lgkmcnt(0)
	s_barrier
	s_waitcnt vmcnt(20)
	ds_write_b128 v209, v[108:111]
	ds_write_b128 v209, v[96:99] offset:17408
	ds_write_b128 v210, v[100:103]
	ds_write_b128 v210, v[104:107] offset:17408
	ds_write_b128 v211, v[112:115]
	ds_write_b128 v212, v[116:119]
	ds_write_b128 v213, v[120:123]
	s_nop 0
	ds_write_b128 v214, v[124:127]
	s_and_saveexec_b64 s[2:3], s[0:1]
	s_cbranch_execz .LBB0_1695
	s_waitcnt vmcnt(12)
	v_mul_f32_e32 v64, 0x3fb8aa3b, v128
	v_mul_f32_e32 v65, 0x3fb8aa3b, v129
	v_mul_f32_e32 v66, 0x3fb8aa3b, v130
	v_mul_f32_e32 v67, 0x3fb8aa3b, v131
	v_exp_f32_e32 v64, v64
	v_exp_f32_e32 v65, v65
	v_exp_f32_e32 v66, v66
	v_exp_f32_e32 v67, v67
	ds_write_b128 v226, v[64:67]

; #define GLA_LOAD_DR(n) do { if (tid < 32) dr = *(const f32x4*)(BC + ((size_t)b * SEQ + 64 * (n) + 63) * 512 + h * 128 + tid * 4); } while (0)
; __device__ __forceinline__ void gla_unit(LAS unsigned char* lds, const unsigned char* ws, const float* g_onorm, const int b, const int h, const int wv) {
;     ...
;         if (n + 1 < SEQ / 64) GLA_LOAD_DR(n + 1);
;         if (n + 2 < SEQ / 64) GLA_LOAD(par, n + 2);
.LBB0_1697:
	s_or_b64 exec, exec, s[2:3]
	s_add_i32 s73, s66, -1
	s_cmp_lt_u32 s73, 30
	s_mov_b64 s[2:3], -1
	s_cmp_gt_u32 s73, 29
	v_lshl_add_u64 v[194:195], s[76:77], 0, v[186:187]
	v_lshl_add_u64 v[192:193], s[76:77], 0, v[184:185]
	s_nop 0
	v_add_co_u32_e32 v64, vcc, 0x46190000, v194
	s_nop 1
	v_addc_co_u32_e32 v65, vcc, 0, v195, vcc
	v_add_co_u32_e32 v66, vcc, 0x47190000, v194
	s_nop 1
	v_addc_co_u32_e32 v67, vcc, 0, v195, vcc
	global_load_dwordx4 v[108:111], v[64:65], off
	global_load_dwordx4 v[96:99], v[66:67], off
	v_add_co_u32_e32 v64, vcc, 0x46192000, v194
	s_nop 1
	v_addc_co_u32_e32 v65, vcc, 0, v195, vcc
	v_add_co_u32_e32 v66, vcc, 0x47192000, v194
	s_nop 1
	v_addc_co_u32_e32 v67, vcc, 0, v195, vcc
	global_load_dwordx4 v[100:103], v[64:65], off
	global_load_dwordx4 v[104:107], v[66:67], off
	v_add_co_u32_e32 v64, vcc, 0x48198000, v192
	s_nop 1
	v_addc_co_u32_e32 v65, vcc, 0, v193, vcc
	v_add_co_u32_e32 v66, vcc, 0x4819a000, v192
	s_nop 1
	v_addc_co_u32_e32 v67, vcc, 0, v193, vcc
	global_load_dwordx4 v[112:115], v[64:65], off
	global_load_dwordx4 v[116:119], v[66:67], off
	v_add_co_u32_e32 v64, vcc, 0x4819c000, v192
	s_nop 1
	v_addc_co_u32_e32 v65, vcc, 0, v193, vcc
	v_add_co_u32_e32 v66, vcc, 0x4819e000, v192
	s_nop 1
	v_addc_co_u32_e32 v67, vcc, 0, v193, vcc
	global_load_dwordx4 v[120:123], v[64:65], off
	global_load_dwordx4 v[124:127], v[66:67], off

; #define LAS __attribute__((address_space(3)))
; __device__ __forceinline__ void gla_unit(LAS unsigned char* lds, const unsigned char* ws, const float* g_onorm, const int b, const int h, const int wv) {
;     ...
;         f32x16 O[2];
; #pragma unroll
;         for (int tt = 0; tt < 2; ++tt)
; #pragma unroll
;             for (int r = 0; r < 16; ++r) O[tt][r] = 0.f;
; #pragma unroll
;         for (int et = 0; et < 4; ++et)
; #pragma unroll
;             for (int s2 = 0; s2 < 2; ++s2) {
;                 const bf16x8 sb = pack8(S[et], s2);
; #pragma unroll
;                 for (int tt = 0; tt < 2; ++tt) {
;                     const bf16x8 aq = ld2x64(qb8 + 32 * tt * QS + (32 * et + 16 * s2) * 2);
;                     O[tt] = __builtin_amdgcn_mfma_f32_32x32x16_bf16(aq, sb, O[tt], 0, 0, 0);
;                 }
;             }
;         __syncthreads();
; #pragma unroll
;         for (int pr = 0; pr < 3; ++pr) {
;             const int st = (pr == 2) ? 1 : 0, tt = (pr == 0) ? 0 : 1;
; #pragma unroll
;             for (int s2 = 0; s2 < 2; ++s2) {
;                 const bf16x8 ax = *(const LAS bf16x8*)(frb + (pr * 2 + s2) * 1024);
;                 const LAS unsigned char* vp = vP + (32 * st + 16 * s2) * VS;
;                 const bf16x8 bv = tr8(vp, vp + 8 * VS);
;                 O[tt] = __builtin_amdgcn_mfma_f32_32x32x16_bf16(ax, bv, O[tt], 0, 0, 0);
;             }
;         }
;         __builtin_amdgcn_sched_barrier(0);
; #pragma unroll
;         for (int tt = 0; tt < 2; ++tt)
; #pragma unroll
;             for (int r = 0; r < 16; ++r) ob[(32 * tt + (r & 3) + 8 * (r >> 2)) * OS] = O[tt][r];
;         __builtin_amdgcn_sched_barrier(0);
; #pragma unroll
;         for (int et = 0; et < 4; ++et)
; #pragma unroll
;             for (int rg = 0; rg < 4; ++rg) { const f32x4 dl = *(const LAS f32x4*)&decb[32 * et + 8 * rg];
.LBB0_1703:
	v_add_u32_e32 v222, v203, v202
	ds_read2_b64 v[64:67], v222 offset1:2
	v_cvt_pk_bf16_f32 v68, v48, v49
	v_cvt_pk_bf16_f32 v69, v50, v51
	v_cvt_pk_bf16_f32 v70, v52, v53
	v_cvt_pk_bf16_f32 v71, v54, v55
	v_add_u32_e32 v223, 0x2000, v222
	ds_read2_b64 v[228:231], v222 offset0:4 offset1:6
	v_cvt_pk_bf16_f32 v232, v56, v57
	v_cvt_pk_bf16_f32 v233, v58, v59
	s_waitcnt lgkmcnt(1)
	v_mfma_f32_32x32x16_bf16 v[80:95], v[64:67], v[68:71], 0
	ds_read2_b64 v[64:67], v223 offset0:64 offset1:66
	v_cvt_pk_bf16_f32 v234, v60, v61
	v_cvt_pk_bf16_f32 v235, v62, v63
	s_waitcnt lgkmcnt(1)
	s_nop 0
	v_mfma_f32_32x32x16_bf16 v[80:95], v[228:231], v[232:235], v[80:95]
	ds_read2_b64 v[228:231], v223 offset0:68 offset1:70
	s_waitcnt lgkmcnt(1)
	v_mfma_f32_32x32x16_bf16 v[64:79], v[64:67], v[68:71], 0
	s_waitcnt lgkmcnt(0)
	v_mfma_f32_32x32x16_bf16 v[64:79], v[228:231], v[232:235], v[64:79]
	ds_read2_b64 v[228:231], v222 offset0:8 offset1:10
	v_cvt_pk_bf16_f32 v232, v16, v17
	v_cvt_pk_bf16_f32 v233, v18, v19
	v_cvt_pk_bf16_f32 v234, v20, v21
	v_cvt_pk_bf16_f32 v235, v22, v23
	s_waitcnt lgkmcnt(0)
	s_nop 0
	v_mfma_f32_32x32x16_bf16 v[80:95], v[228:231], v[232:235], v[80:95]
	ds_read2_b64 v[228:231], v223 offset0:72 offset1:74
	s_waitcnt lgkmcnt(0)
	v_mfma_f32_32x32x16_bf16 v[64:79], v[228:231], v[232:235], v[64:79]
	ds_read2_b64 v[228:231], v222 offset0:12 offset1:14
	v_cvt_pk_bf16_f32 v232, v24, v25
	v_cvt_pk_bf16_f32 v233, v26, v27
	v_cvt_pk_bf16_f32 v234, v28, v29
	v_cvt_pk_bf16_f32 v235, v30, v31
	s_waitcnt lgkmcnt(0)
	s_nop 0
	v_mfma_f32_32x32x16_bf16 v[80:95], v[228:231], v[232:235], v[80:95]
	ds_read2_b64 v[228:231], v223 offset0:76 offset1:78
	s_waitcnt lgkmcnt(0)
	v_mfma_f32_32x32x16_bf16 v[64:79], v[228:231], v[232:235], v[64:79]
	ds_read2_b64 v[228:231], v222 offset0:16 offset1:18
	v_cvt_pk_bf16_f32 v232, v32, v33
	v_cvt_pk_bf16_f32 v233, v34, v35
	v_cvt_pk_bf16_f32 v234, v36, v37
	v_cvt_pk_bf16_f32 v235, v38, v39
	s_waitcnt lgkmcnt(0)
	s_nop 0
	v_mfma_f32_32x32x16_bf16 v[80:95], v[228:231], v[232:235], v[80:95]
	ds_read2_b64 v[228:231], v223 offset0:80 offset1:82
	s_waitcnt lgkmcnt(0)
	v_mfma_f32_32x32x16_bf16 v[64:79], v[228:231], v[232:235], v[64:79]
	ds_read2_b64 v[228:231], v222 offset0:20 offset1:22
	v_cvt_pk_bf16_f32 v232, v40, v41
	v_cvt_pk_bf16_f32 v233, v42, v43
	v_cvt_pk_bf16_f32 v234, v44, v45
	v_cvt_pk_bf16_f32 v235, v46, v47
	s_waitcnt lgkmcnt(0)
	s_nop 0
	v_mfma_f32_32x32x16_bf16 v[80:95], v[228:231], v[232:235], v[80:95]
	ds_read2_b64 v[228:231], v223 offset0:84 offset1:86
	s_waitcnt lgkmcnt(0)
	v_mfma_f32_32x32x16_bf16 v[64:79], v[228:231], v[232:235], v[64:79]
	ds_read2_b64 v[228:231], v222 offset0:24 offset1:26
	v_cvt_pk_bf16_f32 v232, v0, v1
	v_cvt_pk_bf16_f32 v233, v2, v3
	v_cvt_pk_bf16_f32 v234, v4, v5
	v_cvt_pk_bf16_f32 v235, v6, v7
	s_waitcnt lgkmcnt(0)
	s_nop 0
	v_mfma_f32_32x32x16_bf16 v[80:95], v[228:231], v[232:235], v[80:95]
	ds_read2_b64 v[228:231], v223 offset0:88 offset1:90
	s_waitcnt lgkmcnt(0)
	v_mfma_f32_32x32x16_bf16 v[64:79], v[228:231], v[232:235], v[64:79]
	ds_read2_b64 v[228:231], v222 offset0:28 offset1:30
	v_cvt_pk_bf16_f32 v232, v8, v9
	v_cvt_pk_bf16_f32 v233, v10, v11
	v_cvt_pk_bf16_f32 v234, v12, v13
	v_cvt_pk_bf16_f32 v235, v14, v15
	s_waitcnt lgkmcnt(0)
	s_nop 0
	v_mfma_f32_32x32x16_bf16 v[80:95], v[228:231], v[232:235], v[80:95]
	ds_read2_b64 v[228:231], v223 offset0:92 offset1:94
	s_waitcnt lgkmcnt(0)
	s_barrier
	v_mfma_f32_32x32x16_bf16 v[64:79], v[228:231], v[232:235], v[64:79]
	ds_read_b128 v[228:231], v206
	ds_read_b64_tr_b16 v[232:233], v218
	ds_read_b64_tr_b16 v[234:235], v218 offset:4608
	ds_read_b128 v[236:239], v206 offset:1024
	ds_read_b64_tr_b16 v[240:241], v218 offset:9216
	ds_read_b64_tr_b16 v[242:243], v218 offset:13824
	s_waitcnt lgkmcnt(3)
	v_mfma_f32_32x32x16_bf16 v[80:95], v[228:231], v[232:235], v[80:95]
	s_waitcnt lgkmcnt(0)
	v_mfma_f32_32x32x16_bf16 v[80:95], v[236:239], v[240:243], v[80:95]
	ds_read_b128 v[228:231], v206 offset:2048
	ds_read_b128 v[236:239], v206 offset:3072
	s_waitcnt lgkmcnt(1)
	v_mfma_f32_32x32x16_bf16 v[64:79], v[228:231], v[232:235], v[64:79]
	s_waitcnt lgkmcnt(0)
	v_mfma_f32_32x32x16_bf16 v[64:79], v[236:239], v[240:243], v[64:79]
	ds_read_b128 v[228:231], v206 offset:4096
	ds_read_b64_tr_b16 v[232:233], v218 offset:18432
	ds_read_b64_tr_b16 v[234:235], v218 offset:23040
	ds_read_b128 v[236:239], v206 offset:5120
	ds_read_b64_tr_b16 v[240:241], v218 offset:27648
	ds_read_b64_tr_b16 v[242:243], v218 offset:32256
	s_waitcnt lgkmcnt(3)
	v_mfma_f32_32x32x16_bf16 v[64:79], v[228:231], v[232:235], v[64:79]
	s_waitcnt lgkmcnt(0)
	v_mfma_f32_32x32x16_bf16 v[64:79], v[236:239], v[240:243], v[64:79]
	ds_write_b32 v207, v80
	ds_write_b32 v207, v81 offset:1040
	ds_write_b32 v207, v82 offset:2080
	ds_write_b32 v207, v83 offset:3120
	ds_write_b32 v207, v84 offset:8320
	ds_write_b32 v207, v85 offset:9360
	ds_write_b32 v207, v86 offset:10400
	ds_write_b32 v207, v87 offset:11440
	ds_write_b32 v207, v88 offset:16640
	ds_write_b32 v207, v89 offset:17680
	ds_write_b32 v207, v90 offset:18720
	ds_write_b32 v207, v91 offset:19760
	ds_write_b32 v207, v92 offset:24960
	ds_write_b32 v207, v93 offset:26000
	ds_write_b32 v207, v94 offset:27040
	ds_write_b32 v207, v95 offset:28080
	ds_write_b32 v207, v64 offset:33280
	ds_write_b32 v207, v65 offset:34320
	ds_write_b32 v207, v66 offset:35360
	ds_write_b32 v207, v67 offset:36400
	ds_write_b32 v207, v68 offset:41600
	ds_write_b32 v207, v69 offset:42640
	ds_write_b32 v207, v70 offset:43680
	ds_write_b32 v207, v71 offset:44720
	ds_write_b32 v207, v72 offset:49920
	ds_write_b32 v207, v73 offset:50960
	ds_write_b32 v207, v74 offset:52000
	ds_write_b32 v207, v75 offset:53040
	ds_write_b32 v207, v76 offset:58240
	ds_write_b32 v207, v77 offset:59280
	ds_write_b32 v207, v78 offset:60320
	ds_write_b32 v207, v79 offset:61360
	ds_read_b128 v[64:67], v205 offset:96
	ds_read_b128 v[68:71], v205 offset:64
	ds_read_b128 v[72:75], v205 offset:32
	ds_read_b128 v[76:79], v205
	s_waitcnt vmcnt(11)
; #define LAS __attribute__((address_space(3)))
; __device__ __forceinline__ void gla_unit(LAS unsigned char* lds, const unsigned char* ws, const float* g_onorm, const int b, const int h, const int wv) {
;     ...
; #pragma unroll
;         for (int et = 0; et < 4; ++et)
; #pragma unroll
;             for (int rg = 0; rg < 4; ++rg) { const f32x4 dl = *(const LAS f32x4*)&decb[32 * et + 8 * rg];
; #pragma unroll
;                 for (int x = 0; x < 4; ++x) S[et][4 * rg + x] *= dl[x]; }
; #pragma unroll
;         for (int ks = 0; ks < 4; ++ks) {
;             const LAS unsigned char* vp = vN + 16 * ks * VS;
;             const bf16x8 bv = tr8(vp, vp + 4 * VS);
; #pragma unroll
;             for (int et = 0; et < 4; ++et) {
;                 const LAS unsigned char* kp = keN + 32 * et * 2 + 16 * ks * ES;
;                 const bf16x8 ak = tr8(kp, kp + 4 * ES);
;                 S[et] = __builtin_amdgcn_mfma_f32_32x32x16_bf16(ak, bv, S[et], 0, 0, 0);
;             }
;         }
	v_lshlrev_b32_e32 v246, 16, v176
	s_waitcnt lgkmcnt(3)
	v_pk_mul_f32 v[62:63], v[62:63], v[66:67]
	s_waitcnt lgkmcnt(2)
	v_pk_mul_f32 v[58:59], v[58:59], v[70:71]
	v_pk_mul_f32 v[60:61], v[60:61], v[64:65]
	s_waitcnt lgkmcnt(0)
	v_pk_mul_f32 v[50:51], v[50:51], v[78:79]
	v_pk_mul_f32 v[56:57], v[56:57], v[68:69]
	ds_read_b128 v[64:67], v205 offset:192
	ds_read_b128 v[68:71], v205 offset:224
	ds_read_b128 v[78:81], v205 offset:128
	ds_read_b128 v[82:85], v205 offset:160
	v_pk_mul_f32 v[54:55], v[54:55], v[74:75]
	v_pk_mul_f32 v[52:53], v[52:53], v[72:73]
	v_pk_mul_f32 v[48:49], v[48:49], v[76:77]
	s_waitcnt lgkmcnt(2)
	v_pk_mul_f32 v[30:31], v[30:31], v[70:71]
	v_pk_mul_f32 v[26:27], v[26:27], v[66:67]
	s_waitcnt lgkmcnt(0)
	v_pk_mul_f32 v[22:23], v[22:23], v[84:85]
	v_pk_mul_f32 v[18:19], v[18:19], v[80:81]
	v_pk_mul_f32 v[28:29], v[28:29], v[68:69]
	v_pk_mul_f32 v[24:25], v[24:25], v[64:65]
	v_pk_mul_f32 v[20:21], v[20:21], v[82:83]
	ds_read_b128 v[64:67], v205 offset:256
	ds_read_b128 v[68:71], v205 offset:288
	ds_read_b128 v[72:75], v205 offset:320
	ds_read_b128 v[80:83], v205 offset:352
	ds_read_b64_tr_b16 v[84:85], v219
	ds_read_b64_tr_b16 v[86:87], v219 offset:2304
	ds_read_b64_tr_b16 v[90:91], v220 offset:1280
	ds_read_b64_tr_b16 v[88:89], v220
	ds_read_b64_tr_b16 v[92:93], v220 offset:64
	ds_read_b64_tr_b16 v[228:229], v220 offset:128
	ds_read_b64_tr_b16 v[232:233], v220 offset:192
	ds_read_b64_tr_b16 v[94:95], v220 offset:1344
	ds_read_b64_tr_b16 v[230:231], v220 offset:1408
	ds_read_b64_tr_b16 v[234:235], v220 offset:1472
	ds_read_b64_tr_b16 v[236:237], v219 offset:9216
	ds_read_b64_tr_b16 v[238:239], v219 offset:11520
	s_waitcnt lgkmcnt(8)
	v_mfma_f32_32x32x16_bf16 v[48:63], v[88:91], v[84:87], v[48:63]
	v_mul_f32_e64 v16, v16, v78
	v_mul_f32_e64 v17, v17, v79
	v_mul_f32_e64 v42, v42, v74
	v_mul_f32_e64 v43, v43, v75
	v_mul_f32_e64 v38, v38, v70
	v_mul_f32_e64 v39, v39, v71
	v_pk_mul_f32 v[34:35], v[34:35], v[66:67]
	v_pk_mul_f32 v[44:45], v[44:45], v[80:81]
	v_pk_mul_f32 v[40:41], v[40:41], v[72:73]
	ds_read_b128 v[70:73], v205 offset:448
	ds_read_b128 v[74:77], v205 offset:480
	v_pk_mul_f32 v[36:37], v[36:37], v[68:69]
	ds_read_b128 v[66:69], v205 offset:384
	ds_read_b128 v[78:81], v205 offset:416
	v_pk_mul_f32 v[46:47], v[46:47], v[82:83]
	v_pk_mul_f32 v[32:33], v[32:33], v[64:65]
	s_waitcnt lgkmcnt(2)
	v_pk_mul_f32 v[14:15], v[14:15], v[76:77]
	v_pk_mul_f32 v[10:11], v[10:11], v[72:73]
	s_waitcnt lgkmcnt(0)
	v_pk_mul_f32 v[6:7], v[6:7], v[80:81]
	v_pk_mul_f32 v[2:3], v[2:3], v[68:69]
	v_pk_mul_f32 v[12:13], v[12:13], v[74:75]
	v_pk_mul_f32 v[8:9], v[8:9], v[70:71]
	v_pk_mul_f32 v[4:5], v[4:5], v[78:79]
	v_pk_mul_f32 v[0:1], v[0:1], v[66:67]
	v_mfma_f32_32x32x16_bf16 v[16:31], v[92:95], v[84:87], v[16:31]
	ds_read_b64_tr_b16 v[66:67], v220 offset:6400
	ds_read_b64_tr_b16 v[64:65], v220 offset:5120
	ds_read_b64_tr_b16 v[68:69], v220 offset:5184
	ds_read_b64_tr_b16 v[72:73], v220 offset:5248
	ds_read_b64_tr_b16 v[76:77], v220 offset:5312
	ds_read_b64_tr_b16 v[70:71], v220 offset:6464
	ds_read_b64_tr_b16 v[74:75], v220 offset:6528
	ds_read_b64_tr_b16 v[78:79], v220 offset:6592
	v_and_b32_e32 v247, 0xffff0000, v176
	v_mfma_f32_32x32x16_bf16 v[32:47], v[228:231], v[84:87], v[32:47]
	v_mfma_f32_32x32x16_bf16 v[0:15], v[232:235], v[84:87], v[0:15]
	s_waitcnt lgkmcnt(6)
	v_mfma_f32_32x32x16_bf16 v[48:63], v[64:67], v[236:239], v[48:63]
	s_waitcnt lgkmcnt(2)
	v_mfma_f32_32x32x16_bf16 v[16:31], v[68:71], v[236:239], v[16:31]
	s_waitcnt lgkmcnt(1)
	v_mfma_f32_32x32x16_bf16 v[32:47], v[72:75], v[236:239], v[32:47]
	s_waitcnt lgkmcnt(0)
	v_mfma_f32_32x32x16_bf16 v[0:15], v[76:79], v[236:239], v[0:15]
	ds_read_b64_tr_b16 v[64:65], v219 offset:18432
	ds_read_b64_tr_b16 v[66:67], v219 offset:20736
	ds_read_b64_tr_b16 v[70:71], v220 offset:11520
	ds_read_b64_tr_b16 v[68:69], v220 offset:10240
	ds_read_b64_tr_b16 v[72:73], v220 offset:10304
	ds_read_b64_tr_b16 v[76:77], v220 offset:10368
	ds_read_b64_tr_b16 v[80:81], v220 offset:10432
	ds_read_b64_tr_b16 v[74:75], v220 offset:11584
	ds_read_b64_tr_b16 v[78:79], v220 offset:11648
	ds_read_b64_tr_b16 v[82:83], v220 offset:11712
	ds_read_b64_tr_b16 v[84:85], v219 offset:27648
	ds_read_b64_tr_b16 v[86:87], v219 offset:29952
	s_waitcnt lgkmcnt(8)
	v_mfma_f32_32x32x16_bf16 v[48:63], v[68:71], v[64:67], v[48:63]
	ds_read_b64_tr_b16 v[68:69], v220 offset:16640
	s_waitcnt lgkmcnt(5)
	v_mfma_f32_32x32x16_bf16 v[16:31], v[72:75], v[64:67], v[16:31]
	s_waitcnt lgkmcnt(4)
	v_mfma_f32_32x32x16_bf16 v[32:47], v[76:79], v[64:67], v[32:47]
	s_waitcnt lgkmcnt(3)
	v_mfma_f32_32x32x16_bf16 v[0:15], v[80:83], v[64:67], v[0:15]
	ds_read_b64_tr_b16 v[66:67], v220 offset:15360
	ds_read_b64_tr_b16 v[70:71], v220 offset:15424
	ds_read_b64_tr_b16 v[74:75], v220 offset:15488
	ds_read_b64_tr_b16 v[78:79], v220 offset:15552
	ds_read_b64_tr_b16 v[72:73], v220 offset:16704
	ds_read_b64_tr_b16 v[76:77], v220 offset:16768
	ds_read_b64_tr_b16 v[80:81], v220 offset:16832
	s_waitcnt lgkmcnt(0)
	s_barrier
; #define LAS __attribute__((address_space(3)))
; __device__ __forceinline__ unsigned cvt_pk_bf16(float lo, float hi) { const bf16x2_t r = __builtin_convertvector((f32x2_t){lo, hi}, bf16x2_t); return __builtin_bit_cast(unsigned, r); }
; __device__ __forceinline__ float bf_lo(unsigned w) { return __uint_as_float(w << 16); }
; __device__ __forceinline__ float bf_hi(unsigned w) { return __uint_as_float(w & 0xffff0000u); }
; __device__ __forceinline__ void gla_unit(LAS unsigned char* lds, const unsigned char* ws, const float* g_onorm, const int b, const int h, const int wv) {
;     ...
;         {
;             const int t = tid >> 3, g8 = tid & 7;
;             float ov[32]; float ss = 0.f;
; #pragma unroll
;             for (int x = 0; x < 8; ++x) { const f32x4 v = *(const LAS f32x4*)&obuf[t * OS + 32 * g8 + 4 * x]; ov[4 * x] = v[0]; ov[4 * x + 1] = v[1]; ov[4 * x + 2] = v[2]; ov[4 * x + 3] = v[3];
;                 ss += v[0] * v[0] + v[1] * v[1] + v[2] * v[2] + v[3] * v[3]; }
;             ss += __builtin_bit_cast(float, __builtin_amdgcn_ds_swizzle(__builtin_bit_cast(int, ss), (1 << 10) | 0x1F)); ss += __builtin_bit_cast(float, __builtin_amdgcn_ds_swizzle(__builtin_bit_cast(int, ss), (2 << 10) | 0x1F));
;             ss += __builtin_bit_cast(float, __builtin_amdgcn_ds_swizzle(__builtin_bit_cast(int, ss), (4 << 10) | 0x1F));
;             const float rstd = __builtin_amdgcn_rsqf(ss * (1.0f / 256.0f) + EPSV);
;             bf16_t* mp = mix + (t0 + t) * DM + 1024 + h * 256 + 32 * g8;
; #pragma unroll
;             for (int x = 0; x < 4; ++x) {
;                 const u32x4 og = ogr[x];
;                 const f32x4 g0 = *(const LAS f32x4*)&gon[32 * g8 + 8 * x], g1 = *(const LAS f32x4*)&gon[32 * g8 + 8 * x + 4];
;                 const float gg2[8] = {g0[0], g0[1], g0[2], g0[3], g1[0], g1[1], g1[2], g1[3]};
;                 float res[8];
; #pragma unroll
;                 for (int y = 0; y < 4; ++y) { const float a0 = bf_lo(og[y]), a1 = bf_hi(og[y]);
;                     res[2 * y] = ov[8 * x + 2 * y] * rstd * gg2[2 * y] * a0;
;                     res[2 * y + 1] = ov[8 * x + 2 * y + 1] * rstd * gg2[2 * y + 1] * a1; }
;                 u32x4 wv4; wv4[0] = cvt_pk_bf16(res[0], res[1]); wv4[1] = cvt_pk_bf16(res[2], res[3]); wv4[2] = cvt_pk_bf16(res[4], res[5]); wv4[3] = cvt_pk_bf16(res[6], res[7]);
;                 *(u32x4*)(mp + 8 * x) = wv4;
	v_mfma_f32_32x32x16_bf16 v[48:63], v[66:69], v[84:87], v[48:63]
	ds_read_b128 v[64:67], v221
	ds_read_b128 v[88:91], v221 offset:16
	ds_read_b128 v[92:95], v221 offset:32
	ds_read_b128 v[228:231], v221 offset:48
	s_waitcnt lgkmcnt(3)
	v_mul_f32_e32 v68, v65, v65
	s_waitcnt lgkmcnt(2)
	v_mul_f32_e32 v69, v89, v89
	v_fmac_f32_e32 v68, v64, v64
	v_fmac_f32_e32 v69, v88, v88
	v_fmac_f32_e32 v68, v66, v66
	v_fmac_f32_e32 v69, v90, v90
	v_mfma_f32_32x32x16_bf16 v[16:31], v[70:73], v[84:87], v[16:31]
	v_fmac_f32_e32 v68, v67, v67
	v_fmac_f32_e32 v69, v91, v91
	s_waitcnt lgkmcnt(1)
	v_mov_b32_e32 v70, v93
	s_waitcnt lgkmcnt(0)
	v_mov_b32_e32 v71, v229
	v_add_f32_e32 v196, v68, v69
	v_mov_b32_e32 v68, v92
	v_mov_b32_e32 v69, v228
	v_pk_mul_f32 v[70:71], v[70:71], v[70:71]
	v_mov_b32_e32 v82, v95
	v_pk_fma_f32 v[68:69], v[68:69], v[68:69], v[70:71]
	v_mov_b32_e32 v70, v94
	v_mov_b32_e32 v71, v230
	v_pk_fma_f32 v[72:73], v[70:71], v[70:71], v[68:69]
	ds_read_b128 v[68:71], v221 offset:64
	ds_read_b128 v[232:235], v221 offset:80
	v_mov_b32_e32 v83, v231
	v_pk_fma_f32 v[72:73], v[82:83], v[82:83], v[72:73]
	ds_read_b128 v[236:239], v221 offset:96
	ds_read_b128 v[240:243], v221 offset:112
	v_add_f32_e32 v72, v196, v72
	s_waitcnt lgkmcnt(3)
	v_mov_b32_e32 v82, v69
	s_waitcnt lgkmcnt(2)
	v_mov_b32_e32 v83, v233
	v_add_f32_e32 v196, v72, v73
	v_mov_b32_e32 v72, v68
	v_mov_b32_e32 v73, v232
	v_pk_mul_f32 v[82:83], v[82:83], v[82:83]
	v_mfma_f32_32x32x16_bf16 v[32:47], v[74:77], v[84:87], v[32:47]
	v_fma_f32 v72, v72, v72, v82
	v_fma_f32 v73, v73, v73, v83
	v_mov_b32_e32 v82, v70
	v_mov_b32_e32 v83, v234
	v_fma_f32 v72, v82, v82, v72
	v_fma_f32 v73, v83, v83, v73
	v_mov_b32_e32 v82, v71
	v_mov_b32_e32 v83, v235
	v_pk_fma_f32 v[72:73], v[82:83], v[82:83], v[72:73]
	s_waitcnt lgkmcnt(1)
	v_mov_b32_e32 v82, v237
	v_add_f32_e32 v72, v196, v72
	s_waitcnt lgkmcnt(0)
	v_mov_b32_e32 v83, v241
	v_add_f32_e32 v196, v72, v73
	v_mov_b32_e32 v72, v236
	v_mov_b32_e32 v73, v240
	v_pk_mul_f32 v[82:83], v[82:83], v[82:83]
	v_mfma_f32_32x32x16_bf16 v[0:15], v[78:81], v[84:87], v[0:15]
	v_fma_f32 v72, v72, v72, v82
	v_fma_f32 v73, v73, v73, v83
	v_mov_b32_e32 v82, v238
	v_mov_b32_e32 v83, v242
	v_fma_f32 v72, v82, v82, v72
	v_fma_f32 v73, v83, v83, v73
	v_mov_b32_e32 v82, v239
	v_mov_b32_e32 v83, v243
	v_pk_fma_f32 v[72:73], v[82:83], v[82:83], v[72:73]
	s_nop 0
	v_add_f32_e32 v72, v196, v72
	v_add_f32_e32 v72, v72, v73
	ds_swizzle_b32 v73, v72 offset:swizzle(SWAP,1)
	v_lshl_add_u64 v[196:197], s[76:77], 0, v[188:189]
	s_waitcnt lgkmcnt(0)
	v_add_f32_e32 v72, v72, v73
	ds_swizzle_b32 v73, v72 offset:swizzle(SWAP,2)
	s_waitcnt lgkmcnt(0)
	v_add_f32_e32 v72, v72, v73
	ds_swizzle_b32 v73, v72 offset:swizzle(SWAP,4)
	s_waitcnt lgkmcnt(0)
	v_add_f32_e32 v72, v72, v73
	v_fmamk_f32 v72, v72, 0x3b800000, v181
	v_rsq_f32_e32 v244, v72
	ds_read_b128 v[72:75], v208
	ds_read_b128 v[76:79], v208 offset:16
	ds_read_b128 v[80:83], v208 offset:32
	ds_read_b128 v[84:87], v208 offset:48
	v_pk_mul_f32 v[64:65], v[64:65], v[244:245] op_sel_hi:[1,0]
	v_pk_mul_f32 v[66:67], v[66:67], v[244:245] op_sel_hi:[1,0]
	s_waitcnt lgkmcnt(3)
	v_pk_mul_f32 v[64:65], v[72:73], v[64:65]
	v_lshlrev_b32_e32 v72, 16, v177
	v_and_b32_e32 v73, 0xffff0000, v177
	v_pk_mul_f32 v[66:67], v[74:75], v[66:67]
	v_pk_mul_f32 v[74:75], v[88:89], v[244:245] op_sel_hi:[1,0]
	v_pk_mul_f32 v[66:67], v[66:67], v[72:73]
	v_lshlrev_b32_e32 v72, 16, v178
	v_and_b32_e32 v73, 0xffff0000, v178
	s_waitcnt lgkmcnt(2)
	v_pk_mul_f32 v[74:75], v[76:77], v[74:75]
	v_pk_mul_f32 v[76:77], v[90:91], v[244:245] op_sel_hi:[1,0]
	v_pk_mul_f32 v[72:73], v[74:75], v[72:73]
	v_lshlrev_b32_e32 v74, 16, v179
	v_and_b32_e32 v75, 0xffff0000, v179
	v_pk_mul_f32 v[76:77], v[78:79], v[76:77]
	v_pk_mul_f32 v[64:65], v[64:65], v[246:247]
	v_pk_mul_f32 v[74:75], v[76:77], v[74:75]
	v_add_co_u32_e32 v76, vcc, s33, v196
	v_cvt_pk_bf16_f32 v64, v64, v65
	v_cvt_pk_bf16_f32 v65, v66, v67
	v_cvt_pk_bf16_f32 v66, v72, v73
	v_cvt_pk_bf16_f32 v67, v74, v75
	v_addc_co_u32_e32 v77, vcc, 0, v197, vcc
	global_store_dwordx4 v[76:77], v[64:67], off offset:2048
	v_pk_mul_f32 v[72:73], v[94:95], v[244:245] op_sel_hi:[1,0]
	v_pk_mul_f32 v[74:75], v[228:229], v[244:245] op_sel_hi:[1,0]
	v_pk_mul_f32 v[66:67], v[92:93], v[244:245] op_sel_hi:[1,0]
	s_waitcnt vmcnt(9)
; #define LAS __attribute__((address_space(3)))
; __device__ __forceinline__ unsigned cvt_pk_bf16(float lo, float hi) { const bf16x2_t r = __builtin_convertvector((f32x2_t){lo, hi}, bf16x2_t); return __builtin_bit_cast(unsigned, r); }
; __device__ __forceinline__ float bf_lo(unsigned w) { return __uint_as_float(w << 16); }
; __device__ __forceinline__ float bf_hi(unsigned w) { return __uint_as_float(w & 0xffff0000u); }
; __device__ __forceinline__ void gla_unit(LAS unsigned char* lds, const unsigned char* ws, const float* g_onorm, const int b, const int h, const int wv) {
;     ...
;         __syncthreads();
; #pragma unroll
;         for (int i = 0; i < 2; ++i) { const int c = tid + 512 * i, row = c >> 4, cc = (c & 15) * 16;
;             *(LAS u32x4*)(lds + L_Q + row * QS + cc) = qr[par][i]; *(LAS u32x4*)(lds + L_K + row * QS + cc) = kr[par][i]; }
; #pragma unroll
;         for (int i = 0; i < 4; ++i) { const int c = tid + 512 * i; *(LAS u32x4*)(lds + L_V + (c >> 5) * VS + (c & 31) * 16) = vr[par][i]; }
;         if (tid < 32) {
;             const float L2E_ = 1.4426950408889634f;
;             *(LAS f32x4*)&dec[tid * 4] = (f32x4){__builtin_amdgcn_exp2f(dr[0] * L2E_), __builtin_amdgcn_exp2f(dr[1] * L2E_), __builtin_amdgcn_exp2f(dr[2] * L2E_), __builtin_amdgcn_exp2f(dr[3] * L2E_)};
;         }
;     ...
; #pragma unroll
;             for (int x = 0; x < 4; ++x) {
;                 const u32x4 og = ogr[x];
;                 const f32x4 g0 = *(const LAS f32x4*)&gon[32 * g8 + 8 * x], g1 = *(const LAS f32x4*)&gon[32 * g8 + 8 * x + 4];
;                 const float gg2[8] = {g0[0], g0[1], g0[2], g0[3], g1[0], g1[1], g1[2], g1[3]};
;                 float res[8];
; #pragma unroll
;                 for (int y = 0; y < 4; ++y) { const float a0 = bf_lo(og[y]), a1 = bf_hi(og[y]);
;                     res[2 * y] = ov[8 * x + 2 * y] * rstd * gg2[2 * y] * a0;
;                     res[2 * y + 1] = ov[8 * x + 2 * y + 1] * rstd * gg2[2 * y + 1] * a1; }
;                 u32x4 wv4; wv4[0] = cvt_pk_bf16(res[0], res[1]); wv4[1] = cvt_pk_bf16(res[2], res[3]); wv4[2] = cvt_pk_bf16(res[4], res[5]); wv4[3] = cvt_pk_bf16(res[6], res[7]);
;                 *(u32x4*)(mp + 8 * x) = wv4;
;             }
	v_lshlrev_b32_e32 v64, 16, v172
	v_and_b32_e32 v65, 0xffff0000, v172
	s_waitcnt lgkmcnt(1)
	v_pk_mul_f32 v[66:67], v[80:81], v[66:67]
	v_pk_mul_f32 v[72:73], v[82:83], v[72:73]
	v_pk_mul_f32 v[64:65], v[66:67], v[64:65]
	v_lshlrev_b32_e32 v66, 16, v173
	v_and_b32_e32 v67, 0xffff0000, v173
	v_pk_mul_f32 v[66:67], v[72:73], v[66:67]
	v_lshlrev_b32_e32 v72, 16, v174
	v_and_b32_e32 v73, 0xffff0000, v174
	s_waitcnt lgkmcnt(0)
	v_pk_mul_f32 v[74:75], v[84:85], v[74:75]
	v_pk_mul_f32 v[78:79], v[230:231], v[244:245] op_sel_hi:[1,0]
	v_pk_mul_f32 v[72:73], v[74:75], v[72:73]
	v_lshlrev_b32_e32 v74, 16, v175
	v_and_b32_e32 v75, 0xffff0000, v175
	v_pk_mul_f32 v[78:79], v[86:87], v[78:79]
	v_cvt_pk_bf16_f32 v64, v64, v65
	v_pk_mul_f32 v[74:75], v[78:79], v[74:75]
	v_cvt_pk_bf16_f32 v65, v66, v67
	v_cvt_pk_bf16_f32 v66, v72, v73
	v_cvt_pk_bf16_f32 v67, v74, v75
	global_store_dwordx4 v[76:77], v[64:67], off offset:2064
	ds_read_b128 v[64:67], v208 offset:64
	ds_read_b128 v[72:75], v208 offset:80
	v_pk_mul_f32 v[68:69], v[68:69], v[244:245] op_sel_hi:[1,0]
	v_pk_mul_f32 v[70:71], v[70:71], v[244:245] op_sel_hi:[1,0]
	v_lshlrev_b32_e32 v78, 16, v168
	s_waitcnt lgkmcnt(1)
	v_pk_mul_f32 v[64:65], v[64:65], v[68:69]
	v_lshlrev_b32_e32 v68, 16, v169
	v_and_b32_e32 v69, 0xffff0000, v169
	v_pk_mul_f32 v[66:67], v[66:67], v[70:71]
	v_pk_mul_f32 v[70:71], v[232:233], v[244:245] op_sel_hi:[1,0]
	v_pk_mul_f32 v[66:67], v[66:67], v[68:69]
	v_lshlrev_b32_e32 v68, 16, v170
	v_and_b32_e32 v69, 0xffff0000, v170
	s_waitcnt lgkmcnt(0)
	v_pk_mul_f32 v[70:71], v[72:73], v[70:71]
	v_pk_mul_f32 v[72:73], v[234:235], v[244:245] op_sel_hi:[1,0]
	v_and_b32_e32 v79, 0xffff0000, v168
	v_pk_mul_f32 v[68:69], v[70:71], v[68:69]
	v_lshlrev_b32_e32 v70, 16, v171
	v_and_b32_e32 v71, 0xffff0000, v171
	v_pk_mul_f32 v[72:73], v[74:75], v[72:73]
	v_pk_mul_f32 v[64:65], v[64:65], v[78:79]
	v_pk_mul_f32 v[70:71], v[72:73], v[70:71]
	v_cvt_pk_bf16_f32 v64, v64, v65
	v_cvt_pk_bf16_f32 v65, v66, v67
	v_cvt_pk_bf16_f32 v66, v68, v69
	v_cvt_pk_bf16_f32 v67, v70, v71
	global_store_dwordx4 v[76:77], v[64:67], off offset:2080
	ds_read_b128 v[64:67], v208 offset:96
	ds_read_b128 v[68:71], v208 offset:112
	v_pk_mul_f32 v[74:75], v[236:237], v[244:245] op_sel_hi:[1,0]
	v_lshlrev_b32_e32 v72, 16, v164
	v_and_b32_e32 v73, 0xffff0000, v164
	s_waitcnt lgkmcnt(1)
	v_pk_mul_f32 v[64:65], v[74:75], v[64:65]
	v_pk_mul_f32 v[74:75], v[238:239], v[244:245] op_sel_hi:[1,0]
	v_pk_mul_f32 v[64:65], v[64:65], v[72:73]
	v_lshlrev_b32_e32 v72, 16, v165
	v_and_b32_e32 v73, 0xffff0000, v165
	v_pk_mul_f32 v[66:67], v[74:75], v[66:67]
	v_pk_mul_f32 v[74:75], v[240:241], v[244:245] op_sel_hi:[1,0]
	v_pk_mul_f32 v[66:67], v[66:67], v[72:73]
	v_lshlrev_b32_e32 v72, 16, v166
	v_and_b32_e32 v73, 0xffff0000, v166
	s_waitcnt lgkmcnt(0)
	v_pk_mul_f32 v[68:69], v[74:75], v[68:69]
	v_pk_mul_f32 v[74:75], v[242:243], v[244:245] op_sel_hi:[1,0]
	v_pk_mul_f32 v[68:69], v[68:69], v[72:73]
	v_lshlrev_b32_e32 v72, 16, v167
	v_and_b32_e32 v73, 0xffff0000, v167
	v_pk_mul_f32 v[70:71], v[74:75], v[70:71]
	v_cvt_pk_bf16_f32 v64, v64, v65
	v_pk_mul_f32 v[70:71], v[70:71], v[72:73]
	v_cvt_pk_bf16_f32 v65, v66, v67
	v_cvt_pk_bf16_f32 v66, v68, v69
	v_cvt_pk_bf16_f32 v67, v70, v71
	global_store_dwordx4 v[76:77], v[64:67], off offset:2096
	s_barrier
	s_waitcnt vmcnt(20)
	ds_write_b128 v209, v[132:135]
	ds_write_b128 v209, v[136:139] offset:17408
	ds_write_b128 v210, v[140:143]
	ds_write_b128 v210, v[144:147] offset:17408
	ds_write_b128 v211, v[148:151]
	ds_write_b128 v212, v[152:155]
	ds_write_b128 v213, v[156:159]
	ds_write_b128 v214, v[160:163]
	s_and_saveexec_b64 s[42:43], s[0:1]
	s_cbranch_execz .LBB0_1705
	s_waitcnt vmcnt(12)
	v_mul_f32_e32 v64, 0x3fb8aa3b, v128
	v_mul_f32_e32 v65, 0x3fb8aa3b, v129
	v_mul_f32_e32 v66, 0x3fb8aa3b, v130
	v_mul_f32_e32 v67, 0x3fb8aa3b, v131
	v_exp_f32_e32 v64, v64
	v_exp_f32_e32 v65, v65
	v_exp_f32_e32 v66, v66
	v_exp_f32_e32 v67, v67
	ds_write_b128 v226, v[64:67]
